# attention: row sums by 4x4x4 bf16 MFMA instead of 32x32x16 ones-column; mixer-B loop reordered QK-first with the row-max chain in the MFMA gaps; K/V staging loads in late gaps
# speedup vs baseline: 1.0131x; 1.0131x over previous
; __device__ __forceinline__ float bflo(unsigned w) { return __uint_as_float(w << 16); }
; __device__ __forceinline__ float bfhi(unsigned w) { return __uint_as_float(w & 0xffff0000u); }
;     ...
;   for (int r = 0; r < 16; ++r) rli[r] = __builtin_amdgcn_rcpf(lacc[r]);
;     ...
;     asm volatile("s_waitcnt lgkmcnt(0)" ::: "memory");
;     float ss[16];
; #pragma unroll
;     for (int r = 0; r < 16; ++r) ss[r] = 0.f;
; #pragma unroll
;     for (int d0 = 0; d0 < 4; ++d0)
; #pragma unroll
;         for (int r = 0; r < 16; r += 2) { const unsigned w = stash[(d0 * 8 + (r >> 1)) * 64 + lane_];
;             const float x0 = bflo(w) - lam * (o[d0][r] * rli[r]), x1 = bfhi(w) - lam * (o[d0][r + 1] * rli[r + 1]);
;             o[d0][r] = x0; o[d0][r + 1] = x1; ss[r] += x0 * x0; ss[r + 1] += x1 * x1; }
.LBB0_259:
	s_nop 4
	v_add_f32_e32 v240, v240, v244
	v_add_f32_e32 v241, v241, v245
	v_add_f32_e32 v242, v242, v246
	v_add_f32_e32 v243, v243, v247
	v_and_b32_e32 v244, 3, v0
	v_cmp_eq_u32_e64 s[98:99], 1, v244
	s_nop 1
	v_cndmask_b32_e64 v240, v240, v241, s[98:99]
	v_cmp_eq_u32_e64 s[98:99], 2, v244
	s_nop 1
	v_cndmask_b32_e64 v240, v240, v242, s[98:99]
	v_cmp_eq_u32_e64 s[98:99], 3, v244
	s_nop 1
	v_cndmask_b32_e64 v240, v240, v243, s[98:99]
	v_mov_b32_e32 v245, v240
	s_nop 1
	v_permlane32_swap_b32_e32 v245, v240
	s_nop 1
	v_add_f32_e32 v240, v240, v245
	ds_write_b32 v166, v240
	v_add_u32_e32 v245, s6, v184
	s_waitcnt lgkmcnt(0)
	ds_read_b128 v[18:21], v245
	ds_read_b128 v[22:25], v245 offset:32
	ds_read_b128 v[26:29], v245 offset:64
	ds_read_b128 v[30:33], v245 offset:96
	s_waitcnt lgkmcnt(0)
	s_waitcnt lgkmcnt(0)
	s_nop 8
	v_rcp_f32_e32 v90, v18
	v_rcp_f32_e32 v91, v19
	ds_read2st64_b32 v[18:19], v165 offset1:1
	v_rcp_f32_e32 v92, v20
	v_rcp_f32_e32 v93, v21
	v_rcp_f32_e32 v94, v22
	v_rcp_f32_e32 v95, v23
	s_waitcnt lgkmcnt(0)
	v_lshlrev_b32_e32 v22, 16, v18
	v_mul_f32_e32 v23, v66, v90
	v_rcp_f32_e32 v96, v24
	v_rcp_f32_e32 v97, v25
	ds_read2st64_b32 v[20:21], v165 offset0:2 offset1:3
	ds_read2st64_b32 v[24:25], v165 offset0:4 offset1:5
	ds_read2st64_b32 v[88:89], v165 offset0:6 offset1:7
	v_fma_f32 v84, -v208, v23, v22
	v_and_b32_e32 v18, 0xffff0000, v18
	v_mul_f32_e32 v22, v67, v91
	v_fma_f32 v83, -v208, v22, v18
	v_lshlrev_b32_e32 v18, 16, v19
	v_mul_f32_e32 v22, v68, v92
	v_fma_f32 v68, -v208, v22, v18
	v_and_b32_e32 v18, 0xffff0000, v19
	v_mul_f32_e32 v19, v69, v93
	v_rcp_f32_e32 v98, v26
	v_fma_f32 v67, -v208, v19, v18
	s_waitcnt lgkmcnt(2)
	v_lshlrev_b32_e32 v18, 16, v20
	v_mul_f32_e32 v19, v70, v94
	v_rcp_f32_e32 v99, v27
	v_fma_f32 v66, -v208, v19, v18
	v_and_b32_e32 v18, 0xffff0000, v20
	v_mul_f32_e32 v19, v71, v95
	v_rcp_f32_e32 v100, v28
	v_rcp_f32_e32 v86, v32
	v_fma_f32 v32, -v208, v19, v18
	v_lshlrev_b32_e32 v18, 16, v21
	v_mul_f32_e32 v19, v72, v96
	v_rcp_f32_e32 v101, v29
	v_rcp_f32_e32 v102, v30
	v_fma_f32 v30, -v208, v19, v18
	v_and_b32_e32 v18, 0xffff0000, v21
	v_mul_f32_e32 v19, v73, v97
	v_fma_f32 v28, -v208, v19, v18
	s_waitcnt lgkmcnt(1)
	v_lshlrev_b32_e32 v18, 16, v24
	v_mul_f32_e32 v19, v74, v98
	v_rcp_f32_e32 v87, v31
	v_fma_f32 v26, -v208, v19, v18
	v_and_b32_e32 v18, 0xffff0000, v24
	v_mul_f32_e32 v19, v75, v99
	v_fma_f32 v24, -v208, v19, v18
	v_lshlrev_b32_e32 v18, 16, v25
	v_mul_f32_e32 v19, v76, v100
	v_rcp_f32_e32 v85, v33
	v_fma_f32 v23, -v208, v19, v18
	v_and_b32_e32 v18, 0xffff0000, v25
	v_mul_f32_e32 v19, v77, v101
	ds_read2st64_b32 v[74:75], v165 offset0:8 offset1:9
	v_fma_f32 v22, -v208, v19, v18
	s_waitcnt lgkmcnt(1)
	v_lshlrev_b32_e32 v18, 16, v88
	v_mul_f32_e32 v19, v78, v102
	v_fma_f32 v21, -v208, v19, v18
	v_and_b32_e32 v18, 0xffff0000, v88
	v_mul_f32_e32 v19, v79, v87
	v_fma_f32 v20, -v208, v19, v18
	v_lshlrev_b32_e32 v18, 16, v89
	v_mul_f32_e32 v19, v80, v86
	v_fma_f32 v19, -v208, v19, v18
	v_and_b32_e32 v18, 0xffff0000, v89
	v_mul_f32_e32 v25, v81, v85
	v_fma_f32 v18, -v208, v25, v18
	s_waitcnt lgkmcnt(0)
	v_lshlrev_b32_e32 v25, 16, v74
	v_mul_f32_e32 v27, v50, v90
	ds_read2st64_b32 v[76:77], v165 offset0:10 offset1:11
	ds_read2st64_b32 v[78:79], v165 offset0:12 offset1:13
	ds_read2st64_b32 v[80:81], v165 offset0:14 offset1:15
	v_fma_f32 v73, -v208, v27, v25
	v_and_b32_e32 v25, 0xffff0000, v74
	v_mul_f32_e32 v27, v51, v91
	v_fma_f32 v72, -v208, v27, v25
	v_lshlrev_b32_e32 v25, 16, v75
	v_mul_f32_e32 v27, v52, v92
	v_fma_f32 v71, -v208, v27, v25
	v_and_b32_e32 v25, 0xffff0000, v75
	v_mul_f32_e32 v27, v53, v93
	v_fma_f32 v70, -v208, v27, v25
	s_waitcnt lgkmcnt(2)
	v_lshlrev_b32_e32 v25, 16, v76
	v_mul_f32_e32 v27, v54, v94
	v_fma_f32 v69, -v208, v27, v25
	v_and_b32_e32 v25, 0xffff0000, v76
	v_mul_f32_e32 v27, v55, v95
	v_fma_f32 v55, -v208, v27, v25
	v_lshlrev_b32_e32 v25, 16, v77
	v_mul_f32_e32 v27, v56, v96
	v_fma_f32 v54, -v208, v27, v25
	v_and_b32_e32 v25, 0xffff0000, v77
	v_mul_f32_e32 v27, v57, v97
	v_fma_f32 v53, -v208, v27, v25
	s_waitcnt lgkmcnt(1)
	v_lshlrev_b32_e32 v25, 16, v78
	v_mul_f32_e32 v27, v58, v98
	v_fma_f32 v52, -v208, v27, v25
	v_and_b32_e32 v25, 0xffff0000, v78
	v_mul_f32_e32 v27, v59, v99
	v_fma_f32 v51, -v208, v27, v25
	v_lshlrev_b32_e32 v25, 16, v79
	v_mul_f32_e32 v27, v60, v100
	v_fma_f32 v50, -v208, v27, v25
	v_and_b32_e32 v25, 0xffff0000, v79
	v_mul_f32_e32 v27, v61, v101
	v_fma_f32 v33, -v208, v27, v25
	s_waitcnt lgkmcnt(0)
	v_lshlrev_b32_e32 v25, 16, v80
	v_mul_f32_e32 v27, v62, v102
	v_fma_f32 v31, -v208, v27, v25
	v_and_b32_e32 v25, 0xffff0000, v80
	v_mul_f32_e32 v27, v63, v87
	v_fma_f32 v29, -v208, v27, v25
	v_lshlrev_b32_e32 v25, 16, v81
	v_mul_f32_e32 v27, v64, v86
	v_fma_f32 v27, -v208, v27, v25
	v_and_b32_e32 v25, 0xffff0000, v81
	v_mul_f32_e32 v56, v65, v85
	v_fma_f32 v25, -v208, v56, v25
	ds_read2st64_b32 v[56:57], v165 offset0:16 offset1:17
	v_mul_f32_e32 v34, v34, v90
	ds_read2st64_b32 v[78:79], v165 offset0:18 offset1:19
	ds_read2st64_b32 v[80:81], v165 offset0:20 offset1:21
	ds_read2st64_b32 v[88:89], v165 offset0:22 offset1:23
	v_mul_f32_e32 v35, v35, v91
	v_mul_f32_e32 v2, v2, v90
	s_waitcnt lgkmcnt(3)
	v_lshlrev_b32_e32 v58, 16, v56
	v_fma_f32 v65, -v208, v34, v58
	v_and_b32_e32 v34, 0xffff0000, v56
	v_fma_f32 v62, -v208, v35, v34
	v_lshlrev_b32_e32 v34, 16, v57
	v_mul_f32_e32 v35, v36, v92
	v_fma_f32 v61, -v208, v35, v34
	v_and_b32_e32 v34, 0xffff0000, v57
	v_mul_f32_e32 v35, v37, v93
	v_fma_f32 v60, -v208, v35, v34
	s_waitcnt lgkmcnt(2)
; __device__ __forceinline__ float bflo(unsigned w) { return __uint_as_float(w << 16); }
; __device__ __forceinline__ float bfhi(unsigned w) { return __uint_as_float(w & 0xffff0000u); }
;     ...
;     for (int d0 = 0; d0 < 4; ++d0)
; #pragma unroll
;         for (int r = 0; r < 16; r += 2) { const unsigned w = stash[(d0 * 8 + (r >> 1)) * 64 + lane_];
;             const float x0 = bflo(w) - lam * (o[d0][r] * rli[r]), x1 = bfhi(w) - lam * (o[d0][r + 1] * rli[r + 1]);
;             o[d0][r] = x0; o[d0][r + 1] = x1; ss[r] += x0 * x0; ss[r + 1] += x1 * x1; }
; #pragma unroll
;     for (int r = 0; r < 16; ++r) { float s = ss[r]; s += __shfl_xor(s, 1); s += __shfl_xor(s, 2); s += __shfl_xor(s, 4); s += __shfl_xor(s, 8); s += __shfl_xor(s, 16);
;         ss[r] = (1.0f - LAM_INIT) * __builtin_amdgcn_rsqf(s * (1.0f / 128.0f) + EPS); }
	v_lshlrev_b32_e32 v34, 16, v78
	v_mul_f32_e32 v35, v38, v94
	v_fma_f32 v59, -v208, v35, v34
	v_and_b32_e32 v34, 0xffff0000, v78
	v_mul_f32_e32 v35, v39, v95
	v_fma_f32 v58, -v208, v35, v34
	v_lshlrev_b32_e32 v34, 16, v79
	v_mul_f32_e32 v35, v40, v96
	v_fma_f32 v57, -v208, v35, v34
	v_and_b32_e32 v34, 0xffff0000, v79
	v_mul_f32_e32 v35, v41, v97
	v_fma_f32 v56, -v208, v35, v34
	s_waitcnt lgkmcnt(1)
	v_lshlrev_b32_e32 v34, 16, v80
	v_mul_f32_e32 v35, v42, v98
	v_fma_f32 v41, -v208, v35, v34
	v_and_b32_e32 v34, 0xffff0000, v80
	v_mul_f32_e32 v35, v43, v99
	v_fma_f32 v40, -v208, v35, v34
	v_lshlrev_b32_e32 v34, 16, v81
	v_mul_f32_e32 v35, v44, v100
	v_fma_f32 v39, -v208, v35, v34
	v_and_b32_e32 v34, 0xffff0000, v81
	v_mul_f32_e32 v35, v45, v101
	v_fma_f32 v38, -v208, v35, v34
	s_waitcnt lgkmcnt(0)
	v_lshlrev_b32_e32 v34, 16, v88
	v_mul_f32_e32 v35, v46, v102
	v_fma_f32 v37, -v208, v35, v34
	v_and_b32_e32 v34, 0xffff0000, v88
	v_mul_f32_e32 v35, v47, v87
	v_fma_f32 v36, -v208, v35, v34
	v_lshlrev_b32_e32 v34, 16, v89
	v_mul_f32_e32 v35, v48, v86
	v_fma_f32 v35, -v208, v35, v34
	v_and_b32_e32 v34, 0xffff0000, v89
	v_mul_f32_e32 v42, v49, v85
	v_fma_f32 v34, -v208, v42, v34
	ds_read2st64_b32 v[42:43], v165 offset0:24 offset1:25
	ds_read2st64_b32 v[78:79], v165 offset0:26 offset1:27
	ds_read2st64_b32 v[80:81], v165 offset0:28 offset1:29
	ds_read2st64_b32 v[88:89], v165 offset0:30 offset1:31
	v_mul_f32_e32 v3, v3, v91
	v_mul_f32_e32 v103, v73, v73
	v_fmac_f32_e32 v103, v84, v84
	s_waitcnt lgkmcnt(3)
	v_lshlrev_b32_e32 v44, 16, v42
	v_fma_f32 v49, -v208, v2, v44
	v_and_b32_e32 v2, 0xffff0000, v42
	v_fma_f32 v90, -v208, v3, v2
	v_lshlrev_b32_e32 v2, 16, v43
	v_mul_f32_e32 v3, v4, v92
	v_fma_f32 v48, -v208, v3, v2
	v_and_b32_e32 v2, 0xffff0000, v43
	v_mul_f32_e32 v3, v5, v93
	v_fma_f32 v47, -v208, v3, v2
	s_waitcnt lgkmcnt(2)
	v_lshlrev_b32_e32 v2, 16, v78
	v_mul_f32_e32 v3, v6, v94
	v_fma_f32 v46, -v208, v3, v2
	v_and_b32_e32 v2, 0xffff0000, v78
	v_mul_f32_e32 v3, v7, v95
	v_fma_f32 v45, -v208, v3, v2
	v_lshlrev_b32_e32 v2, 16, v79
	v_mul_f32_e32 v3, v8, v96
	v_fma_f32 v44, -v208, v3, v2
	v_and_b32_e32 v2, 0xffff0000, v79
	v_mul_f32_e32 v3, v9, v97
	v_fma_f32 v43, -v208, v3, v2
	s_waitcnt lgkmcnt(1)
	v_lshlrev_b32_e32 v2, 16, v80
	v_mul_f32_e32 v3, v10, v98
	v_fma_f32 v42, -v208, v3, v2
	v_and_b32_e32 v2, 0xffff0000, v80
	v_mul_f32_e32 v3, v11, v99
	v_fma_f32 v10, -v208, v3, v2
	v_lshlrev_b32_e32 v2, 16, v81
	v_mul_f32_e32 v3, v12, v100
	v_fmac_f32_e32 v103, v65, v65
	v_fma_f32 v9, -v208, v3, v2
	v_and_b32_e32 v2, 0xffff0000, v81
	v_mul_f32_e32 v3, v13, v101
	v_fmac_f32_e32 v103, v49, v49
	v_fma_f32 v8, -v208, v3, v2
	s_waitcnt lgkmcnt(0)
	v_lshlrev_b32_e32 v2, 16, v88
	v_mul_f32_e32 v3, v14, v102
	v_fma_f32 v7, -v208, v3, v2
	ds_bpermute_b32 v3, v1, v103
	v_and_b32_e32 v2, 0xffff0000, v88
	v_mul_f32_e32 v4, v15, v87
	v_fma_f32 v6, -v208, v4, v2
	v_mul_f32_e32 v104, v72, v72
	s_waitcnt lgkmcnt(0)
	v_add_f32_e32 v2, v103, v3
	ds_bpermute_b32 v3, v203, v2
	v_fmac_f32_e32 v104, v83, v83
	v_fmac_f32_e32 v104, v62, v62
	v_fmac_f32_e32 v104, v90, v90
	ds_bpermute_b32 v12, v1, v104
	s_waitcnt lgkmcnt(1)
	v_add_f32_e32 v2, v2, v3
	ds_bpermute_b32 v3, v204, v2
	v_mul_f32_e32 v105, v71, v71
	v_fmac_f32_e32 v105, v68, v68
	v_lshlrev_b32_e32 v4, 16, v89
	v_mul_f32_e32 v5, v16, v86
	v_fmac_f32_e32 v105, v61, v61
	v_fma_f32 v5, -v208, v5, v4
	v_and_b32_e32 v4, 0xffff0000, v89
	v_mul_f32_e32 v11, v17, v85
	v_fmac_f32_e32 v105, v48, v48
	v_fma_f32 v4, -v208, v11, v4
	s_waitcnt lgkmcnt(0)
	v_add_f32_e32 v2, v2, v3
	v_add_f32_e32 v11, v104, v12
	ds_bpermute_b32 v3, v205, v2
	ds_bpermute_b32 v12, v203, v11
	ds_bpermute_b32 v13, v1, v105
	v_mul_f32_e32 v106, v70, v70
	v_fmac_f32_e32 v106, v67, v67
	s_waitcnt lgkmcnt(2)
	v_add_f32_e32 v2, v2, v3
	s_waitcnt lgkmcnt(1)
	v_add_f32_e32 v11, v11, v12
	s_waitcnt lgkmcnt(0)
	v_add_f32_e32 v13, v105, v13
	ds_bpermute_b32 v3, v206, v2
	ds_bpermute_b32 v12, v204, v11
	ds_bpermute_b32 v14, v203, v13
	v_fmac_f32_e32 v106, v60, v60
	v_fmac_f32_e32 v106, v47, v47
	s_waitcnt lgkmcnt(2)
	v_add_f32_e32 v2, v2, v3
	s_waitcnt lgkmcnt(1)
	v_add_f32_e32 v3, v11, v12
	s_waitcnt lgkmcnt(0)
	v_add_f32_e32 v12, v13, v14
	ds_bpermute_b32 v11, v205, v3
	ds_bpermute_b32 v13, v204, v12
	ds_bpermute_b32 v14, v1, v106
	v_fmamk_f32 v2, v2, 0x3c000000, v209
	v_rsq_f32_e32 v2, v2
	s_waitcnt lgkmcnt(2)
	v_add_f32_e32 v3, v3, v11
	s_waitcnt lgkmcnt(1)
	v_add_f32_e32 v12, v12, v13
	s_waitcnt lgkmcnt(0)
	v_add_f32_e32 v14, v106, v14
	ds_bpermute_b32 v11, v206, v3
	ds_bpermute_b32 v13, v205, v12
	ds_bpermute_b32 v15, v203, v14
	v_mul_f32_e32 v16, 0x3f4ccccd, v2
	v_mul_f32_e32 v107, v69, v69
	s_waitcnt lgkmcnt(2)
	v_add_f32_e32 v2, v3, v11
	s_waitcnt lgkmcnt(1)
	v_add_f32_e32 v3, v12, v13
	s_waitcnt lgkmcnt(0)
	v_add_f32_e32 v12, v14, v15
	ds_bpermute_b32 v11, v206, v3
	ds_bpermute_b32 v13, v204, v12
	v_fmac_f32_e32 v107, v66, v66
	v_fmac_f32_e32 v107, v59, v59
	v_fmac_f32_e32 v107, v46, v46
	s_waitcnt lgkmcnt(1)
	v_add_f32_e32 v3, v3, v11
	ds_bpermute_b32 v11, v1, v107
	s_waitcnt lgkmcnt(1)
	v_add_f32_e32 v12, v12, v13
	ds_bpermute_b32 v13, v205, v12
	v_fmamk_f32 v2, v2, 0x3c000000, v209
	v_rsq_f32_e32 v2, v2
	s_waitcnt lgkmcnt(1)
	v_add_f32_e32 v11, v107, v11
	ds_bpermute_b32 v14, v203, v11
	s_waitcnt lgkmcnt(1)
	v_add_f32_e32 v12, v12, v13
	v_fmamk_f32 v3, v3, 0x3c000000, v209
	ds_bpermute_b32 v13, v206, v12
	v_mul_f32_e32 v108, v55, v55
	v_rsq_f32_e32 v3, v3
	v_fmac_f32_e32 v108, v32, v32
	v_fmac_f32_e32 v108, v58, v58
	v_fmac_f32_e32 v108, v45, v45
	v_mul_f32_e32 v17, 0x3f4ccccd, v2
	s_waitcnt lgkmcnt(1)
;     ...
;     for (int r = 0; r < 16; ++r) { float s = ss[r]; s += __shfl_xor(s, 1); s += __shfl_xor(s, 2); s += __shfl_xor(s, 4); s += __shfl_xor(s, 8); s += __shfl_xor(s, 16);
;         ss[r] = (1.0f - LAM_INIT) * __builtin_amdgcn_rsqf(s * (1.0f / 128.0f) + EPS); }
;     const float* sg = a->in[9]; float g4[4];
; #pragma unroll
;     for (int d0 = 0; d0 < 4; ++d0) g4[d0] = sg[d0 * 32 + r32];
	v_add_f32_e32 v2, v11, v14
	v_mul_f32_e32 v78, 0x3f4ccccd, v3
	ds_bpermute_b32 v3, v204, v2
	s_waitcnt lgkmcnt(1)
	v_add_f32_e32 v11, v12, v13
	ds_bpermute_b32 v12, v1, v108
	v_mul_f32_e32 v109, v54, v54
	v_fmac_f32_e32 v109, v30, v30
	v_fmac_f32_e32 v109, v57, v57
	v_fmac_f32_e32 v109, v44, v44
	s_waitcnt lgkmcnt(1)
	v_add_f32_e32 v2, v2, v3
	s_waitcnt lgkmcnt(0)
	v_add_f32_e32 v12, v108, v12
	ds_bpermute_b32 v3, v205, v2
	ds_bpermute_b32 v13, v203, v12
	ds_bpermute_b32 v14, v1, v109
	v_mul_f32_e32 v110, v53, v53
	v_fmac_f32_e32 v110, v28, v28
	s_waitcnt lgkmcnt(2)
	v_add_f32_e32 v2, v2, v3
	s_waitcnt lgkmcnt(1)
	v_add_f32_e32 v12, v12, v13
	s_waitcnt lgkmcnt(0)
	v_add_f32_e32 v14, v109, v14
	ds_bpermute_b32 v3, v206, v2
	ds_bpermute_b32 v13, v204, v12
	ds_bpermute_b32 v15, v203, v14
	v_fmac_f32_e32 v110, v56, v56
	v_fmac_f32_e32 v110, v43, v43
	s_waitcnt lgkmcnt(2)
	v_add_f32_e32 v2, v2, v3
	s_waitcnt lgkmcnt(1)
	v_add_f32_e32 v3, v12, v13
	s_waitcnt lgkmcnt(0)
	v_add_f32_e32 v13, v14, v15
	ds_bpermute_b32 v12, v205, v3
	ds_bpermute_b32 v14, v204, v13
	ds_bpermute_b32 v15, v1, v110
	v_fmamk_f32 v2, v2, 0x3c000000, v209
	v_rsq_f32_e32 v2, v2
	s_waitcnt lgkmcnt(2)
	v_add_f32_e32 v3, v3, v12
	s_waitcnt lgkmcnt(1)
	v_add_f32_e32 v13, v13, v14
	s_waitcnt lgkmcnt(0)
	v_add_f32_e32 v15, v110, v15
	ds_bpermute_b32 v12, v206, v3
	ds_bpermute_b32 v14, v205, v13
	ds_bpermute_b32 v79, v203, v15
	v_mul_f32_e32 v111, v52, v52
	v_fmac_f32_e32 v111, v26, v26
	v_fmac_f32_e32 v111, v41, v41
	v_fmac_f32_e32 v111, v42, v42
	v_mul_f32_e32 v80, 0x3f4ccccd, v2
	s_waitcnt lgkmcnt(2)
	v_add_f32_e32 v2, v3, v12
	s_waitcnt lgkmcnt(1)
	v_add_f32_e32 v3, v13, v14
	s_waitcnt lgkmcnt(0)
	v_add_f32_e32 v13, v15, v79
	ds_bpermute_b32 v12, v206, v3
	ds_bpermute_b32 v14, v204, v13
	ds_bpermute_b32 v15, v1, v111
	v_fmamk_f32 v2, v2, 0x3c000000, v209
	v_mul_f32_e32 v112, v51, v51
	s_waitcnt lgkmcnt(2)
	v_add_f32_e32 v3, v3, v12
	s_waitcnt lgkmcnt(1)
	v_add_f32_e32 v12, v13, v14
	s_waitcnt lgkmcnt(0)
	v_add_f32_e32 v14, v111, v15
	ds_bpermute_b32 v13, v205, v12
	ds_bpermute_b32 v15, v203, v14
	v_rsq_f32_e32 v2, v2
	v_fmac_f32_e32 v112, v24, v24
	v_fmac_f32_e32 v112, v40, v40
	s_waitcnt lgkmcnt(1)
	v_add_f32_e32 v12, v12, v13
	s_waitcnt lgkmcnt(0)
	v_add_f32_e32 v14, v14, v15
	v_fmamk_f32 v3, v3, 0x3c000000, v209
	ds_bpermute_b32 v13, v206, v12
	ds_bpermute_b32 v15, v204, v14
	v_fmac_f32_e32 v112, v10, v10
	v_rsq_f32_e32 v3, v3
	v_mul_f32_e32 v79, 0x3f4ccccd, v2
	ds_bpermute_b32 v2, v1, v112
	v_mul_f32_e32 v77, v50, v50
	v_mul_f32_e32 v81, 0x3f4ccccd, v3
	s_waitcnt lgkmcnt(2)
	v_add_f32_e32 v3, v12, v13
	s_waitcnt lgkmcnt(1)
	v_add_f32_e32 v12, v14, v15
	ds_bpermute_b32 v13, v205, v12
	s_waitcnt lgkmcnt(1)
	v_add_f32_e32 v2, v112, v2
	v_fmac_f32_e32 v77, v23, v23
	ds_bpermute_b32 v14, v203, v2
	v_fmac_f32_e32 v77, v39, v39
	v_fmac_f32_e32 v77, v9, v9
	v_fmamk_f32 v3, v3, 0x3c000000, v209
	s_waitcnt lgkmcnt(1)
	v_add_f32_e32 v12, v12, v13
	ds_bpermute_b32 v13, v1, v77
	v_rsq_f32_e32 v3, v3
	s_waitcnt lgkmcnt(1)
	v_add_f32_e32 v2, v2, v14
	ds_bpermute_b32 v14, v204, v2
	ds_bpermute_b32 v15, v206, v12
	v_mul_f32_e32 v85, 0x3f4ccccd, v3
	s_waitcnt lgkmcnt(2)
	v_add_f32_e32 v3, v77, v13
	ds_bpermute_b32 v13, v203, v3
	s_waitcnt lgkmcnt(2)
	v_add_f32_e32 v2, v2, v14
	ds_bpermute_b32 v14, v205, v2
	v_mul_f32_e32 v76, v33, v33
	v_fmac_f32_e32 v76, v22, v22
	s_waitcnt lgkmcnt(1)
	v_add_f32_e32 v3, v3, v13
	v_fmac_f32_e32 v76, v38, v38
	ds_bpermute_b32 v13, v204, v3
	v_fmac_f32_e32 v76, v8, v8
	v_add_f32_e32 v12, v12, v15
	v_fmamk_f32 v12, v12, 0x3c000000, v209
	s_waitcnt lgkmcnt(1)
	v_add_f32_e32 v2, v2, v14
	ds_bpermute_b32 v14, v1, v76
	v_rsq_f32_e32 v12, v12
	s_waitcnt lgkmcnt(1)
	v_add_f32_e32 v3, v3, v13
	ds_bpermute_b32 v13, v205, v3
	v_mul_f32_e32 v75, v31, v31
	v_mul_f32_e32 v77, 0x3f4ccccd, v12
	s_waitcnt lgkmcnt(1)
	v_add_f32_e32 v12, v76, v14
	ds_bpermute_b32 v14, v203, v12
	s_waitcnt lgkmcnt(1)
	v_add_f32_e32 v3, v3, v13
	ds_bpermute_b32 v13, v206, v3
	v_fmac_f32_e32 v75, v21, v21
	ds_bpermute_b32 v15, v206, v2
	s_waitcnt lgkmcnt(2)
	v_add_f32_e32 v12, v12, v14
	ds_bpermute_b32 v14, v204, v12
	v_fmac_f32_e32 v75, v37, v37
	v_fmac_f32_e32 v75, v7, v7
	s_waitcnt lgkmcnt(2)
	v_add_f32_e32 v3, v3, v13
	ds_bpermute_b32 v13, v1, v75
	s_load_dwordx2 s[4:5], s[26:27], 0x48
	s_waitcnt lgkmcnt(0)
	v_add_f32_e32 v2, v2, v15
	v_add_f32_e32 v12, v12, v14
	v_fmamk_f32 v2, v2, 0x3c000000, v209
	ds_bpermute_b32 v14, v205, v12
	v_and_b32_e32 v82, 31, v164
	v_rsq_f32_e32 v2, v2
	v_lshlrev_b32_e32 v15, 2, v82
	v_add_f32_e32 v13, v75, v13
	v_fmamk_f32 v3, v3, 0x3c000000, v209
	global_load_dword v76, v15, s[4:5]
	global_load_dword v88, v15, s[4:5] offset:256
	ds_bpermute_b32 v75, v203, v13
	v_rsq_f32_e32 v3, v3
	v_mul_f32_e32 v86, 0x3f4ccccd, v2
	s_waitcnt lgkmcnt(1)
	v_add_f32_e32 v2, v12, v14
	ds_bpermute_b32 v12, v206, v2
	v_mul_f32_e32 v74, v29, v29
	v_fmac_f32_e32 v74, v20, v20
	v_mul_f32_e32 v87, 0x3f4ccccd, v3
	s_waitcnt lgkmcnt(1)
	v_add_f32_e32 v3, v13, v75
	global_load_dword v75, v15, s[4:5] offset:128
	v_fmac_f32_e32 v74, v36, v36
	v_fmac_f32_e32 v74, v6, v6
	s_waitcnt lgkmcnt(0)
	v_add_f32_e32 v2, v2, v12
	ds_bpermute_b32 v12, v1, v74
	ds_bpermute_b32 v13, v204, v3
	v_fmamk_f32 v2, v2, 0x3c000000, v209
	v_mul_f32_e32 v64, v25, v25
	v_rsq_f32_e32 v2, v2
	s_waitcnt lgkmcnt(1)
	v_add_f32_e32 v12, v74, v12
	global_load_dword v74, v15, s[4:5] offset:384
	s_waitcnt lgkmcnt(0)
	v_add_f32_e32 v3, v3, v13
	ds_bpermute_b32 v13, v205, v3
	ds_bpermute_b32 v14, v203, v12
	v_mul_f32_e32 v63, v27, v27
	v_fmac_f32_e32 v64, v18, v18
	v_fmac_f32_e32 v63, v19, v19
	s_waitcnt lgkmcnt(1)
; __device__ __forceinline__ int crow(int r, int hi) { return (r & 3) + 8 * (r >> 2) + 4 * hi; }
; __device__ __forceinline__ unsigned f2bf(float f) { unsigned u = __builtin_bit_cast(unsigned, f); return (u + 0x7fffu + ((u >> 16) & 1u)) >> 16; }
;     ...
;     for (int r = 0; r < 16; ++r) { float s = ss[r]; s += __shfl_xor(s, 1); s += __shfl_xor(s, 2); s += __shfl_xor(s, 4); s += __shfl_xor(s, 8); s += __shfl_xor(s, 16);
;         ss[r] = (1.0f - LAM_INIT) * __builtin_amdgcn_rsqf(s * (1.0f / 128.0f) + EPS); }
;     const float* sg = a->in[9]; float g4[4];
; #pragma unroll
;     for (int d0 = 0; d0 < 4; ++d0) g4[d0] = sg[d0 * 32 + r32];
;     att::bf16* Ow = Obase + ((size_t)b * SEQ + (size_t)qb * 256 + wave_ * 32) * 2048 + 1024 + h * 128;
; #pragma unroll
;     for (int r = 0; r < 16; ++r) { const int orow = crow(r, hi);
; #pragma unroll
;         for (int d0 = 0; d0 < 4; ++d0) Ow[(size_t)orow * 2048 + d0 * 32 + r32] = (att::bf16)f2bf(o[d0][r] * ss[r] * g4[d0]); }
	v_add_f32_e32 v3, v3, v13
	ds_bpermute_b32 v13, v206, v3
	v_fmac_f32_e32 v64, v34, v34
	v_fmac_f32_e32 v63, v35, v35
	v_fmac_f32_e32 v64, v4, v4
	v_fmac_f32_e32 v63, v5, v5
	s_waitcnt lgkmcnt(1)
	v_add_f32_e32 v12, v12, v14
	v_mul_f32_e32 v89, 0x3f4ccccd, v2
	s_waitcnt lgkmcnt(0)
	v_add_f32_e32 v2, v3, v13
	ds_bpermute_b32 v3, v1, v64
	ds_bpermute_b32 v14, v204, v12
	ds_bpermute_b32 v15, v1, v63
	s_lshl_b32 s4, s89, 5
	s_ashr_i32 s5, s4, 31
	s_waitcnt lgkmcnt(2)
	v_add_f32_e32 v3, v64, v3
	s_waitcnt lgkmcnt(1)
	v_add_f32_e32 v12, v12, v14
	s_waitcnt lgkmcnt(0)
	v_add_f32_e32 v13, v63, v15
	ds_bpermute_b32 v63, v203, v3
	ds_bpermute_b32 v15, v205, v12
	ds_bpermute_b32 v14, v203, v13
	s_add_u32 s4, s4, s88
	s_addc_u32 s5, s5, 0
	s_waitcnt lgkmcnt(2)
	v_add_f32_e32 v3, v3, v63
	s_waitcnt lgkmcnt(1)
	v_add_f32_e32 v12, v12, v15
	ds_bpermute_b32 v15, v204, v3
	s_waitcnt lgkmcnt(1)
	v_add_f32_e32 v13, v13, v14
	ds_bpermute_b32 v14, v204, v13
	ds_bpermute_b32 v63, v206, v12
	v_fmamk_f32 v2, v2, 0x3c000000, v209
	s_waitcnt lgkmcnt(2)
	v_add_f32_e32 v3, v3, v15
	ds_bpermute_b32 v15, v205, v3
	s_waitcnt lgkmcnt(2)
	v_add_f32_e32 v13, v13, v14
	ds_bpermute_b32 v14, v205, v13
	s_waitcnt lgkmcnt(2)
	v_add_f32_e32 v12, v12, v63
	v_fmamk_f32 v12, v12, 0x3c000000, v209
	s_waitcnt lgkmcnt(1)
	v_add_f32_e32 v3, v3, v15
	ds_bpermute_b32 v15, v206, v3
	s_waitcnt lgkmcnt(1)
	v_add_f32_e32 v13, v13, v14
	ds_bpermute_b32 v14, v206, v13
	v_rsq_f32_e32 v12, v12
	s_lshl_b64 s[4:5], s[4:5], 12
	s_waitcnt lgkmcnt(1)
	v_add_f32_e32 v3, v3, v15
	v_fmamk_f32 v3, v3, 0x3c000000, v209
	v_rsq_f32_e32 v2, v2
	v_rsq_f32_e32 v3, v3
	s_add_u32 s4, s44, s4
	s_addc_u32 s5, s45, s5
	s_add_u32 s4, s4, s46
	s_waitcnt lgkmcnt(0)
	v_add_f32_e32 v13, v13, v14
	v_mul_f32_e32 v64, 0x3f4ccccd, v12
	s_addc_u32 s5, s5, s47
	v_lshlrev_b32_e32 v184, 1, v82
	v_lshlrev_b32_e32 v12, 9, v164
	v_mul_f32_e32 v14, v84, v16
	v_mul_f32_e32 v63, 0x3f4ccccd, v2
	v_mul_f32_e32 v92, 0x3f4ccccd, v3
	v_lshl_add_u64 v[2:3], s[4:5], 0, v[184:185]
	v_and_b32_e32 v184, 0x4000, v12
	s_waitcnt vmcnt(3)
	v_mul_f32_e32 v14, v14, v76
	v_lshl_add_u64 v[2:3], v[2:3], 0, v[184:185]
	v_bfe_u32 v15, v14, 16, 1
	v_fmamk_f32 v13, v13, 0x3c000000, v209
	v_add3_u32 v82, v14, v15, s61
	v_add_co_u32_e32 v14, vcc, s62, v2
	v_rsq_f32_e32 v13, v13
	s_nop 0
	v_addc_co_u32_e32 v15, vcc, 0, v3, vcc
	global_store_short_d16_hi v[14:15], v82, off offset:2048
	v_mul_f32_e32 v14, v73, v16
	s_waitcnt vmcnt(2)
	v_mul_f32_e32 v14, v14, v75
	v_bfe_u32 v15, v14, 16, 1
	v_mul_f32_e32 v91, 0x3f4ccccd, v13
	v_lshl_add_u64 v[12:13], v[2:3], 0, s[42:43]
	v_add3_u32 v14, v14, v15, s61
	global_store_short_d16_hi v[12:13], v14, off offset:64
	v_mul_f32_e32 v14, v65, v16
	v_mul_f32_e32 v14, v14, v88
	v_bfe_u32 v15, v14, 16, 1
	v_add3_u32 v14, v14, v15, s61
	global_store_short_d16_hi v[12:13], v14, off offset:128
	v_mul_f32_e32 v14, v49, v16
	s_waitcnt vmcnt(3)
	v_mul_f32_e32 v14, v14, v74
	v_bfe_u32 v15, v14, 16, 1
	v_add3_u32 v14, v14, v15, s61
	global_store_short_d16_hi v[12:13], v14, off offset:192
	v_mul_f32_e32 v12, v83, v17
	v_mul_f32_e32 v12, v12, v76
	v_bfe_u32 v13, v12, 16, 1
	v_add3_u32 v14, v12, v13, s61
	v_add_co_u32_e32 v12, vcc, s63, v2
	v_fmamk_f32 v11, v11, 0x3c000000, v209
	s_nop 0
	v_addc_co_u32_e32 v13, vcc, 0, v3, vcc
	global_store_short_d16_hi v[12:13], v14, off offset:2048
	v_mul_f32_e32 v14, v72, v17
	v_mul_f32_e32 v14, v14, v75
	v_bfe_u32 v15, v14, 16, 1
	v_add3_u32 v14, v14, v15, s61
	global_store_short_d16_hi v[12:13], v14, off offset:2112
	v_mul_f32_e32 v14, v62, v17
	v_mul_f32_e32 v14, v14, v88
	v_bfe_u32 v15, v14, 16, 1
	v_add3_u32 v14, v14, v15, s61
	global_store_short_d16_hi v[12:13], v14, off offset:2176
	v_mul_f32_e32 v14, v90, v17
	v_mul_f32_e32 v14, v14, v74
	v_bfe_u32 v15, v14, 16, 1
	v_add3_u32 v14, v14, v15, s61
	global_store_short_d16_hi v[12:13], v14, off offset:2240
	v_mul_f32_e32 v12, v68, v78
	v_mul_f32_e32 v12, v12, v76
	v_bfe_u32 v13, v12, 16, 1
	v_add3_u32 v14, v12, v13, s61
	v_add_co_u32_e32 v12, vcc, s64, v2
	v_rsq_f32_e32 v11, v11
	s_nop 0
	v_addc_co_u32_e32 v13, vcc, 0, v3, vcc
	global_store_short_d16_hi v[12:13], v14, off offset:2048
	v_mul_f32_e32 v14, v71, v78
	v_mul_f32_e32 v14, v14, v75
	v_bfe_u32 v15, v14, 16, 1
	v_add3_u32 v14, v14, v15, s61
	global_store_short_d16_hi v[12:13], v14, off offset:2112
	v_mul_f32_e32 v14, v61, v78
	v_mul_f32_e32 v14, v14, v88
	v_bfe_u32 v15, v14, 16, 1
	v_add3_u32 v14, v14, v15, s61
	global_store_short_d16_hi v[12:13], v14, off offset:2176
	v_mul_f32_e32 v14, v48, v78
	v_mul_f32_e32 v14, v14, v74
	v_bfe_u32 v15, v14, 16, 1
	v_mul_f32_e32 v11, 0x3f4ccccd, v11
	v_add3_u32 v14, v14, v15, s61
	global_store_short_d16_hi v[12:13], v14, off offset:2240
	v_mul_f32_e32 v12, v67, v11
	v_mul_f32_e32 v12, v12, v76
	v_bfe_u32 v13, v12, 16, 1
	v_add3_u32 v14, v12, v13, s61
	v_add_co_u32_e32 v12, vcc, s65, v2
	v_mul_f32_e32 v10, v10, v86
	s_nop 0
	v_addc_co_u32_e32 v13, vcc, 0, v3, vcc
	global_store_short_d16_hi v[12:13], v14, off offset:2048
	v_mul_f32_e32 v14, v70, v11
	v_mul_f32_e32 v14, v14, v75
	v_bfe_u32 v15, v14, 16, 1
	v_add3_u32 v14, v14, v15, s61
	global_store_short_d16_hi v[12:13], v14, off offset:2112
	v_mul_f32_e32 v14, v60, v11
	v_mul_f32_e32 v14, v14, v88
	v_bfe_u32 v15, v14, 16, 1
	v_mul_f32_e32 v11, v47, v11
	v_add3_u32 v14, v14, v15, s61
	v_mul_f32_e32 v11, v11, v74
	global_store_short_d16_hi v[12:13], v14, off offset:2176
	v_bfe_u32 v14, v11, 16, 1
	v_add3_u32 v11, v11, v14, s61
	global_store_short_d16_hi v[12:13], v11, off offset:2240
	v_mul_f32_e32 v11, v66, v80
	v_mul_f32_e32 v11, v11, v76
	v_bfe_u32 v12, v11, 16, 1
	v_add3_u32 v11, v11, v12, s61
; __device__ __forceinline__ int crow(int r, int hi) { return (r & 3) + 8 * (r >> 2) + 4 * hi; }
; __device__ __forceinline__ unsigned f2bf(float f) { unsigned u = __builtin_bit_cast(unsigned, f); return (u + 0x7fffu + ((u >> 16) & 1u)) >> 16; }
;     ...
;     for (int r = 0; r < 16; ++r) { const int orow = crow(r, hi);
; #pragma unroll
;         for (int d0 = 0; d0 < 4; ++d0) Ow[(size_t)orow * 2048 + d0 * 32 + r32] = (att::bf16)f2bf(o[d0][r] * ss[r] * g4[d0]); }
	v_add_co_u32_e32 v12, vcc, s66, v2
	v_mul_f32_e32 v10, v10, v74
	s_nop 0
	v_addc_co_u32_e32 v13, vcc, 0, v3, vcc
	global_store_short_d16_hi v[12:13], v11, off offset:2048
	v_mul_f32_e32 v11, v69, v80
	v_mul_f32_e32 v11, v11, v75
	v_bfe_u32 v14, v11, 16, 1
	v_add3_u32 v11, v11, v14, s61
	global_store_short_d16_hi v[12:13], v11, off offset:2112
	v_mul_f32_e32 v11, v59, v80
	v_mul_f32_e32 v11, v11, v88
	v_bfe_u32 v14, v11, 16, 1
	v_add3_u32 v11, v11, v14, s61
	global_store_short_d16_hi v[12:13], v11, off offset:2176
	v_mul_f32_e32 v11, v46, v80
	v_mul_f32_e32 v11, v11, v74
	v_bfe_u32 v14, v11, 16, 1
	v_add3_u32 v11, v11, v14, s61
	global_store_short_d16_hi v[12:13], v11, off offset:2240
	v_mul_f32_e32 v11, v32, v79
	v_mul_f32_e32 v11, v11, v76
	v_bfe_u32 v12, v11, 16, 1
	v_add3_u32 v11, v11, v12, s61
	v_add_co_u32_e32 v12, vcc, s67, v2
	v_mul_f32_e32 v9, v9, v87
	s_nop 0
	v_addc_co_u32_e32 v13, vcc, 0, v3, vcc
	global_store_short_d16_hi v[12:13], v11, off offset:2048
	v_mul_f32_e32 v11, v55, v79
	v_mul_f32_e32 v11, v11, v75
	v_bfe_u32 v14, v11, 16, 1
	v_add3_u32 v11, v11, v14, s61
	global_store_short_d16_hi v[12:13], v11, off offset:2112
	v_mul_f32_e32 v11, v58, v79
	v_mul_f32_e32 v11, v11, v88
	v_bfe_u32 v14, v11, 16, 1
	v_add3_u32 v11, v11, v14, s61
	global_store_short_d16_hi v[12:13], v11, off offset:2176
	v_mul_f32_e32 v11, v45, v79
	v_mul_f32_e32 v11, v11, v74
	v_bfe_u32 v14, v11, 16, 1
	v_add3_u32 v11, v11, v14, s61
	global_store_short_d16_hi v[12:13], v11, off offset:2240
	v_mul_f32_e32 v11, v30, v81
	v_mul_f32_e32 v11, v11, v76
	v_bfe_u32 v12, v11, 16, 1
	v_add3_u32 v11, v11, v12, s61
	v_add_co_u32_e32 v12, vcc, s68, v2
	v_mul_f32_e32 v9, v9, v74
	s_nop 0
	v_addc_co_u32_e32 v13, vcc, 0, v3, vcc
	global_store_short_d16_hi v[12:13], v11, off offset:2048
	v_mul_f32_e32 v11, v54, v81
	v_mul_f32_e32 v11, v11, v75
	v_bfe_u32 v14, v11, 16, 1
	v_add3_u32 v11, v11, v14, s61
	global_store_short_d16_hi v[12:13], v11, off offset:2112
	v_mul_f32_e32 v11, v57, v81
	v_mul_f32_e32 v11, v11, v88
	v_bfe_u32 v14, v11, 16, 1
	v_add3_u32 v11, v11, v14, s61
	global_store_short_d16_hi v[12:13], v11, off offset:2176
	v_mul_f32_e32 v11, v44, v81
	v_mul_f32_e32 v11, v11, v74
	v_bfe_u32 v14, v11, 16, 1
	v_add3_u32 v11, v11, v14, s61
	global_store_short_d16_hi v[12:13], v11, off offset:2240
	v_mul_f32_e32 v11, v28, v85
	v_mul_f32_e32 v11, v11, v76
	v_bfe_u32 v12, v11, 16, 1
	v_add3_u32 v11, v11, v12, s61
	v_add_co_u32_e32 v12, vcc, s69, v2
	v_mul_f32_e32 v8, v8, v89
	s_nop 0
	v_addc_co_u32_e32 v13, vcc, 0, v3, vcc
	global_store_short_d16_hi v[12:13], v11, off offset:2048
	v_mul_f32_e32 v11, v53, v85
	v_mul_f32_e32 v11, v11, v75
	v_bfe_u32 v14, v11, 16, 1
	v_add3_u32 v11, v11, v14, s61
	global_store_short_d16_hi v[12:13], v11, off offset:2112
	v_mul_f32_e32 v11, v56, v85
	v_mul_f32_e32 v11, v11, v88
	v_bfe_u32 v14, v11, 16, 1
	v_add3_u32 v11, v11, v14, s61
	global_store_short_d16_hi v[12:13], v11, off offset:2176
	v_mul_f32_e32 v11, v43, v85
	v_mul_f32_e32 v11, v11, v74
	v_bfe_u32 v14, v11, 16, 1
	v_add3_u32 v11, v11, v14, s61
	global_store_short_d16_hi v[12:13], v11, off offset:2240
	v_mul_f32_e32 v11, v26, v77
	v_mul_f32_e32 v11, v11, v76
	v_bfe_u32 v12, v11, 16, 1
	v_add3_u32 v11, v11, v12, s61
	v_add_co_u32_e32 v12, vcc, s74, v2
	v_mul_f32_e32 v8, v8, v74
	s_nop 0
	v_addc_co_u32_e32 v13, vcc, 0, v3, vcc
	global_store_short_d16_hi v[12:13], v11, off offset:2048
	v_mul_f32_e32 v11, v52, v77
	v_mul_f32_e32 v11, v11, v75
	v_bfe_u32 v14, v11, 16, 1
	v_add3_u32 v11, v11, v14, s61
	global_store_short_d16_hi v[12:13], v11, off offset:2112
	v_mul_f32_e32 v11, v41, v77
	v_mul_f32_e32 v11, v11, v88
	v_bfe_u32 v14, v11, 16, 1
	v_add3_u32 v11, v11, v14, s61
	global_store_short_d16_hi v[12:13], v11, off offset:2176
	v_mul_f32_e32 v11, v42, v77
	v_mul_f32_e32 v11, v11, v74
	v_bfe_u32 v14, v11, 16, 1
	v_add3_u32 v11, v11, v14, s61
	global_store_short_d16_hi v[12:13], v11, off offset:2240
	v_mul_f32_e32 v11, v24, v86
	v_mul_f32_e32 v11, v11, v76
	v_bfe_u32 v12, v11, 16, 1
	v_add3_u32 v11, v11, v12, s61
	v_add_co_u32_e32 v12, vcc, s75, v2
	v_mul_f32_e32 v7, v7, v63
	s_nop 0
	v_addc_co_u32_e32 v13, vcc, 0, v3, vcc
	global_store_short_d16_hi v[12:13], v11, off offset:2048
	v_mul_f32_e32 v11, v51, v86
	v_mul_f32_e32 v11, v11, v75
	v_bfe_u32 v14, v11, 16, 1
	v_add3_u32 v11, v11, v14, s61
	global_store_short_d16_hi v[12:13], v11, off offset:2112
	v_mul_f32_e32 v11, v40, v86
	v_mul_f32_e32 v11, v11, v88
	v_bfe_u32 v14, v11, 16, 1
	v_add3_u32 v11, v11, v14, s61
; __device__ __forceinline__ int crow(int r, int hi) { return (r & 3) + 8 * (r >> 2) + 4 * hi; }
; __device__ __forceinline__ unsigned f2bf(float f) { unsigned u = __builtin_bit_cast(unsigned, f); return (u + 0x7fffu + ((u >> 16) & 1u)) >> 16; }
;     ...
;     for (int r = 0; r < 16; ++r) { const int orow = crow(r, hi);
; #pragma unroll
;         for (int d0 = 0; d0 < 4; ++d0) Ow[(size_t)orow * 2048 + d0 * 32 + r32] = (att::bf16)f2bf(o[d0][r] * ss[r] * g4[d0]); }
	global_store_short_d16_hi v[12:13], v11, off offset:2176
	v_bfe_u32 v11, v10, 16, 1
	v_add3_u32 v10, v10, v11, s61
	global_store_short_d16_hi v[12:13], v10, off offset:2240
	v_mul_f32_e32 v10, v23, v87
	v_mul_f32_e32 v10, v10, v76
	v_bfe_u32 v11, v10, 16, 1
	v_add3_u32 v12, v10, v11, s61
	v_add_co_u32_e32 v10, vcc, s76, v2
	v_mul_f32_e32 v7, v7, v74
	s_nop 0
	v_addc_co_u32_e32 v11, vcc, 0, v3, vcc
	global_store_short_d16_hi v[10:11], v12, off offset:2048
	v_mul_f32_e32 v12, v50, v87
	v_mul_f32_e32 v12, v12, v75
	v_bfe_u32 v13, v12, 16, 1
	v_add3_u32 v12, v12, v13, s61
	global_store_short_d16_hi v[10:11], v12, off offset:2112
	v_mul_f32_e32 v12, v39, v87
	v_mul_f32_e32 v12, v12, v88
	v_bfe_u32 v13, v12, 16, 1
	v_add3_u32 v12, v12, v13, s61
	global_store_short_d16_hi v[10:11], v12, off offset:2176
	v_bfe_u32 v12, v9, 16, 1
	v_add3_u32 v9, v9, v12, s61
	global_store_short_d16_hi v[10:11], v9, off offset:2240
	v_mul_f32_e32 v9, v22, v89
	v_mul_f32_e32 v9, v9, v76
	v_bfe_u32 v10, v9, 16, 1
	v_add3_u32 v9, v9, v10, s61
	v_add_co_u32_e32 v10, vcc, s77, v2
	v_mul_f32_e32 v6, v6, v64
	s_nop 0
	v_addc_co_u32_e32 v11, vcc, 0, v3, vcc
	global_store_short_d16_hi v[10:11], v9, off offset:2048
	v_mul_f32_e32 v9, v33, v89
	v_mul_f32_e32 v9, v9, v75
	v_bfe_u32 v12, v9, 16, 1
	v_add3_u32 v9, v9, v12, s61
	global_store_short_d16_hi v[10:11], v9, off offset:2112
	v_mul_f32_e32 v9, v38, v89
	v_mul_f32_e32 v9, v9, v88
	v_bfe_u32 v12, v9, 16, 1
	v_add3_u32 v9, v9, v12, s61
	global_store_short_d16_hi v[10:11], v9, off offset:2176
	v_bfe_u32 v9, v8, 16, 1
	v_add3_u32 v8, v8, v9, s61
	global_store_short_d16_hi v[10:11], v8, off offset:2240
	v_mul_f32_e32 v8, v21, v63
	v_mul_f32_e32 v8, v8, v76
	v_bfe_u32 v9, v8, 16, 1
	v_add3_u32 v10, v8, v9, s61
	v_add_co_u32_e32 v8, vcc, s78, v2
	v_mul_f32_e32 v6, v6, v74
	s_nop 0
	v_addc_co_u32_e32 v9, vcc, 0, v3, vcc
	global_store_short_d16_hi v[8:9], v10, off offset:2048
	v_mul_f32_e32 v10, v31, v63
	v_mul_f32_e32 v10, v10, v75
	v_bfe_u32 v11, v10, 16, 1
	v_add3_u32 v10, v10, v11, s61
	global_store_short_d16_hi v[8:9], v10, off offset:2112
	v_mul_f32_e32 v10, v37, v63
	v_mul_f32_e32 v10, v10, v88
	v_bfe_u32 v11, v10, 16, 1
	v_add3_u32 v10, v10, v11, s61
	global_store_short_d16_hi v[8:9], v10, off offset:2176
	v_bfe_u32 v10, v7, 16, 1
	v_add3_u32 v7, v7, v10, s61
	global_store_short_d16_hi v[8:9], v7, off offset:2240
	v_mul_f32_e32 v7, v20, v64
	v_mul_f32_e32 v7, v7, v76
	v_bfe_u32 v8, v7, 16, 1
	v_add3_u32 v7, v7, v8, s61
	v_add_co_u32_e32 v8, vcc, s79, v2
	v_mul_f32_e32 v5, v5, v91
	s_nop 0
	v_addc_co_u32_e32 v9, vcc, 0, v3, vcc
	global_store_short_d16_hi v[8:9], v7, off offset:2048
	v_mul_f32_e32 v7, v29, v64
	v_mul_f32_e32 v7, v7, v75
	v_bfe_u32 v10, v7, 16, 1
	v_add3_u32 v7, v7, v10, s61
	global_store_short_d16_hi v[8:9], v7, off offset:2112
	v_mul_f32_e32 v7, v36, v64
	v_mul_f32_e32 v7, v7, v88
	v_bfe_u32 v10, v7, 16, 1
	v_add3_u32 v7, v7, v10, s61
	global_store_short_d16_hi v[8:9], v7, off offset:2176
	v_bfe_u32 v7, v6, 16, 1
	v_add3_u32 v6, v6, v7, s61
	global_store_short_d16_hi v[8:9], v6, off offset:2240
	v_mul_f32_e32 v6, v19, v91
	v_mul_f32_e32 v6, v6, v76
	v_bfe_u32 v7, v6, 16, 1
	v_add3_u32 v8, v6, v7, s61
	v_add_co_u32_e32 v6, vcc, s80, v2
	v_mul_f32_e32 v5, v5, v74
	s_nop 0
	v_addc_co_u32_e32 v7, vcc, 0, v3, vcc
	global_store_short_d16_hi v[6:7], v8, off offset:2048
	v_mul_f32_e32 v8, v27, v91
	v_mul_f32_e32 v8, v8, v75
	v_bfe_u32 v9, v8, 16, 1
	v_add3_u32 v8, v8, v9, s61
	global_store_short_d16_hi v[6:7], v8, off offset:2112
	v_mul_f32_e32 v8, v35, v91
	v_mul_f32_e32 v8, v8, v88
	v_bfe_u32 v9, v8, 16, 1
	v_add3_u32 v8, v8, v9, s61
	global_store_short_d16_hi v[6:7], v8, off offset:2176
	v_bfe_u32 v8, v5, 16, 1
	v_add3_u32 v5, v5, v8, s61
	global_store_short_d16_hi v[6:7], v5, off offset:2240
	v_mul_f32_e32 v5, v18, v92
	v_mul_f32_e32 v5, v76, v5
	v_bfe_u32 v6, v5, 16, 1
	v_add_co_u32_e32 v2, vcc, s81, v2
	v_add3_u32 v5, v5, v6, s61
	s_nop 0
	v_addc_co_u32_e32 v3, vcc, 0, v3, vcc
	global_store_short_d16_hi v[2:3], v5, off offset:2048
	v_mul_f32_e32 v5, v25, v92
	v_mul_f32_e32 v5, v75, v5
	v_bfe_u32 v6, v5, 16, 1
	v_add3_u32 v5, v5, v6, s61
	global_store_short_d16_hi v[2:3], v5, off offset:2112
	v_mul_f32_e32 v5, v34, v92
	v_mul_f32_e32 v5, v88, v5
	v_bfe_u32 v6, v5, 16, 1
	v_mul_f32_e32 v4, v4, v92
	v_add3_u32 v5, v5, v6, s61
	v_mul_f32_e32 v4, v74, v4
	global_store_short_d16_hi v[2:3], v5, off offset:2176
	v_bfe_u32 v5, v4, 16, 1
	v_add3_u32 v4, v4, v5, s61
	global_store_short_d16_hi v[2:3], v4, off offset:2240

; __device__ __forceinline__ float softmax_rowmax(const f32x16& p0, const f32x16& p1) {
;   const float m0 = p1[0] + 0.0f; float a, b;
;   asm("v_max3_f32 %0, %1, %2, %3\n\tv_max3_f32 %0, %0, %4, %5\n\tv_max3_f32 %0, %0, %6, %7\n\tv_max3_f32 %0, %0, %8, %9\n\t"
;       "v_max3_f32 %0, %0, %10, %11\n\tv_max3_f32 %0, %0, %12, %13\n\tv_max3_f32 %0, %0, %14, %15\n\tv_max3_f32 %0, %0, %16, %17"
;       : "=&v"(a) : "v"(m0), "v"(p0[0]), "v"(p0[1]), "v"(p0[2]), "v"(p0[3]), "v"(p0[4]), "v"(p0[5]), "v"(p0[6]), "v"(p0[7]), "v"(p0[8]), "v"(p0[9]), "v"(p0[10]), "v"(p0[11]), "v"(p0[12]), "v"(p0[13]), "v"(p0[14]), "v"(p0[15]));
;   asm("v_max3_f32 %0, %1, %2, %3\n\tv_max3_f32 %0, %0, %4, %5\n\tv_max3_f32 %0, %0, %6, %7\n\tv_max3_f32 %0, %0, %8, %9\n\t"
;       "v_max3_f32 %0, %0, %10, %11\n\tv_max3_f32 %0, %0, %12, %13\n\tv_max3_f32 %0, %0, %14, %15\n\tv_max_f32 %0, %0, %16"
;       : "=&v"(b) : "v"(a), "v"(p1[1]), "v"(p1[2]), "v"(p1[3]), "v"(p1[4]), "v"(p1[5]), "v"(p1[6]), "v"(p1[7]), "v"(p1[8]), "v"(p1[9]), "v"(p1[10]), "v"(p1[11]), "v"(p1[12]), "v"(p1[13]), "v"(p1[14]), "v"(p1[15]));
;   return b;
; }
; __device__ __forceinline__ float softmax_shift(f32x16& p0, f32x16& p1, f32x16& negm, float pmax, bool first) {
;   asm volatile("s_nop 4" ::: "memory");
;   { auto rr = __builtin_amdgcn_permlane32_swap(__float_as_uint(pmax), __float_as_uint(pmax), false, false);
;     pmax = fmaxf(__uint_as_float(rr[0]), __uint_as_float(rr[1])); }
;   const float delta = first ? pmax : fmaxf(pmax, 0.f);
; #pragma unroll
;   for (int r = 0; r < 16; ++r) { p0[r] -= delta; p1[r] -= delta; negm[r] -= delta; }
;   return first ? 1.f : __builtin_amdgcn_exp2f(-delta);
; }
; __device__ __forceinline__ void softmax_exp_pack(f32x16& p0, f32x16& p1, bf16x8& pa0, bf16x8& pa1, bf16x8& pa2, bf16x8& pa3) {
; #pragma unroll
;   for (int r = 0; r < 16; ++r) { p0[r] = __builtin_amdgcn_exp2f(p0[r]); p1[r] = __builtin_amdgcn_exp2f(p1[r]); }
;     ...
;   ATT_PK4(p0, 0, pa0); ATT_PK4(p0, 8, pa1); ATT_PK4(p1, 0, pa2); ATT_PK4(p1, 8, pa3);
;     ...
; }
;     ...
;   for (int t = 0; t + 1 < NT; ++t) {
;     if constexpr (ABL & 1) { u32x4 w0 = {cvtpk(p0[0], p0[1]), cvtpk(p0[2], p0[3]), cvtpk(p0[4], p0[5]), cvtpk(p0[6], p0[7])}, w1 = {cvtpk(p0[8], p0[9]), cvtpk(p0[10], p0[11]), cvtpk(p0[12], p0[13]), cvtpk(p0[14], p0[15])};
.LBB0_264:
	v_mul_u32_u24_e32 v18, 0x110, v213
	v_add3_u32 v69, 0, v184, v18
	ds_read_b128 v[18:21], v69 offset:49152
	v_mad_u32_u24 v188, v213, s54, 0
	v_add_u32_e32 v192, v188, v184
	ds_read_b128 v[34:37], v192 offset:57856
	ds_read_b128 v[70:73], v69 offset:49184
	ds_read_b128 v[74:77], v69 offset:49216
	s_and_b32 s4, s89, 0x3fffffc0
	s_lshl_b32 s4, s4, 2
	s_add_i32 s90, s4, 0
	s_add_i32 s90, s90, 0x23080
	s_waitcnt lgkmcnt(3)
	v_mfma_f32_32x32x16_bf16 v[18:33], v[18:21], v[136:139], 0
	s_mov_b32 s95, 1
	s_waitcnt lgkmcnt(2)
	v_mfma_f32_32x32x16_bf16 v[34:49], v[34:37], v[136:139], 0
	s_waitcnt lgkmcnt(1)
	v_mfma_f32_32x32x16_bf16 v[18:33], v[70:73], v[140:143], v[18:33]
	ds_read_b128 v[70:73], v69 offset:57888
	ds_read_b128 v[78:81], v69 offset:49376
	s_waitcnt lgkmcnt(1)
	v_mfma_f32_32x32x16_bf16 v[34:49], v[70:73], v[140:143], v[34:49]
	v_mfma_f32_32x32x16_bf16 v[18:33], v[74:77], v[144:147], v[18:33]
	ds_read_b128 v[70:73], v69 offset:57920
	ds_read_b128 v[74:77], v69 offset:57952
	s_waitcnt lgkmcnt(1)
	v_mfma_f32_32x32x16_bf16 v[34:49], v[70:73], v[144:147], v[34:49]
	ds_read_b128 v[70:73], v69 offset:49248
	ds_read_b128 v[82:85], v69 offset:49280
	s_waitcnt lgkmcnt(1)
	v_mfma_f32_32x32x16_bf16 v[18:33], v[70:73], v[148:151], v[18:33]
	v_mfma_f32_32x32x16_bf16 v[34:49], v[74:77], v[148:151], v[34:49]
	ds_read_b128 v[70:73], v69 offset:57984
	ds_read_b128 v[74:77], v69 offset:58016
	s_waitcnt lgkmcnt(2)
	v_mfma_f32_32x32x16_bf16 v[18:33], v[82:85], v[152:155], v[18:33]
	s_waitcnt lgkmcnt(1)
	v_mfma_f32_32x32x16_bf16 v[34:49], v[70:73], v[152:155], v[34:49]
	ds_read_b128 v[70:73], v69 offset:49312
	ds_read_b128 v[82:85], v69 offset:49344
	s_waitcnt lgkmcnt(1)
	v_mfma_f32_32x32x16_bf16 v[18:33], v[70:73], v[156:159], v[18:33]
	v_mfma_f32_32x32x16_bf16 v[34:49], v[74:77], v[156:159], v[34:49]
	ds_read_b128 v[70:73], v69 offset:58048
	ds_read_b128 v[74:77], v69 offset:58080
	v_and_b32_e32 v69, 63, v212
	s_waitcnt lgkmcnt(2)
	v_mfma_f32_32x32x16_bf16 v[18:33], v[82:85], v[160:163], v[18:33]
	s_waitcnt lgkmcnt(1)
	v_mfma_f32_32x32x16_bf16 v[34:49], v[70:73], v[160:163], v[34:49]
	v_lshlrev_b32_e32 v70, 3, v69
	v_lshlrev_b32_e32 v72, 4, v69
	v_lshlrev_b32_e32 v73, 1, v69
	v_and_b32_e32 v71, 24, v70
	v_and_b32_e32 v72, 0xc0, v72
	v_and_b32_e32 v73, 32, v73
	v_and_b32_e32 v70, 0x100, v70
	v_mfma_f32_32x32x16_bf16 v[18:33], v[78:81], v[164:167], v[18:33]
	s_waitcnt lgkmcnt(0)
	v_mfma_f32_32x32x16_bf16 v[34:49], v[74:77], v[164:167], v[34:49]
	s_barrier
	v_add3_u32 v71, 0, v71, v72
	v_add3_u32 v131, v71, v73, v70
	v_cmp_gt_u32_e64 s[4:5], 32, v69
	s_nop 8
	v_add_f32_e32 v69, 0, v34
	v_max3_f32 v70, v69, v18, v19
	v_max3_f32 v70, v70, v20, v21
	v_max3_f32 v70, v70, v22, v23
	v_max3_f32 v70, v70, v24, v25
	v_max3_f32 v70, v70, v26, v27
	v_max3_f32 v70, v70, v28, v29
	v_max3_f32 v70, v70, v30, v31
	v_max3_f32 v70, v70, v32, v33
	s_nop 4
	v_lshl_add_u32 v187, v213, 2, s90
	v_max3_f32 v69, v70, v35, v36
	v_max3_f32 v69, v69, v37, v38
	v_max3_f32 v69, v69, v39, v40
	v_max3_f32 v69, v69, v41, v42
	v_max3_f32 v69, v69, v43, v44
	v_max3_f32 v69, v69, v45, v46
	v_max3_f32 v69, v69, v47, v48
	v_max_f32 v69, v69, v49
	s_nop 0
	v_mov_b32_e32 v70, v69
	s_nop 1
	v_permlane32_swap_b32_e32 v69, v70
	v_max_f32_e32 v70, v70, v70
	v_max_f32_e32 v69, v69, v69
	v_max_f32_e32 v69, v69, v70
	v_sub_f32_e32 v18, v18, v69
	v_sub_f32_e32 v34, v34, v69
	v_sub_f32_e32 v19, v19, v69
	v_sub_f32_e32 v35, v35, v69
	v_sub_f32_e32 v20, v20, v69
	v_sub_f32_e32 v36, v36, v69
	v_sub_f32_e32 v21, v21, v69
	v_sub_f32_e32 v37, v37, v69
	v_sub_f32_e32 v22, v22, v69
	v_sub_f32_e32 v38, v38, v69
	v_sub_f32_e32 v23, v23, v69
	v_sub_f32_e32 v39, v39, v69
	v_sub_f32_e32 v24, v24, v69
	v_sub_f32_e32 v40, v40, v69
	v_sub_f32_e32 v25, v25, v69
	v_sub_f32_e32 v41, v41, v69
	v_sub_f32_e32 v26, v26, v69
	v_sub_f32_e32 v42, v42, v69
	v_sub_f32_e32 v27, v27, v69
	v_sub_f32_e32 v43, v43, v69
	v_sub_f32_e32 v28, v28, v69
	v_sub_f32_e32 v44, v44, v69
	v_sub_f32_e32 v29, v29, v69
	v_sub_f32_e32 v45, v45, v69
	v_sub_f32_e32 v30, v30, v69
	v_sub_f32_e32 v46, v46, v69
	v_sub_f32_e32 v31, v31, v69
	v_sub_f32_e32 v47, v47, v69
	v_sub_f32_e32 v32, v32, v69
	v_sub_f32_e32 v48, v48, v69
	v_sub_f32_e32 v33, v33, v69
	v_sub_f32_e32 v49, v49, v69
	v_exp_f32_e32 v18, v18
	v_exp_f32_e32 v34, v34
	v_exp_f32_e32 v19, v19
	v_exp_f32_e32 v35, v35
	v_exp_f32_e32 v20, v20
	v_exp_f32_e32 v36, v36
	v_exp_f32_e32 v21, v21
	v_exp_f32_e32 v37, v37
	v_exp_f32_e32 v22, v22
	v_exp_f32_e32 v38, v38
	v_exp_f32_e32 v23, v23
	v_exp_f32_e32 v39, v39
	v_exp_f32_e32 v24, v24
	v_exp_f32_e32 v40, v40
	v_exp_f32_e32 v25, v25
	v_exp_f32_e32 v41, v41
	v_exp_f32_e32 v26, v26
	v_exp_f32_e32 v42, v42
	v_exp_f32_e32 v27, v27
	v_exp_f32_e32 v43, v43
	v_exp_f32_e32 v28, v28
	v_exp_f32_e32 v44, v44
	v_exp_f32_e32 v29, v29
	v_exp_f32_e32 v45, v45
	v_exp_f32_e32 v30, v30
	v_exp_f32_e32 v46, v46
	v_exp_f32_e32 v31, v31
	v_exp_f32_e32 v47, v47
	v_exp_f32_e32 v32, v32
	v_exp_f32_e32 v48, v48
	v_exp_f32_e32 v33, v33
	v_exp_f32_e32 v49, v49
	v_sub_f32_e32 v82, 0, v69
	v_mov_b32_e32 v83, v82
	v_mov_b32_e32 v84, v82
	v_mov_b32_e32 v85, v82
	v_mov_b32_e32 v86, v82
	v_mov_b32_e32 v87, v82
	v_mov_b32_e32 v88, v82
	v_mov_b32_e32 v89, v82
	v_mov_b32_e32 v90, v82
	v_mov_b32_e32 v91, v82
	v_mov_b32_e32 v92, v82
	v_mov_b32_e32 v93, v82
	v_mov_b32_e32 v94, v82
	v_mov_b32_e32 v95, v82
	v_mov_b32_e32 v96, v82
	v_mov_b32_e32 v97, v82
	v_cvt_pk_bf16_f32 v98, v18, v19
	v_cvt_pk_bf16_f32 v99, v20, v21
	v_cvt_pk_bf16_f32 v100, v22, v23
	v_cvt_pk_bf16_f32 v101, v24, v25
	v_cvt_pk_bf16_f32 v102, v26, v27
	v_cvt_pk_bf16_f32 v103, v28, v29
	v_cvt_pk_bf16_f32 v104, v30, v31
	v_cvt_pk_bf16_f32 v105, v32, v33
	v_cvt_pk_bf16_f32 v106, v34, v35
	v_cvt_pk_bf16_f32 v107, v36, v37
	v_cvt_pk_bf16_f32 v108, v38, v39
	v_cvt_pk_bf16_f32 v109, v40, v41
	v_cvt_pk_bf16_f32 v110, v42, v43
	v_cvt_pk_bf16_f32 v111, v44, v45
	v_cvt_pk_bf16_f32 v112, v46, v47
	v_cvt_pk_bf16_f32 v113, v48, v49
	v_add_u32_e32 v18, 0x14800, v66
	s_waitcnt vmcnt(3)
	ds_write_b128 v18, v[50:53]
	s_waitcnt vmcnt(2)
	ds_write_b128 v18, v[54:57] offset:8704
	s_waitcnt vmcnt(1)
	ds_write_b128 v67, v[58:61] offset:16384
	s_waitcnt vmcnt(0)
	ds_write_b128 v68, v[62:65] offset:16384
	ds_read_b64_tr_b16 v[18:19], v131
	ds_read_b64_tr_b16 v[20:21], v131 offset:2048
	ds_read_b64_tr_b16 v[34:35], v131 offset:4096
	ds_read_b64_tr_b16 v[36:37], v131 offset:6144
	ds_read_b64_tr_b16 v[38:39], v131 offset:8192
	ds_read_b64_tr_b16 v[40:41], v131 offset:10240
	ds_read_b64_tr_b16 v[42:43], v131 offset:12288
	ds_read_b64_tr_b16 v[44:45], v131 offset:14336
	s_waitcnt lgkmcnt(8)
	s_barrier
; #define ATT_SBAR() __builtin_amdgcn_sched_barrier(0)
; __device__ __forceinline__ unsigned cvtpk(float lo, float hi) { f32x2_t v = {lo, hi}; bf16x2_t b = __builtin_convertvector(v, bf16x2_t); return __builtin_bit_cast(unsigned, b); }
; #define ATT_LOAD_K(t) do { const unsigned so_ = (unsigned)(t) * (unsigned)(KVBLK * LDK * 2); sk0 = __builtin_bit_cast(bf16x8, __builtin_amdgcn_raw_buffer_load_b128(krs, koff, so_, 0)); \
;     if constexpr (DQK == 128) sk1 = __builtin_bit_cast(bf16x8, __builtin_amdgcn_raw_buffer_load_b128(krs, koff, so_ + (unsigned)(32 * LDK * 2), 0)); } while (0)
; #define ATT_LOAD_V(t) do { const unsigned so_ = (unsigned)(t) * (unsigned)(KVBLK * LDV * 2); sv0 = __builtin_bit_cast(bf16x8, __builtin_amdgcn_raw_buffer_load_b128(vrs, voff, so_, 0)); \
;     sv1 = __builtin_bit_cast(bf16x8, __builtin_amdgcn_raw_buffer_load_b128(vrs, voff, so_ + (unsigned)(32 * LDV * 2), 0)); } while (0)
; #define ATT_WRITE_K(so) do { *(bf16x8*)(K_lds + (so) + kswz<DQK>(kr, kc * 2)) = sk0; if constexpr (DQK == 128) *(bf16x8*)(K_lds + (so) + kswz<DQK>(32 + kr, kc * 2)) = sk1; } while (0)
; #define ATT_WRITE_V(so) do { *(bf16x8*)(V_lds + (so) + vst0) = sv0; *(bf16x8*)(V_lds + (so) + vst1) = sv1; } while (0)
;     ...
;   for (int t = 0; t + 1 < NT; ++t) {
;     if constexpr (ABL & 1) { u32x4 w0 = {cvtpk(p0[0], p0[1]), cvtpk(p0[2], p0[3]), cvtpk(p0[4], p0[5]), cvtpk(p0[6], p0[7])}, w1 = {cvtpk(p0[8], p0[9]), cvtpk(p0[10], p0[11]), cvtpk(p0[12], p0[13]), cvtpk(p0[14], p0[15])};
;         u32x4 w2 = {cvtpk(p1[0], p1[1]), cvtpk(p1[2], p1[3]), cvtpk(p1[4], p1[5]), cvtpk(p1[6], p1[7])}, w3 = {cvtpk(p1[8], p1[9]), cvtpk(p1[10], p1[11]), cvtpk(p1[12], p1[13]), cvtpk(p1[14], p1[15])};
;         pa0 = *reinterpret_cast<bf16x8*>(&w0); pa1 = *reinterpret_cast<bf16x8*>(&w1); pa2 = *reinterpret_cast<bf16x8*>(&w2); pa3 = *reinterpret_cast<bf16x8*>(&w3); }
;     else { ATT_SOFTMAX(t == 0); }
;     if constexpr (!(ABL & 4)) { ATT_WRITE_K(k2); ATT_WRITE_V(v1); }
;     ATT_SBAR();
; #pragma unroll
;     for (int ks = 0; ks < 4; ++ks) ATT_VPAIR(va, v0, 0, ks);
;     asm volatile("s_waitcnt lgkmcnt(8)" ::: "memory"); ATT_BAR();
;     ATT_XSECTION(true);
;     if constexpr (!(ABL & 4)) { const int tk = (t + 3 < NT) ? t + 3 : NT - 1, tv = (t + 2 < NT) ? t + 2 : NT - 1; ATT_LOAD_K(tk); ATT_LOAD_V(tv); }
;     ATT_BAR();
	s_setprio 2
	s_waitcnt lgkmcnt(6)
	v_mfma_f32_32x32x16_bf16 v[18:33], v[98:101], v[18:21], 0
	ds_read_b64_tr_b16 v[46:47], v131 offset:512
	ds_read_b64_tr_b16 v[48:49], v131 offset:2560
	s_waitcnt lgkmcnt(6)
	v_mfma_f32_32x32x16_bf16 v[18:33], v[102:105], v[34:37], v[18:33]
	ds_read_b64_tr_b16 v[50:51], v131 offset:4608
	ds_read_b64_tr_b16 v[52:53], v131 offset:6656
	s_waitcnt lgkmcnt(6)
	v_mfma_f32_32x32x16_bf16 v[18:33], v[106:109], v[38:41], v[18:33]
	ds_read_b64_tr_b16 v[54:55], v131 offset:8704
	ds_read_b64_tr_b16 v[56:57], v131 offset:10752
	s_waitcnt lgkmcnt(6)
	v_mfma_f32_32x32x16_bf16 v[18:33], v[110:113], v[42:45], v[18:33]
	ds_read_b64_tr_b16 v[58:59], v131 offset:12800
	ds_read_b64_tr_b16 v[60:61], v131 offset:14848
	s_waitcnt lgkmcnt(6)
	v_mfma_f32_32x32x16_bf16 v[34:49], v[98:101], v[46:49], 0
	ds_read_b64_tr_b16 v[62:63], v131 offset:1024
	ds_read_b64_tr_b16 v[64:65], v131 offset:3072
	s_waitcnt lgkmcnt(6)
	v_mfma_f32_32x32x16_bf16 v[34:49], v[102:105], v[50:53], v[34:49]
	ds_read_b64_tr_b16 v[66:67], v131 offset:5120
	ds_read_b64_tr_b16 v[68:69], v131 offset:7168
	s_waitcnt lgkmcnt(6)
	v_mfma_f32_32x32x16_bf16 v[34:49], v[106:109], v[54:57], v[34:49]
	ds_read_b64_tr_b16 v[70:71], v131 offset:9216
	ds_read_b64_tr_b16 v[72:73], v131 offset:11264
	s_waitcnt lgkmcnt(6)
	v_mfma_f32_32x32x16_bf16 v[34:49], v[110:113], v[58:61], v[34:49]
	ds_read_b64_tr_b16 v[74:75], v131 offset:13312
	ds_read_b64_tr_b16 v[76:77], v131 offset:15360
	s_waitcnt lgkmcnt(6)
	v_mfma_f32_32x32x16_bf16 v[50:65], v[98:101], v[62:65], 0
	ds_read_b64_tr_b16 v[78:79], v131 offset:1536
	ds_read_b64_tr_b16 v[80:81], v131 offset:3584
	s_waitcnt lgkmcnt(6)
	v_mfma_f32_32x32x16_bf16 v[50:65], v[102:105], v[66:69], v[50:65]
	ds_read_b64_tr_b16 v[114:115], v131 offset:5632
	ds_read_b64_tr_b16 v[116:117], v131 offset:7680
	s_waitcnt lgkmcnt(6)
	v_mfma_f32_32x32x16_bf16 v[50:65], v[106:109], v[70:73], v[50:65]
	ds_read_b64_tr_b16 v[118:119], v131 offset:9728
	ds_read_b64_tr_b16 v[120:121], v131 offset:11776
	s_waitcnt lgkmcnt(6)
	v_mfma_f32_32x32x16_bf16 v[50:65], v[110:113], v[74:77], v[50:65]
	ds_read_b64_tr_b16 v[122:123], v131 offset:13824
	ds_read_b64_tr_b16 v[124:125], v131 offset:15872
	s_waitcnt lgkmcnt(6)
	v_mfma_f32_32x32x16_bf16 v[66:81], v[98:101], v[78:81], 0
	v_add_u32_e32 v193, 0xc000, v192
	ds_read_b128 v[126:129], v193 offset:17408
	s_waitcnt lgkmcnt(5)
	v_mfma_f32_32x32x16_bf16 v[66:81], v[102:105], v[114:117], v[66:81]
	ds_read_b128 v[168:171], v193 offset:26112
	s_waitcnt lgkmcnt(4)
	v_mfma_f32_32x32x16_bf16 v[66:81], v[106:109], v[118:121], v[66:81]
	ds_read_b128 v[172:175], v193 offset:17440
	s_waitcnt lgkmcnt(3)
	v_mfma_f32_32x32x16_bf16 v[66:81], v[110:113], v[122:125], v[66:81]
	ds_read_b128 v[176:179], v193 offset:26144
	v_mfma_f32_4x4x4_16b_bf16 v[240:243], v[98:99], v[132:133], 0
	ds_read_b128 v[180:183], v193 offset:17472
	v_mfma_f32_4x4x4_16b_bf16 v[244:247], v[100:101], v[132:133], 0
	v_mfma_f32_4x4x4_16b_bf16 v[240:243], v[102:103], v[132:133], v[240:243]
	ds_read_b128 v[194:197], v193 offset:26176
	v_mfma_f32_4x4x4_16b_bf16 v[244:247], v[104:105], v[132:133], v[244:247]
	v_mfma_f32_4x4x4_16b_bf16 v[240:243], v[106:107], v[132:133], v[240:243]
	ds_read_b128 v[198:201], v193 offset:17504
	v_mfma_f32_4x4x4_16b_bf16 v[244:247], v[108:109], v[132:133], v[244:247]
	v_mfma_f32_4x4x4_16b_bf16 v[240:243], v[110:111], v[132:133], v[240:243]
	ds_read_b128 v[212:215], v193 offset:26208
	v_mfma_f32_4x4x4_16b_bf16 v[244:247], v[112:113], v[132:133], v[244:247]
	s_waitcnt lgkmcnt(7)
	v_mfma_f32_32x32x16_bf16 v[98:113], v[126:129], v[136:139], v[82:97]
	ds_read_b128 v[216:219], v193 offset:17536
	v_mov_b64_e32 v[128:129], v[96:97]
	v_mov_b64_e32 v[126:127], v[94:95]
	v_mov_b64_e32 v[124:125], v[92:93]
	v_mov_b64_e32 v[122:123], v[90:91]
	v_mov_b64_e32 v[120:121], v[88:89]
	v_mov_b64_e32 v[118:119], v[86:87]
	v_mov_b64_e32 v[116:117], v[84:85]
	v_mov_b64_e32 v[114:115], v[82:83]
	ds_read_b128 v[220:223], v193 offset:26240
	s_waitcnt lgkmcnt(8)
	v_mfma_f32_32x32x16_bf16 v[114:129], v[168:171], v[136:139], v[114:129]
	s_waitcnt lgkmcnt(7)
	v_mfma_f32_32x32x16_bf16 v[98:113], v[172:175], v[140:143], v[98:113]
	ds_read_b128 v[168:171], v193 offset:17568
	s_waitcnt lgkmcnt(7)
	v_mfma_f32_32x32x16_bf16 v[114:129], v[176:179], v[140:143], v[114:129]
	ds_read_b128 v[172:175], v193 offset:26272
	s_waitcnt lgkmcnt(7)
	v_mfma_f32_32x32x16_bf16 v[98:113], v[180:183], v[144:147], v[98:113]
	ds_read_b128 v[176:179], v193 offset:17600
	s_waitcnt lgkmcnt(7)
	v_mfma_f32_32x32x16_bf16 v[114:129], v[194:197], v[144:147], v[114:129]
	ds_read_b128 v[180:183], v193 offset:26304
	s_waitcnt lgkmcnt(7)
	v_mfma_f32_32x32x16_bf16 v[98:113], v[198:201], v[148:151], v[98:113]
	ds_read_b128 v[194:197], v193 offset:17632
	s_waitcnt lgkmcnt(7)
	v_mfma_f32_32x32x16_bf16 v[114:129], v[212:215], v[148:151], v[114:129]
	ds_read_b128 v[198:201], v193 offset:26336
	s_waitcnt lgkmcnt(7)
	v_mfma_f32_32x32x16_bf16 v[98:113], v[216:219], v[152:155], v[98:113]
	s_waitcnt lgkmcnt(6)
	v_mfma_f32_32x32x16_bf16 v[114:129], v[220:223], v[152:155], v[114:129]
	s_waitcnt lgkmcnt(5)
	v_mfma_f32_32x32x16_bf16 v[98:113], v[168:171], v[156:159], v[98:113]
	s_waitcnt lgkmcnt(4)
	v_mfma_f32_32x32x16_bf16 v[114:129], v[172:175], v[156:159], v[114:129]
	s_waitcnt lgkmcnt(3)
	v_mfma_f32_32x32x16_bf16 v[98:113], v[176:179], v[160:163], v[98:113]
	s_waitcnt lgkmcnt(2)
	v_mfma_f32_32x32x16_bf16 v[114:129], v[180:183], v[160:163], v[114:129]
	s_waitcnt lgkmcnt(1)
	v_mfma_f32_32x32x16_bf16 v[98:113], v[194:197], v[164:167], v[98:113]
	s_waitcnt lgkmcnt(0)
	v_mfma_f32_32x32x16_bf16 v[114:129], v[198:201], v[164:167], v[114:129]
	s_setprio 0
	s_mov_b32 s14, s10
	s_mov_b32 s15, s11
	s_mov_b32 s96, 0x1c000
	buffer_load_dwordx4 v[224:227], v191, s[8:11], s59 offen
	buffer_load_dwordx4 v[228:231], v191, s[8:11], s96 offen
	buffer_load_dwordx4 v[232:235], v191, s[12:15], s57 offen
	buffer_load_dwordx4 v[236:239], v191, s[12:15], s58 offen
	s_barrier
	s_mov_b32 s93, 0x8000
	s_movk_i32 s15, 0x4000
	s_movk_i32 s94, 0x4400
	s_mov_b32 s92, 0
	s_mov_b32 s14, 0x8800
	s_mov_b32 s91, 0

; #define ATT_SBAR() __builtin_amdgcn_sched_barrier(0)
; __device__ __forceinline__ unsigned cvtpk(float lo, float hi) { f32x2_t v = {lo, hi}; bf16x2_t b = __builtin_convertvector(v, bf16x2_t); return __builtin_bit_cast(unsigned, b); }
; #define ATT_PK4(P, BASE, OUT) do { u32x4 w = {cvtpk(P[BASE + 0], P[BASE + 1]), cvtpk(P[BASE + 2], P[BASE + 3]), cvtpk(P[BASE + 4], P[BASE + 5]), cvtpk(P[BASE + 6], P[BASE + 7])}; \
;     OUT = *reinterpret_cast<bf16x8*>(&w); } while (0)
; #define ATT_LOAD_K(t) do { const unsigned so_ = (unsigned)(t) * (unsigned)(KVBLK * LDK * 2); sk0 = __builtin_bit_cast(bf16x8, __builtin_amdgcn_raw_buffer_load_b128(krs, koff, so_, 0)); \
;     if constexpr (DQK == 128) sk1 = __builtin_bit_cast(bf16x8, __builtin_amdgcn_raw_buffer_load_b128(krs, koff, so_ + (unsigned)(32 * LDK * 2), 0)); } while (0)
; #define ATT_BAR() do { ATT_SBAR(); asm volatile("s_barrier" ::: "memory"); ATT_SBAR(); } while (0)
; __device__ __forceinline__ void softmax_exp_pack(f32x16& p0, f32x16& p1, bf16x8& pa0, bf16x8& pa1, bf16x8& pa2, bf16x8& pa3) {
; #pragma unroll
;   for (int r = 0; r < 16; ++r) { p0[r] = __builtin_amdgcn_exp2f(p0[r]); p1[r] = __builtin_amdgcn_exp2f(p1[r]); }
;     ...
;   ATT_PK4(p0, 0, pa0); ATT_PK4(p0, 8, pa1); ATT_PK4(p1, 0, pa2); ATT_PK4(p1, 8, pa3);
;     ...
; }
;     ...
;   for (int t = 0; t + 1 < NT; ++t) {
;     if constexpr (ABL & 1) { u32x4 w0 = {cvtpk(p0[0], p0[1]), cvtpk(p0[2], p0[3]), cvtpk(p0[4], p0[5]), cvtpk(p0[6], p0[7])}, w1 = {cvtpk(p0[8], p0[9]), cvtpk(p0[10], p0[11]), cvtpk(p0[12], p0[13]), cvtpk(p0[14], p0[15])};
;         u32x4 w2 = {cvtpk(p1[0], p1[1]), cvtpk(p1[2], p1[3]), cvtpk(p1[4], p1[5]), cvtpk(p1[6], p1[7])}, w3 = {cvtpk(p1[8], p1[9]), cvtpk(p1[10], p1[11]), cvtpk(p1[12], p1[13]), cvtpk(p1[14], p1[15])};
;         pa0 = *reinterpret_cast<bf16x8*>(&w0); pa1 = *reinterpret_cast<bf16x8*>(&w1); pa2 = *reinterpret_cast<bf16x8*>(&w2); pa3 = *reinterpret_cast<bf16x8*>(&w3); }
;     else { ATT_SOFTMAX(t == 0); }
;     if constexpr (!(ABL & 4)) { ATT_WRITE_K(k2); ATT_WRITE_V(v1); }
;     ATT_SBAR();
; #pragma unroll
;     for (int ks = 0; ks < 4; ++ks) ATT_VPAIR(va, v0, 0, ks);
;     asm volatile("s_waitcnt lgkmcnt(8)" ::: "memory"); ATT_BAR();
;     ATT_XSECTION(true);
;     if constexpr (!(ABL & 4)) { const int tk = (t + 3 < NT) ? t + 3 : NT - 1, tv = (t + 2 < NT) ? t + 2 : NT - 1; ATT_LOAD_K(tk); ATT_LOAD_V(tv); }
;     ATT_BAR();
.LBB0_266:
	v_exp_f32_e32 v98, v98
	v_exp_f32_e32 v114, v114
	v_exp_f32_e32 v99, v99
	v_exp_f32_e32 v115, v115
	v_exp_f32_e32 v100, v100
	v_exp_f32_e32 v101, v101
	v_exp_f32_e32 v102, v102
	v_exp_f32_e32 v103, v103
	v_exp_f32_e32 v106, v106
	v_exp_f32_e32 v107, v107
	v_exp_f32_e32 v116, v116
	v_exp_f32_e32 v117, v117
	v_exp_f32_e32 v118, v118
	v_exp_f32_e32 v119, v119
	v_exp_f32_e32 v104, v104
	v_exp_f32_e32 v120, v120
	v_exp_f32_e32 v105, v105
	v_exp_f32_e32 v121, v121
	v_exp_f32_e32 v122, v122
	v_exp_f32_e32 v123, v123
	v_exp_f32_e32 v108, v108
	v_exp_f32_e32 v124, v124
	v_exp_f32_e32 v109, v109
	v_exp_f32_e32 v125, v125
	v_exp_f32_e32 v110, v110
	v_exp_f32_e32 v126, v126
	v_exp_f32_e32 v111, v111
	v_exp_f32_e32 v127, v127
	v_exp_f32_e32 v112, v112
	v_exp_f32_e32 v128, v128
	v_exp_f32_e32 v113, v113
	v_exp_f32_e32 v129, v129
	s_add_i32 s14, s92, 0
	v_cvt_pk_bf16_f32 v98, v98, v99
	v_cvt_pk_bf16_f32 v99, v100, v101
	v_cvt_pk_bf16_f32 v100, v102, v103
	v_cvt_pk_bf16_f32 v102, v106, v107
	v_cvt_pk_bf16_f32 v106, v114, v115
	v_add_u32_e32 v114, s14, v186
	s_add_i32 s14, s93, 0
	s_waitcnt vmcnt(3)
	ds_write_b128 v114, v[224:227] offset:49152
	s_waitcnt vmcnt(2)
	ds_write_b128 v114, v[228:231] offset:57856
	v_add_u32_e32 v114, s14, v189
	v_cvt_pk_bf16_f32 v101, v104, v105
	v_cvt_pk_bf16_f32 v103, v108, v109
	v_cvt_pk_bf16_f32 v104, v110, v111
	v_cvt_pk_bf16_f32 v105, v112, v113
	v_cvt_pk_bf16_f32 v107, v116, v117
	v_cvt_pk_bf16_f32 v108, v118, v119
	v_cvt_pk_bf16_f32 v109, v120, v121
	v_cvt_pk_bf16_f32 v110, v122, v123
	v_cvt_pk_bf16_f32 v111, v124, v125
	v_cvt_pk_bf16_f32 v112, v126, v127
	v_cvt_pk_bf16_f32 v113, v128, v129
	s_waitcnt vmcnt(1)
	ds_write_b128 v114, v[232:235]
	v_add_u32_e32 v114, s14, v190
	s_waitcnt vmcnt(0)
	ds_write_b128 v114, v[236:239]
	v_add_u32_e32 v172, s97, v131
	ds_read_b64_tr_b16 v[114:115], v172
	ds_read_b64_tr_b16 v[116:117], v172 offset:2048
	ds_read_b64_tr_b16 v[118:119], v172 offset:4096
	ds_read_b64_tr_b16 v[120:121], v172 offset:6144
	ds_read_b64_tr_b16 v[122:123], v172 offset:8192
	ds_read_b64_tr_b16 v[124:125], v172 offset:10240
	ds_read_b64_tr_b16 v[126:127], v172 offset:12288
	ds_read_b64_tr_b16 v[128:129], v172 offset:14336
	s_waitcnt lgkmcnt(8)
	s_barrier
	s_setprio 2
	s_waitcnt lgkmcnt(6)
	v_mfma_f32_32x32x16_bf16 v[18:33], v[98:101], v[114:117], v[18:33]
	ds_read_b64_tr_b16 v[168:169], v172 offset:512
	ds_read_b64_tr_b16 v[170:171], v172 offset:2560
	s_waitcnt lgkmcnt(6)
	v_mfma_f32_32x32x16_bf16 v[18:33], v[102:105], v[118:121], v[18:33]
	ds_read_b64_tr_b16 v[114:115], v172 offset:4608
	ds_read_b64_tr_b16 v[116:117], v172 offset:6656
	s_waitcnt lgkmcnt(6)
	v_mfma_f32_32x32x16_bf16 v[18:33], v[106:109], v[122:125], v[18:33]
	ds_read_b64_tr_b16 v[118:119], v172 offset:8704
	ds_read_b64_tr_b16 v[120:121], v172 offset:10752
	s_waitcnt lgkmcnt(6)
	v_mfma_f32_32x32x16_bf16 v[18:33], v[110:113], v[126:129], v[18:33]
	ds_read_b64_tr_b16 v[122:123], v172 offset:12800
	ds_read_b64_tr_b16 v[124:125], v172 offset:14848
	s_waitcnt lgkmcnt(6)
	v_mfma_f32_32x32x16_bf16 v[34:49], v[98:101], v[168:171], v[34:49]
	ds_read_b64_tr_b16 v[126:127], v172 offset:1024
	ds_read_b64_tr_b16 v[128:129], v172 offset:3072
	s_waitcnt lgkmcnt(6)
	v_mfma_f32_32x32x16_bf16 v[34:49], v[102:105], v[114:117], v[34:49]
	ds_read_b64_tr_b16 v[168:169], v172 offset:5120
	ds_read_b64_tr_b16 v[170:171], v172 offset:7168
	s_waitcnt lgkmcnt(6)
	v_mfma_f32_32x32x16_bf16 v[34:49], v[106:109], v[118:121], v[34:49]
	ds_read_b64_tr_b16 v[114:115], v172 offset:9216
	ds_read_b64_tr_b16 v[116:117], v172 offset:11264
	s_waitcnt lgkmcnt(6)
	v_mfma_f32_32x32x16_bf16 v[34:49], v[110:113], v[122:125], v[34:49]
	ds_read_b64_tr_b16 v[118:119], v172 offset:13312
	ds_read_b64_tr_b16 v[120:121], v172 offset:15360
	s_waitcnt lgkmcnt(6)
	v_mfma_f32_32x32x16_bf16 v[50:65], v[98:101], v[126:129], v[50:65]
	ds_read_b64_tr_b16 v[122:123], v172 offset:1536
	ds_read_b64_tr_b16 v[124:125], v172 offset:3584
	s_waitcnt lgkmcnt(6)
	v_mfma_f32_32x32x16_bf16 v[50:65], v[102:105], v[168:171], v[50:65]
	ds_read_b64_tr_b16 v[126:127], v172 offset:5632
	ds_read_b64_tr_b16 v[128:129], v172 offset:7680
	s_waitcnt lgkmcnt(6)
	v_mfma_f32_32x32x16_bf16 v[50:65], v[106:109], v[114:117], v[50:65]
	ds_read_b64_tr_b16 v[168:169], v172 offset:9728
	ds_read_b64_tr_b16 v[170:171], v172 offset:11776
	s_waitcnt lgkmcnt(6)
	v_mfma_f32_32x32x16_bf16 v[50:65], v[110:113], v[118:121], v[50:65]
	ds_read_b64_tr_b16 v[114:115], v172 offset:13824
	ds_read_b64_tr_b16 v[116:117], v172 offset:15872
	s_waitcnt lgkmcnt(6)
	v_mfma_f32_32x32x16_bf16 v[66:81], v[98:101], v[122:125], v[66:81]
	v_add_u32_e32 v193, s36, v192
	ds_read_b128 v[118:121], v193 offset:49152
	s_waitcnt lgkmcnt(5)
	v_mfma_f32_32x32x16_bf16 v[66:81], v[102:105], v[126:129], v[66:81]
	ds_read_b128 v[172:175], v193 offset:57856
	s_waitcnt lgkmcnt(4)
	v_mfma_f32_32x32x16_bf16 v[66:81], v[106:109], v[168:171], v[66:81]
	ds_read_b128 v[176:179], v193 offset:49184
	s_waitcnt lgkmcnt(3)
	v_mfma_f32_32x32x16_bf16 v[66:81], v[110:113], v[114:117], v[66:81]
	ds_read_b128 v[168:171], v193 offset:57888
	v_mfma_f32_4x4x4_16b_bf16 v[240:243], v[98:99], v[132:133], v[240:243]
	ds_read_b128 v[180:183], v193 offset:49216
	v_mfma_f32_4x4x4_16b_bf16 v[244:247], v[100:101], v[132:133], v[244:247]
	v_mfma_f32_4x4x4_16b_bf16 v[240:243], v[102:103], v[132:133], v[240:243]
	ds_read_b128 v[194:197], v193 offset:57920
	v_mfma_f32_4x4x4_16b_bf16 v[244:247], v[104:105], v[132:133], v[244:247]
	v_mfma_f32_4x4x4_16b_bf16 v[240:243], v[106:107], v[132:133], v[240:243]
	ds_read_b128 v[198:201], v193 offset:49248
	v_mfma_f32_4x4x4_16b_bf16 v[244:247], v[108:109], v[132:133], v[244:247]
	v_mfma_f32_4x4x4_16b_bf16 v[240:243], v[110:111], v[132:133], v[240:243]
	ds_read_b128 v[212:215], v193 offset:57952
	v_mfma_f32_4x4x4_16b_bf16 v[244:247], v[112:113], v[132:133], v[244:247]
	s_waitcnt lgkmcnt(7)
; #define ATT_SBAR() __builtin_amdgcn_sched_barrier(0)
; __device__ __forceinline__ unsigned cvtpk(float lo, float hi) { f32x2_t v = {lo, hi}; bf16x2_t b = __builtin_convertvector(v, bf16x2_t); return __builtin_bit_cast(unsigned, b); }
; #define ATT_LOAD_K(t) do { const unsigned so_ = (unsigned)(t) * (unsigned)(KVBLK * LDK * 2); sk0 = __builtin_bit_cast(bf16x8, __builtin_amdgcn_raw_buffer_load_b128(krs, koff, so_, 0)); \
;     if constexpr (DQK == 128) sk1 = __builtin_bit_cast(bf16x8, __builtin_amdgcn_raw_buffer_load_b128(krs, koff, so_ + (unsigned)(32 * LDK * 2), 0)); } while (0)
; #define ATT_LOAD_V(t) do { const unsigned so_ = (unsigned)(t) * (unsigned)(KVBLK * LDV * 2); sv0 = __builtin_bit_cast(bf16x8, __builtin_amdgcn_raw_buffer_load_b128(vrs, voff, so_, 0)); \
;     sv1 = __builtin_bit_cast(bf16x8, __builtin_amdgcn_raw_buffer_load_b128(vrs, voff, so_ + (unsigned)(32 * LDV * 2), 0)); } while (0)
; #define ATT_WRITE_K(so) do { *(bf16x8*)(K_lds + (so) + kswz<DQK>(kr, kc * 2)) = sk0; if constexpr (DQK == 128) *(bf16x8*)(K_lds + (so) + kswz<DQK>(32 + kr, kc * 2)) = sk1; } while (0)
;     ...
;   for (int t = 0; t + 1 < NT; ++t) {
;     if constexpr (ABL & 1) { u32x4 w0 = {cvtpk(p0[0], p0[1]), cvtpk(p0[2], p0[3]), cvtpk(p0[4], p0[5]), cvtpk(p0[6], p0[7])}, w1 = {cvtpk(p0[8], p0[9]), cvtpk(p0[10], p0[11]), cvtpk(p0[12], p0[13]), cvtpk(p0[14], p0[15])};
;         u32x4 w2 = {cvtpk(p1[0], p1[1]), cvtpk(p1[2], p1[3]), cvtpk(p1[4], p1[5]), cvtpk(p1[6], p1[7])}, w3 = {cvtpk(p1[8], p1[9]), cvtpk(p1[10], p1[11]), cvtpk(p1[12], p1[13]), cvtpk(p1[14], p1[15])};
;         pa0 = *reinterpret_cast<bf16x8*>(&w0); pa1 = *reinterpret_cast<bf16x8*>(&w1); pa2 = *reinterpret_cast<bf16x8*>(&w2); pa3 = *reinterpret_cast<bf16x8*>(&w3); }
;     else { ATT_SOFTMAX(t == 0); }
;     if constexpr (!(ABL & 4)) { ATT_WRITE_K(k2); ATT_WRITE_V(v1); }
;     ATT_SBAR();
; #pragma unroll
;     for (int ks = 0; ks < 4; ++ks) ATT_VPAIR(va, v0, 0, ks);
;     asm volatile("s_waitcnt lgkmcnt(8)" ::: "memory"); ATT_BAR();
;     ATT_XSECTION(true);
;     if constexpr (!(ABL & 4)) { const int tk = (t + 3 < NT) ? t + 3 : NT - 1, tv = (t + 2 < NT) ? t + 2 : NT - 1; ATT_LOAD_K(tk); ATT_LOAD_V(tv); }
;     ATT_BAR();
;     { const int tk_ = k0; k0 = k1; k1 = k2; k2 = tk_; const int tv_ = v0; v0 = v1; v1 = v2; v2 = tv_; }
	v_mfma_f32_32x32x16_bf16 v[98:113], v[118:121], v[136:139], v[82:97]
	ds_read_b128 v[216:219], v193 offset:49280
	s_waitcnt lgkmcnt(7)
	v_mfma_f32_32x32x16_bf16 v[114:129], v[172:175], v[136:139], v[82:97]
	ds_read_b128 v[220:223], v193 offset:57984
	s_waitcnt lgkmcnt(7)
	v_mfma_f32_32x32x16_bf16 v[98:113], v[176:179], v[140:143], v[98:113]
	ds_read_b128 v[172:175], v193 offset:49312
	s_waitcnt lgkmcnt(7)
	v_mfma_f32_32x32x16_bf16 v[114:129], v[168:171], v[140:143], v[114:129]
	ds_read_b128 v[176:179], v193 offset:58016
	s_waitcnt lgkmcnt(7)
	v_mfma_f32_32x32x16_bf16 v[98:113], v[180:183], v[144:147], v[98:113]
	ds_read_b128 v[168:171], v193 offset:49344
	s_waitcnt lgkmcnt(7)
	v_mfma_f32_32x32x16_bf16 v[114:129], v[194:197], v[144:147], v[114:129]
	ds_read_b128 v[180:183], v193 offset:58048
	s_waitcnt lgkmcnt(7)
	v_mfma_f32_32x32x16_bf16 v[98:113], v[198:201], v[148:151], v[98:113]
	ds_read_b128 v[194:197], v193 offset:49376
	s_waitcnt lgkmcnt(7)
	v_mfma_f32_32x32x16_bf16 v[114:129], v[212:215], v[148:151], v[114:129]
	ds_read_b128 v[198:201], v193 offset:58080
	s_waitcnt lgkmcnt(7)
	v_mfma_f32_32x32x16_bf16 v[98:113], v[216:219], v[152:155], v[98:113]
	s_min_u32 s14, s95, 0x7c
	s_lshl_b32 s14, s14, 15
	s_add_i32 s15, s14, 0x18000
	s_add_i32 s14, s14, 0x1c000
	buffer_load_dwordx4 v[224:227], v191, s[8:11], s15 offen
	s_waitcnt lgkmcnt(6)
	v_mfma_f32_32x32x16_bf16 v[114:129], v[220:223], v[152:155], v[114:129]
	buffer_load_dwordx4 v[228:231], v191, s[8:11], s14 offen
	s_waitcnt lgkmcnt(5)
	v_mfma_f32_32x32x16_bf16 v[98:113], v[172:175], v[156:159], v[98:113]
	s_add_i32 s18, s96, 0xffffc000
	s_mov_b32 s14, s10
	s_mov_b32 s15, s11
	buffer_load_dwordx4 v[232:235], v191, s[12:15], s18 offen
	s_waitcnt lgkmcnt(4)
	v_mfma_f32_32x32x16_bf16 v[114:129], v[176:179], v[156:159], v[114:129]
	buffer_load_dwordx4 v[236:239], v191, s[12:15], s96 offen
	s_waitcnt lgkmcnt(3)
	v_mfma_f32_32x32x16_bf16 v[98:113], v[168:171], v[160:163], v[98:113]
	s_waitcnt lgkmcnt(2)
	v_mfma_f32_32x32x16_bf16 v[114:129], v[180:183], v[160:163], v[114:129]
	s_waitcnt lgkmcnt(1)
	v_mfma_f32_32x32x16_bf16 v[98:113], v[194:197], v[164:167], v[98:113]
	s_waitcnt lgkmcnt(0)
	v_mfma_f32_32x32x16_bf16 v[114:129], v[198:201], v[164:167], v[114:129]
	s_setprio 0
	s_barrier
	s_add_i32 s96, s96, 0x8000
	s_add_i32 s95, s95, 1
	s_cmpk_eq_i32 s95, 0x7e
	s_cbranch_scc1 .LBB0_274
	s_mov_b32 s14, s92
	s_mov_b32 s92, s94
	s_mov_b32 s94, s36
	s_mov_b32 s15, s93
	s_mov_b32 s93, s91
	s_mov_b32 s91, s97
	s_branch .LBB0_265
.LBB0_268:
	v_mov_b32_e32 v194, v193
	s_nop 1
	v_permlane32_swap_b32_e32 v193, v194
	v_max3_f32 v193, v193, v194, 0
	v_exp_f32_e64 v194, -v193
	s_nop 4
	s_nop 0
	v_cmp_gt_f32_e32 vcc, 1.0, v194
	s_cbranch_vccz .LBB0_272
	v_mul_f32_dpp v240, v194, v240 quad_perm:[0,0,0,0] row_mask:0xf bank_mask:0xf
	v_mul_f32_dpp v241, v194, v241 quad_perm:[1,1,1,1] row_mask:0xf bank_mask:0xf
	v_mul_f32_dpp v242, v194, v242 quad_perm:[2,2,2,2] row_mask:0xf bank_mask:0xf
	v_mul_f32_dpp v243, v194, v243 quad_perm:[3,3,3,3] row_mask:0xf bank_mask:0xf
	v_mul_f32_dpp v244, v194, v244 quad_perm:[0,0,0,0] row_mask:0xf bank_mask:0xf
	v_mul_f32_dpp v245, v194, v245 quad_perm:[1,1,1,1] row_mask:0xf bank_mask:0xf
	v_mul_f32_dpp v246, v194, v246 quad_perm:[2,2,2,2] row_mask:0xf bank_mask:0xf
	v_mul_f32_dpp v247, v194, v247 quad_perm:[3,3,3,3] row_mask:0xf bank_mask:0xf
	s_and_saveexec_b64 s[14:15], s[4:5]
	ds_write_b32 v187, v194
	s_or_b64 exec, exec, s[14:15]
	s_waitcnt lgkmcnt(0)
	v_add_u32_e32 v216, s90, v184
	ds_read_b128 v[194:197], v216 offset:96
	ds_read_b128 v[198:201], v216 offset:64
	ds_read_b128 v[212:215], v216 offset:32
	ds_read_b128 v[216:219], v216
	s_waitcnt lgkmcnt(3)
	v_pk_mul_f32 v[30:31], v[30:31], v[194:195]
	s_waitcnt lgkmcnt(2)
	v_pk_mul_f32 v[26:27], v[26:27], v[198:199]
	s_waitcnt lgkmcnt(1)
	v_pk_mul_f32 v[22:23], v[22:23], v[212:213]
	v_pk_mul_f32 v[32:33], v[32:33], v[196:197]
	v_pk_mul_f32 v[28:29], v[28:29], v[200:201]
	v_pk_mul_f32 v[24:25], v[24:25], v[214:215]
	s_waitcnt lgkmcnt(0)
	v_pk_mul_f32 v[20:21], v[20:21], v[218:219]
	v_pk_mul_f32 v[18:19], v[18:19], v[216:217]
	v_pk_mul_f32 v[46:47], v[46:47], v[194:195]
	v_pk_mul_f32 v[42:43], v[42:43], v[198:199]
	v_pk_mul_f32 v[38:39], v[38:39], v[212:213]
	v_pk_mul_f32 v[48:49], v[48:49], v[196:197]
	v_pk_mul_f32 v[44:45], v[44:45], v[200:201]
	v_pk_mul_f32 v[40:41], v[40:41], v[214:215]
	v_pk_mul_f32 v[36:37], v[36:37], v[218:219]
	v_pk_mul_f32 v[34:35], v[34:35], v[216:217]
	v_pk_mul_f32 v[62:63], v[62:63], v[194:195]
	v_pk_mul_f32 v[58:59], v[58:59], v[198:199]
	v_pk_mul_f32 v[54:55], v[54:55], v[212:213]
	v_pk_mul_f32 v[64:65], v[64:65], v[196:197]
	v_pk_mul_f32 v[60:61], v[60:61], v[200:201]
	v_pk_mul_f32 v[56:57], v[56:57], v[214:215]
	v_pk_mul_f32 v[52:53], v[52:53], v[218:219]
	v_pk_mul_f32 v[50:51], v[50:51], v[216:217]
	v_pk_mul_f32 v[78:79], v[78:79], v[194:195]
	v_pk_mul_f32 v[74:75], v[74:75], v[198:199]
	v_pk_mul_f32 v[70:71], v[70:71], v[212:213]
	v_pk_mul_f32 v[80:81], v[80:81], v[196:197]
	v_pk_mul_f32 v[76:77], v[76:77], v[200:201]
	v_pk_mul_f32 v[72:73], v[72:73], v[214:215]
	v_pk_mul_f32 v[68:69], v[68:69], v[218:219]
	v_pk_mul_f32 v[66:67], v[66:67], v[216:217]

; #define ATT_SBAR() __builtin_amdgcn_sched_barrier(0)
; __device__ __forceinline__ unsigned cvtpk(float lo, float hi) { f32x2_t v = {lo, hi}; bf16x2_t b = __builtin_convertvector(v, bf16x2_t); return __builtin_bit_cast(unsigned, b); }
; #define ATT_PK4(P, BASE, OUT) do { u32x4 w = {cvtpk(P[BASE + 0], P[BASE + 1]), cvtpk(P[BASE + 2], P[BASE + 3]), cvtpk(P[BASE + 4], P[BASE + 5]), cvtpk(P[BASE + 6], P[BASE + 7])}; \
;     OUT = *reinterpret_cast<bf16x8*>(&w); } while (0)
; #define ATT_LOAD_K(t) do { const unsigned so_ = (unsigned)(t) * (unsigned)(KVBLK * LDK * 2); sk0 = __builtin_bit_cast(bf16x8, __builtin_amdgcn_raw_buffer_load_b128(krs, koff, so_, 0)); \
;     if constexpr (DQK == 128) sk1 = __builtin_bit_cast(bf16x8, __builtin_amdgcn_raw_buffer_load_b128(krs, koff, so_ + (unsigned)(32 * LDK * 2), 0)); } while (0)
; __device__ __forceinline__ void softmax_exp_pack(f32x16& p0, f32x16& p1, bf16x8& pa0, bf16x8& pa1, bf16x8& pa2, bf16x8& pa3) {
; #pragma unroll
;   for (int r = 0; r < 16; ++r) { p0[r] = __builtin_amdgcn_exp2f(p0[r]); p1[r] = __builtin_amdgcn_exp2f(p1[r]); }
;     ...
;   ATT_PK4(p0, 0, pa0); ATT_PK4(p0, 8, pa1); ATT_PK4(p1, 0, pa2); ATT_PK4(p1, 8, pa3);
;     ...
; }
;     ...
;   for (int t = 0; t + 1 < NT; ++t) {
;     if constexpr (ABL & 1) { u32x4 w0 = {cvtpk(p0[0], p0[1]), cvtpk(p0[2], p0[3]), cvtpk(p0[4], p0[5]), cvtpk(p0[6], p0[7])}, w1 = {cvtpk(p0[8], p0[9]), cvtpk(p0[10], p0[11]), cvtpk(p0[12], p0[13]), cvtpk(p0[14], p0[15])};
;         u32x4 w2 = {cvtpk(p1[0], p1[1]), cvtpk(p1[2], p1[3]), cvtpk(p1[4], p1[5]), cvtpk(p1[6], p1[7])}, w3 = {cvtpk(p1[8], p1[9]), cvtpk(p1[10], p1[11]), cvtpk(p1[12], p1[13]), cvtpk(p1[14], p1[15])};
;         pa0 = *reinterpret_cast<bf16x8*>(&w0); pa1 = *reinterpret_cast<bf16x8*>(&w1); pa2 = *reinterpret_cast<bf16x8*>(&w2); pa3 = *reinterpret_cast<bf16x8*>(&w3); }
;     else { ATT_SOFTMAX(t == 0); }
;     if constexpr (!(ABL & 4)) { ATT_WRITE_K(k2); ATT_WRITE_V(v1); }
;     ATT_SBAR();
; #pragma unroll
;     for (int ks = 0; ks < 4; ++ks) ATT_VPAIR(va, v0, 0, ks);
;     asm volatile("s_waitcnt lgkmcnt(8)" ::: "memory"); ATT_BAR();
;     ATT_XSECTION(true);
;     if constexpr (!(ABL & 4)) { const int tk = (t + 3 < NT) ? t + 3 : NT - 1, tv = (t + 2 < NT) ? t + 2 : NT - 1; ATT_LOAD_K(tk); ATT_LOAD_V(tv); }
;     ATT_BAR();
;     { const int tk_ = k0; k0 = k1; k1 = k2; k2 = tk_; const int tv_ = v0; v0 = v1; v1 = v2; v2 = tv_; }
.LBB0_275:
	v_exp_f32_e32 v98, v98
	v_exp_f32_e32 v114, v114
	v_exp_f32_e32 v99, v99
	v_exp_f32_e32 v115, v115
	v_exp_f32_e32 v100, v100
	v_exp_f32_e32 v101, v101
	v_exp_f32_e32 v102, v102
	v_exp_f32_e32 v103, v103
	v_exp_f32_e32 v106, v106
	v_exp_f32_e32 v107, v107
	v_exp_f32_e32 v116, v116
	v_exp_f32_e32 v117, v117
	v_exp_f32_e32 v118, v118
	v_exp_f32_e32 v119, v119
	v_exp_f32_e32 v104, v104
	v_exp_f32_e32 v120, v120
	v_exp_f32_e32 v105, v105
	v_exp_f32_e32 v121, v121
	v_exp_f32_e32 v122, v122
	v_exp_f32_e32 v123, v123
	v_exp_f32_e32 v108, v108
	v_exp_f32_e32 v124, v124
	v_exp_f32_e32 v109, v109
	v_exp_f32_e32 v125, v125
	v_exp_f32_e32 v110, v110
	v_exp_f32_e32 v126, v126
	v_exp_f32_e32 v111, v111
	v_exp_f32_e32 v127, v127
	v_exp_f32_e32 v112, v112
	v_exp_f32_e32 v128, v128
	v_exp_f32_e32 v113, v113
	v_exp_f32_e32 v129, v129
	s_add_i32 s8, s94, 0
	v_cvt_pk_bf16_f32 v98, v98, v99
	v_cvt_pk_bf16_f32 v99, v100, v101
	v_cvt_pk_bf16_f32 v100, v102, v103
	v_cvt_pk_bf16_f32 v102, v106, v107
	v_cvt_pk_bf16_f32 v106, v114, v115
	v_add_u32_e32 v114, s8, v186
	s_add_i32 s8, s91, 0
	s_waitcnt vmcnt(3)
	ds_write_b128 v114, v[224:227] offset:49152
	s_waitcnt vmcnt(2)
	ds_write_b128 v114, v[228:231] offset:57856
	v_add_u32_e32 v114, s8, v189
	v_cvt_pk_bf16_f32 v101, v104, v105
	v_cvt_pk_bf16_f32 v103, v108, v109
	v_cvt_pk_bf16_f32 v104, v110, v111
	v_cvt_pk_bf16_f32 v105, v112, v113
	v_cvt_pk_bf16_f32 v107, v116, v117
	v_cvt_pk_bf16_f32 v108, v118, v119
	v_cvt_pk_bf16_f32 v109, v120, v121
	v_cvt_pk_bf16_f32 v110, v122, v123
	v_cvt_pk_bf16_f32 v111, v124, v125
	v_cvt_pk_bf16_f32 v112, v126, v127
	v_cvt_pk_bf16_f32 v113, v128, v129
	s_waitcnt vmcnt(1)
	ds_write_b128 v114, v[232:235]
	v_add_u32_e32 v114, s8, v190
	s_waitcnt vmcnt(0)
	ds_write_b128 v114, v[236:239]
	v_add_u32_e32 v172, s93, v131
	ds_read_b64_tr_b16 v[114:115], v172
	ds_read_b64_tr_b16 v[116:117], v172 offset:2048
	ds_read_b64_tr_b16 v[118:119], v172 offset:4096
	ds_read_b64_tr_b16 v[120:121], v172 offset:6144
	ds_read_b64_tr_b16 v[122:123], v172 offset:8192
	ds_read_b64_tr_b16 v[124:125], v172 offset:10240
	ds_read_b64_tr_b16 v[126:127], v172 offset:12288
	ds_read_b64_tr_b16 v[128:129], v172 offset:14336
	s_waitcnt lgkmcnt(8)
	s_barrier
	s_setprio 2
	s_waitcnt lgkmcnt(6)
	v_mfma_f32_32x32x16_bf16 v[18:33], v[98:101], v[114:117], v[18:33]
	ds_read_b64_tr_b16 v[168:169], v172 offset:512
	ds_read_b64_tr_b16 v[170:171], v172 offset:2560
	s_waitcnt lgkmcnt(6)
	v_mfma_f32_32x32x16_bf16 v[18:33], v[102:105], v[118:121], v[18:33]
	ds_read_b64_tr_b16 v[114:115], v172 offset:4608
	ds_read_b64_tr_b16 v[116:117], v172 offset:6656
	s_waitcnt lgkmcnt(6)
	v_mfma_f32_32x32x16_bf16 v[18:33], v[106:109], v[122:125], v[18:33]
	ds_read_b64_tr_b16 v[118:119], v172 offset:8704
	ds_read_b64_tr_b16 v[120:121], v172 offset:10752
	s_waitcnt lgkmcnt(6)
	v_mfma_f32_32x32x16_bf16 v[18:33], v[110:113], v[126:129], v[18:33]
	ds_read_b64_tr_b16 v[122:123], v172 offset:12800
	ds_read_b64_tr_b16 v[124:125], v172 offset:14848
	s_waitcnt lgkmcnt(6)
	v_mfma_f32_32x32x16_bf16 v[34:49], v[98:101], v[168:171], v[34:49]
	ds_read_b64_tr_b16 v[126:127], v172 offset:1024
	ds_read_b64_tr_b16 v[128:129], v172 offset:3072
	s_waitcnt lgkmcnt(6)
	v_mfma_f32_32x32x16_bf16 v[34:49], v[102:105], v[114:117], v[34:49]
	ds_read_b64_tr_b16 v[168:169], v172 offset:5120
	ds_read_b64_tr_b16 v[170:171], v172 offset:7168
	s_waitcnt lgkmcnt(6)
	v_mfma_f32_32x32x16_bf16 v[34:49], v[106:109], v[118:121], v[34:49]
	ds_read_b64_tr_b16 v[114:115], v172 offset:9216
	ds_read_b64_tr_b16 v[116:117], v172 offset:11264
	s_waitcnt lgkmcnt(6)
	v_mfma_f32_32x32x16_bf16 v[34:49], v[110:113], v[122:125], v[34:49]
	ds_read_b64_tr_b16 v[118:119], v172 offset:13312
	ds_read_b64_tr_b16 v[120:121], v172 offset:15360
	s_waitcnt lgkmcnt(6)
	v_mfma_f32_32x32x16_bf16 v[50:65], v[98:101], v[126:129], v[50:65]
	ds_read_b64_tr_b16 v[122:123], v172 offset:1536
	ds_read_b64_tr_b16 v[124:125], v172 offset:3584
	s_waitcnt lgkmcnt(6)
	v_mfma_f32_32x32x16_bf16 v[50:65], v[102:105], v[168:171], v[50:65]
	ds_read_b64_tr_b16 v[126:127], v172 offset:5632
	ds_read_b64_tr_b16 v[128:129], v172 offset:7680
	s_waitcnt lgkmcnt(6)
	v_mfma_f32_32x32x16_bf16 v[50:65], v[106:109], v[114:117], v[50:65]
	ds_read_b64_tr_b16 v[168:169], v172 offset:9728
	ds_read_b64_tr_b16 v[170:171], v172 offset:11776
	s_waitcnt lgkmcnt(6)
	v_mfma_f32_32x32x16_bf16 v[50:65], v[110:113], v[118:121], v[50:65]
	ds_read_b64_tr_b16 v[114:115], v172 offset:13824
	ds_read_b64_tr_b16 v[116:117], v172 offset:15872
	s_waitcnt lgkmcnt(6)
	v_mfma_f32_32x32x16_bf16 v[66:81], v[98:101], v[122:125], v[66:81]
	v_add3_u32 v186, v188, s92, v184
	ds_read_b128 v[118:121], v186 offset:49152
	s_waitcnt lgkmcnt(5)
	v_mfma_f32_32x32x16_bf16 v[66:81], v[102:105], v[126:129], v[66:81]
	ds_read_b128 v[122:125], v186 offset:57856
	s_waitcnt lgkmcnt(4)
	v_mfma_f32_32x32x16_bf16 v[66:81], v[106:109], v[168:171], v[66:81]
	ds_read_b128 v[126:129], v186 offset:49184
	s_waitcnt lgkmcnt(3)
	v_mfma_f32_32x32x16_bf16 v[66:81], v[110:113], v[114:117], v[66:81]
	ds_read_b128 v[168:171], v186 offset:57888
	v_mfma_f32_4x4x4_16b_bf16 v[240:243], v[98:99], v[132:133], v[240:243]
	ds_read_b128 v[114:117], v186 offset:49216
	v_mfma_f32_4x4x4_16b_bf16 v[244:247], v[100:101], v[132:133], v[244:247]
	v_mfma_f32_4x4x4_16b_bf16 v[240:243], v[102:103], v[132:133], v[240:243]
	ds_read_b128 v[172:175], v186 offset:57920
	v_mfma_f32_4x4x4_16b_bf16 v[244:247], v[104:105], v[132:133], v[244:247]
	v_mfma_f32_4x4x4_16b_bf16 v[240:243], v[106:107], v[132:133], v[240:243]
	ds_read_b128 v[176:179], v186 offset:49248
	v_mfma_f32_4x4x4_16b_bf16 v[244:247], v[108:109], v[132:133], v[244:247]
	v_mfma_f32_4x4x4_16b_bf16 v[240:243], v[110:111], v[132:133], v[240:243]
	ds_read_b128 v[180:183], v186 offset:57952
	v_mfma_f32_4x4x4_16b_bf16 v[244:247], v[112:113], v[132:133], v[244:247]
	s_waitcnt lgkmcnt(7)
; #define ATT_SBAR() __builtin_amdgcn_sched_barrier(0)
; __device__ __forceinline__ unsigned cvtpk(float lo, float hi) { f32x2_t v = {lo, hi}; bf16x2_t b = __builtin_convertvector(v, bf16x2_t); return __builtin_bit_cast(unsigned, b); }
; #define ATT_LOAD_K(t) do { const unsigned so_ = (unsigned)(t) * (unsigned)(KVBLK * LDK * 2); sk0 = __builtin_bit_cast(bf16x8, __builtin_amdgcn_raw_buffer_load_b128(krs, koff, so_, 0)); \
;     if constexpr (DQK == 128) sk1 = __builtin_bit_cast(bf16x8, __builtin_amdgcn_raw_buffer_load_b128(krs, koff, so_ + (unsigned)(32 * LDK * 2), 0)); } while (0)
; #define ATT_LOAD_V(t) do { const unsigned so_ = (unsigned)(t) * (unsigned)(KVBLK * LDV * 2); sv0 = __builtin_bit_cast(bf16x8, __builtin_amdgcn_raw_buffer_load_b128(vrs, voff, so_, 0)); \
;     sv1 = __builtin_bit_cast(bf16x8, __builtin_amdgcn_raw_buffer_load_b128(vrs, voff, so_ + (unsigned)(32 * LDV * 2), 0)); } while (0)
; #define ATT_BAR() do { ATT_SBAR(); asm volatile("s_barrier" ::: "memory"); ATT_SBAR(); } while (0)
;     ...
;   for (int t = 0; t + 1 < NT; ++t) {
;     if constexpr (ABL & 1) { u32x4 w0 = {cvtpk(p0[0], p0[1]), cvtpk(p0[2], p0[3]), cvtpk(p0[4], p0[5]), cvtpk(p0[6], p0[7])}, w1 = {cvtpk(p0[8], p0[9]), cvtpk(p0[10], p0[11]), cvtpk(p0[12], p0[13]), cvtpk(p0[14], p0[15])};
;         u32x4 w2 = {cvtpk(p1[0], p1[1]), cvtpk(p1[2], p1[3]), cvtpk(p1[4], p1[5]), cvtpk(p1[6], p1[7])}, w3 = {cvtpk(p1[8], p1[9]), cvtpk(p1[10], p1[11]), cvtpk(p1[12], p1[13]), cvtpk(p1[14], p1[15])};
;         pa0 = *reinterpret_cast<bf16x8*>(&w0); pa1 = *reinterpret_cast<bf16x8*>(&w1); pa2 = *reinterpret_cast<bf16x8*>(&w2); pa3 = *reinterpret_cast<bf16x8*>(&w3); }
;     else { ATT_SOFTMAX(t == 0); }
;     if constexpr (!(ABL & 4)) { ATT_WRITE_K(k2); ATT_WRITE_V(v1); }
;     ATT_SBAR();
; #pragma unroll
;     for (int ks = 0; ks < 4; ++ks) ATT_VPAIR(va, v0, 0, ks);
;     asm volatile("s_waitcnt lgkmcnt(8)" ::: "memory"); ATT_BAR();
;     ATT_XSECTION(true);
;     if constexpr (!(ABL & 4)) { const int tk = (t + 3 < NT) ? t + 3 : NT - 1, tv = (t + 2 < NT) ? t + 2 : NT - 1; ATT_LOAD_K(tk); ATT_LOAD_V(tv); }
;     ATT_BAR();
;     { const int tk_ = k0; k0 = k1; k1 = k2; k2 = tk_; const int tv_ = v0; v0 = v1; v1 = v2; v2 = tv_; }
;   }
;   ATT_SOFTMAX(false);
; #pragma unroll
;   for (int ks = 0; ks < 4; ++ks) ATT_VPAIR(va, v0, 0, ks);
;   asm volatile("s_waitcnt lgkmcnt(0)" ::: "memory"); ATT_BAR();
	v_mfma_f32_32x32x16_bf16 v[98:113], v[118:121], v[136:139], v[82:97]
	ds_read_b128 v[188:191], v186 offset:49280
	s_waitcnt lgkmcnt(7)
	v_mfma_f32_32x32x16_bf16 v[82:97], v[122:125], v[136:139], v[82:97]
	ds_read_b128 v[118:121], v186 offset:57984
	s_waitcnt lgkmcnt(7)
	v_mfma_f32_32x32x16_bf16 v[98:113], v[126:129], v[140:143], v[98:113]
	ds_read_b128 v[122:125], v186 offset:49312
	s_waitcnt lgkmcnt(7)
	v_mfma_f32_32x32x16_bf16 v[82:97], v[168:171], v[140:143], v[82:97]
	ds_read_b128 v[126:129], v186 offset:58016
	s_waitcnt lgkmcnt(7)
	v_mfma_f32_32x32x16_bf16 v[98:113], v[114:117], v[144:147], v[98:113]
	ds_read_b128 v[136:139], v186 offset:49344
	s_waitcnt lgkmcnt(7)
	v_mfma_f32_32x32x16_bf16 v[82:97], v[172:175], v[144:147], v[82:97]
	ds_read_b128 v[114:117], v186 offset:58048
	s_waitcnt lgkmcnt(7)
	v_mfma_f32_32x32x16_bf16 v[98:113], v[176:179], v[148:151], v[98:113]
	ds_read_b128 v[140:143], v186 offset:49376
	s_waitcnt lgkmcnt(7)
	v_mfma_f32_32x32x16_bf16 v[82:97], v[180:183], v[148:151], v[82:97]
	ds_read_b128 v[144:147], v186 offset:58080
	s_waitcnt lgkmcnt(7)
	v_mfma_f32_32x32x16_bf16 v[98:113], v[188:191], v[152:155], v[98:113]
	s_waitcnt lgkmcnt(6)
	v_mfma_f32_32x32x16_bf16 v[82:97], v[118:121], v[152:155], v[82:97]
	s_waitcnt lgkmcnt(5)
	v_mfma_f32_32x32x16_bf16 v[98:113], v[122:125], v[156:159], v[98:113]
	s_waitcnt lgkmcnt(4)
	v_mfma_f32_32x32x16_bf16 v[82:97], v[126:129], v[156:159], v[82:97]
	s_waitcnt lgkmcnt(3)
	v_mfma_f32_32x32x16_bf16 v[98:113], v[136:139], v[160:163], v[98:113]
	s_waitcnt lgkmcnt(2)
	v_mfma_f32_32x32x16_bf16 v[82:97], v[114:117], v[160:163], v[82:97]
	s_waitcnt lgkmcnt(1)
	v_mfma_f32_32x32x16_bf16 v[98:113], v[140:143], v[164:167], v[98:113]
	s_waitcnt lgkmcnt(0)
	v_mfma_f32_32x32x16_bf16 v[82:97], v[144:147], v[164:167], v[82:97]
	s_setprio 0
	s_barrier
	s_nop 10
	v_add_f32_e32 v114, 0, v82
	v_max3_f32 v115, v114, v98, v99
	v_max3_f32 v115, v115, v100, v101
	v_max3_f32 v115, v115, v102, v103
	v_max3_f32 v115, v115, v104, v105
	v_max3_f32 v115, v115, v106, v107
	v_max3_f32 v115, v115, v108, v109
	v_max3_f32 v115, v115, v110, v111
	v_max3_f32 v115, v115, v112, v113
	s_nop 0
	v_max3_f32 v114, v115, v83, v84
	v_max3_f32 v114, v114, v85, v86
	v_max3_f32 v114, v114, v87, v88
	v_max3_f32 v114, v114, v89, v90
	v_max3_f32 v114, v114, v91, v92
	v_max3_f32 v114, v114, v93, v94
	v_max3_f32 v114, v114, v95, v96
	v_max_f32 v114, v114, v97
	s_nop 0
	v_cmp_ge_f32_e32 vcc, s60, v114
	s_cmp_lg_u64 vcc, exec
	s_cbranch_scc1 .LBB0_314
.LBB0_276:
	v_exp_f32_e32 v98, v98
	v_exp_f32_e32 v114, v82
	v_exp_f32_e32 v82, v99
	v_exp_f32_e32 v99, v83
	v_exp_f32_e32 v83, v100
	v_exp_f32_e32 v100, v84
	v_exp_f32_e32 v84, v101
	v_exp_f32_e32 v101, v85
	v_exp_f32_e32 v85, v102
	v_exp_f32_e32 v102, v86
	v_exp_f32_e32 v86, v103
	v_exp_f32_e32 v103, v87
	v_exp_f32_e32 v87, v104
	v_exp_f32_e32 v104, v88
	v_exp_f32_e32 v88, v105
	v_exp_f32_e32 v105, v89
	v_exp_f32_e32 v89, v106
	v_exp_f32_e32 v106, v90
	v_exp_f32_e32 v90, v107
	v_exp_f32_e32 v107, v91
	v_exp_f32_e32 v91, v108
	v_exp_f32_e32 v108, v92
	v_exp_f32_e32 v92, v109
	v_exp_f32_e32 v109, v93
	v_exp_f32_e32 v93, v110
	v_exp_f32_e32 v110, v94
	v_exp_f32_e32 v94, v111
	v_exp_f32_e32 v111, v95
	v_exp_f32_e32 v95, v112
	v_exp_f32_e32 v112, v96
	v_exp_f32_e32 v96, v113
	v_exp_f32_e32 v97, v97
	v_add_u32_e32 v118, s91, v131
	v_cvt_pk_bf16_f32 v82, v98, v82
	v_cvt_pk_bf16_f32 v83, v83, v84
	v_cvt_pk_bf16_f32 v84, v85, v86
	v_cvt_pk_bf16_f32 v85, v87, v88
	v_cvt_pk_bf16_f32 v86, v89, v90
	v_cvt_pk_bf16_f32 v87, v91, v92
	v_cvt_pk_bf16_f32 v88, v93, v94
	v_cvt_pk_bf16_f32 v89, v95, v96
	v_cvt_pk_bf16_f32 v90, v114, v99
	v_cvt_pk_bf16_f32 v91, v100, v101
	v_cvt_pk_bf16_f32 v92, v102, v103
	v_cvt_pk_bf16_f32 v93, v104, v105
	v_cvt_pk_bf16_f32 v94, v106, v107
	v_cvt_pk_bf16_f32 v95, v108, v109
	v_cvt_pk_bf16_f32 v96, v110, v111
	v_cvt_pk_bf16_f32 v97, v112, v97
	ds_read_b64_tr_b16 v[98:99], v118
	ds_read_b64_tr_b16 v[100:101], v118 offset:2048
	ds_read_b64_tr_b16 v[102:103], v118 offset:4096
	ds_read_b64_tr_b16 v[104:105], v118 offset:6144
	ds_read_b64_tr_b16 v[106:107], v118 offset:8192
	ds_read_b64_tr_b16 v[108:109], v118 offset:10240
	ds_read_b64_tr_b16 v[110:111], v118 offset:12288
	ds_read_b64_tr_b16 v[112:113], v118 offset:14336
	s_waitcnt lgkmcnt(0)
	s_barrier
; __device__ __forceinline__ int crow(int r, int hi) { return (r & 3) + 8 * (r >> 2) + 4 * hi; }
; #define ATT_BAR() do { ATT_SBAR(); asm volatile("s_barrier" ::: "memory"); ATT_SBAR(); } while (0)
; __device__ __forceinline__ unsigned f2bf(float f) { unsigned u = __builtin_bit_cast(unsigned, f); return (u + 0x7fffu + ((u >> 16) & 1u)) >> 16; }
;     ...
;   ATT_XSECTION(false);
;   ATT_BAR();
;   if (grp == 0) ATT_BAR();
; #pragma unroll
;   for (int r = 0; r < 16; ++r) rli[r] = __builtin_amdgcn_rcpf(lacc[r]);
;     ...
;     att::bf16* Ow = Obase + ((size_t)b * SEQ + (size_t)qb * 256 + wave_ * 32) * 2048 + h * 128;
; #pragma unroll
;     for (int r = 0; r < 16; ++r) { const int orow = crow(r, hi);
; #pragma unroll
;         for (int d0 = 0; d0 < 4; ++d0) Ow[(size_t)orow * 2048 + d0 * 32 + r32] = (att::bf16)f2bf(o[d0][r] * rli[r]); }
	s_setprio 2
	s_waitcnt lgkmcnt(6)
	v_mfma_f32_32x32x16_bf16 v[18:33], v[82:85], v[98:101], v[18:33]
	ds_read_b64_tr_b16 v[114:115], v118 offset:512
	ds_read_b64_tr_b16 v[116:117], v118 offset:2560
	s_waitcnt lgkmcnt(6)
	v_mfma_f32_32x32x16_bf16 v[18:33], v[86:89], v[102:105], v[18:33]
	ds_read_b64_tr_b16 v[98:99], v118 offset:4608
	ds_read_b64_tr_b16 v[100:101], v118 offset:6656
	s_waitcnt lgkmcnt(6)
	v_mfma_f32_32x32x16_bf16 v[18:33], v[90:93], v[106:109], v[18:33]
	ds_read_b64_tr_b16 v[102:103], v118 offset:8704
	ds_read_b64_tr_b16 v[104:105], v118 offset:10752
	s_waitcnt lgkmcnt(6)
	v_mfma_f32_32x32x16_bf16 v[18:33], v[94:97], v[110:113], v[18:33]
	ds_read_b64_tr_b16 v[106:107], v118 offset:12800
	ds_read_b64_tr_b16 v[108:109], v118 offset:14848
	s_waitcnt lgkmcnt(6)
	v_mfma_f32_32x32x16_bf16 v[34:49], v[82:85], v[114:117], v[34:49]
	ds_read_b64_tr_b16 v[110:111], v118 offset:1024
	ds_read_b64_tr_b16 v[112:113], v118 offset:3072
	s_waitcnt lgkmcnt(6)
	v_mfma_f32_32x32x16_bf16 v[34:49], v[86:89], v[98:101], v[34:49]
	ds_read_b64_tr_b16 v[114:115], v118 offset:5120
	ds_read_b64_tr_b16 v[116:117], v118 offset:7168
	s_waitcnt lgkmcnt(6)
	v_mfma_f32_32x32x16_bf16 v[34:49], v[90:93], v[102:105], v[34:49]
	ds_read_b64_tr_b16 v[98:99], v118 offset:9216
	ds_read_b64_tr_b16 v[100:101], v118 offset:11264
	s_waitcnt lgkmcnt(6)
	v_mfma_f32_32x32x16_bf16 v[34:49], v[94:97], v[106:109], v[34:49]
	ds_read_b64_tr_b16 v[102:103], v118 offset:13312
	ds_read_b64_tr_b16 v[104:105], v118 offset:15360
	s_waitcnt lgkmcnt(6)
	v_mfma_f32_32x32x16_bf16 v[50:65], v[82:85], v[110:113], v[50:65]
	ds_read_b64_tr_b16 v[106:107], v118 offset:1536
	ds_read_b64_tr_b16 v[108:109], v118 offset:3584
	s_waitcnt lgkmcnt(6)
	v_mfma_f32_32x32x16_bf16 v[50:65], v[86:89], v[114:117], v[50:65]
	ds_read_b64_tr_b16 v[110:111], v118 offset:5632
	ds_read_b64_tr_b16 v[112:113], v118 offset:7680
	s_waitcnt lgkmcnt(6)
	v_mfma_f32_32x32x16_bf16 v[50:65], v[90:93], v[98:101], v[50:65]
	ds_read_b64_tr_b16 v[114:115], v118 offset:9728
	ds_read_b64_tr_b16 v[116:117], v118 offset:11776
	s_waitcnt lgkmcnt(6)
	v_mfma_f32_32x32x16_bf16 v[50:65], v[94:97], v[102:105], v[50:65]
	ds_read_b64_tr_b16 v[98:99], v118 offset:13824
	ds_read_b64_tr_b16 v[100:101], v118 offset:15872
	s_waitcnt lgkmcnt(6)
	v_mfma_f32_32x32x16_bf16 v[66:81], v[82:85], v[106:109], v[66:81]
	s_waitcnt lgkmcnt(4)
	v_mfma_f32_32x32x16_bf16 v[66:81], v[86:89], v[110:113], v[66:81]
	s_waitcnt lgkmcnt(2)
	v_mfma_f32_32x32x16_bf16 v[66:81], v[90:93], v[114:117], v[66:81]
	s_waitcnt lgkmcnt(0)
	v_mfma_f32_32x32x16_bf16 v[66:81], v[94:97], v[98:101], v[66:81]
	v_mfma_f32_4x4x4_16b_bf16 v[240:243], v[82:83], v[132:133], v[240:243]
	v_mfma_f32_4x4x4_16b_bf16 v[244:247], v[84:85], v[132:133], v[244:247]
	s_nop 0
	v_mfma_f32_4x4x4_16b_bf16 v[240:243], v[86:87], v[132:133], v[240:243]
	v_mfma_f32_4x4x4_16b_bf16 v[244:247], v[88:89], v[132:133], v[244:247]
	s_nop 0
	v_mfma_f32_4x4x4_16b_bf16 v[240:243], v[90:91], v[132:133], v[240:243]
	v_mfma_f32_4x4x4_16b_bf16 v[244:247], v[92:93], v[132:133], v[244:247]
	s_nop 0
	v_mfma_f32_4x4x4_16b_bf16 v[240:243], v[94:95], v[132:133], v[240:243]
	v_mfma_f32_4x4x4_16b_bf16 v[244:247], v[96:97], v[132:133], v[244:247]
	s_nop 0
	s_setprio 0
	s_barrier
	s_cmpk_gt_u32 s88, 0xff
	s_cbranch_scc1 .LBB0_278
	s_barrier
.LBB0_278:
	s_nop 4
	v_add_f32_e32 v240, v240, v244
	v_add_f32_e32 v241, v241, v245
	v_add_f32_e32 v242, v242, v246
	v_add_f32_e32 v243, v243, v247
	v_and_b32_e32 v244, 3, v0
	v_cmp_eq_u32_e64 s[98:99], 1, v244
	s_nop 1
	v_cndmask_b32_e64 v240, v240, v241, s[98:99]
	v_cmp_eq_u32_e64 s[98:99], 2, v244
	s_nop 1
	v_cndmask_b32_e64 v240, v240, v242, s[98:99]
	v_cmp_eq_u32_e64 s[98:99], 3, v244
	s_nop 1
	v_cndmask_b32_e64 v240, v240, v243, s[98:99]
	v_mov_b32_e32 v245, v240
	s_nop 1
	v_permlane32_swap_b32_e32 v245, v240
	s_nop 1
	v_add_f32_e32 v240, v240, v245
	ds_write_b32 v187, v240
	v_add_u32_e32 v245, s90, v184
	s_waitcnt lgkmcnt(0)
	ds_read_b128 v[2:5], v245
	ds_read_b128 v[6:9], v245 offset:32
	ds_read_b128 v[10:13], v245 offset:64
	ds_read_b128 v[14:17], v245 offset:96
	s_waitcnt lgkmcnt(0)
	s_ashr_i32 s4, s89, 1
	s_andn2_b32 s4, s4, 31
	s_ashr_i32 s5, s4, 31
	s_add_u32 s4, s4, s51
	s_addc_u32 s5, s5, 0
	s_lshl_b64 s[4:5], s[4:5], 12
	s_nop 2
	v_rcp_f32_e32 v83, v2
	s_add_u32 s4, s44, s4
	s_addc_u32 s5, s45, s5
	v_and_b32_e32 v82, 31, v211
	s_add_u32 s4, s4, s46
	v_rcp_f32_e32 v85, v4
	s_addc_u32 s5, s5, s47
	v_lshlrev_b32_e32 v184, 1, v82
	v_lshlrev_b32_e32 v4, 9, v211
	v_rcp_f32_e32 v84, v3
	v_rcp_f32_e32 v87, v6
	v_lshl_add_u64 v[2:3], s[4:5], 0, v[184:185]
	v_and_b32_e32 v184, 0x4000, v4
	v_mul_f32_e32 v6, v18, v83
	v_rcp_f32_e32 v88, v7
	v_lshl_add_u64 v[2:3], v[2:3], 0, v[184:185]
	v_bfe_u32 v7, v6, 16, 1
	v_add3_u32 v18, v6, v7, s61
	v_add_co_u32_e32 v6, vcc, s63, v2
	v_rcp_f32_e32 v86, v5
	s_nop 0
	v_addc_co_u32_e32 v7, vcc, 0, v3, vcc
	global_store_short_d16_hi v[6:7], v18, off offset:-4096
	v_mul_f32_e32 v18, v34, v83
	v_bfe_u32 v34, v18, 16, 1
	v_lshl_add_u64 v[4:5], v[2:3], 0, s[38:39]
	v_add3_u32 v18, v18, v34, s61
	global_store_short_d16_hi v[4:5], v18, off offset:64
	v_mul_f32_e32 v18, v50, v83
	v_bfe_u32 v34, v18, 16, 1
	v_add3_u32 v18, v18, v34, s61
	global_store_short_d16_hi v[4:5], v18, off offset:128
	v_mul_f32_e32 v18, v66, v83
	v_bfe_u32 v34, v18, 16, 1
	v_add3_u32 v18, v18, v34, s61
	global_store_short_d16_hi v[4:5], v18, off offset:192
	v_mul_f32_e32 v4, v19, v84
	v_bfe_u32 v5, v4, 16, 1
	v_add3_u32 v4, v4, v5, s61
	global_store_short_d16_hi v[6:7], v4, off
	v_mul_f32_e32 v4, v35, v84
	v_bfe_u32 v5, v4, 16, 1
	v_add3_u32 v4, v4, v5, s61
	global_store_short_d16_hi v[6:7], v4, off offset:64
; __device__ __forceinline__ int crow(int r, int hi) { return (r & 3) + 8 * (r >> 2) + 4 * hi; }
; __device__ __forceinline__ unsigned f2bf(float f) { unsigned u = __builtin_bit_cast(unsigned, f); return (u + 0x7fffu + ((u >> 16) & 1u)) >> 16; }
;     ...
;     att::bf16* Ow = Obase + ((size_t)b * SEQ + (size_t)qb * 256 + wave_ * 32) * 2048 + h * 128;
; #pragma unroll
;     for (int r = 0; r < 16; ++r) { const int orow = crow(r, hi);
; #pragma unroll
;         for (int d0 = 0; d0 < 4; ++d0) Ow[(size_t)orow * 2048 + d0 * 32 + r32] = (att::bf16)f2bf(o[d0][r] * rli[r]); }
	v_mul_f32_e32 v4, v51, v84
	v_bfe_u32 v5, v4, 16, 1
	v_add3_u32 v4, v4, v5, s61
	global_store_short_d16_hi v[6:7], v4, off offset:128
	v_mul_f32_e32 v4, v67, v84
	v_bfe_u32 v5, v4, 16, 1
	v_add3_u32 v4, v4, v5, s61
	global_store_short_d16_hi v[6:7], v4, off offset:192
	v_mul_f32_e32 v4, v20, v85
	v_bfe_u32 v5, v4, 16, 1
	v_add3_u32 v18, v4, v5, s61
	v_add_co_u32_e32 v4, vcc, s64, v2
	v_rcp_f32_e32 v8, v8
	s_nop 0
	v_addc_co_u32_e32 v5, vcc, 0, v3, vcc
	v_add_co_u32_e32 v6, vcc, s65, v2
	v_rcp_f32_e32 v9, v9
	s_nop 0
	v_addc_co_u32_e32 v7, vcc, 0, v3, vcc
	global_store_short_d16_hi v[6:7], v18, off offset:-4096
	v_mul_f32_e32 v18, v36, v85
	v_bfe_u32 v19, v18, 16, 1
	v_add3_u32 v18, v18, v19, s61
	global_store_short_d16_hi v[4:5], v18, off offset:64
	v_mul_f32_e32 v18, v52, v85
	v_bfe_u32 v19, v18, 16, 1
	v_add3_u32 v18, v18, v19, s61
	global_store_short_d16_hi v[4:5], v18, off offset:128
	v_mul_f32_e32 v18, v68, v85
	v_bfe_u32 v19, v18, 16, 1
	v_add3_u32 v18, v18, v19, s61
	global_store_short_d16_hi v[4:5], v18, off offset:192
	v_mul_f32_e32 v4, v21, v86
	v_bfe_u32 v5, v4, 16, 1
	v_add3_u32 v4, v4, v5, s61
	global_store_short_d16_hi v[6:7], v4, off
	v_mul_f32_e32 v4, v37, v86
	v_bfe_u32 v5, v4, 16, 1
	v_add3_u32 v4, v4, v5, s61
	global_store_short_d16_hi v[6:7], v4, off offset:64
	v_mul_f32_e32 v4, v53, v86
	v_bfe_u32 v5, v4, 16, 1
	v_add3_u32 v4, v4, v5, s61
	global_store_short_d16_hi v[6:7], v4, off offset:128
	v_mul_f32_e32 v4, v69, v86
	v_bfe_u32 v5, v4, 16, 1
	v_add3_u32 v4, v4, v5, s61
	global_store_short_d16_hi v[6:7], v4, off offset:192
	v_mul_f32_e32 v4, v22, v87
	v_bfe_u32 v5, v4, 16, 1
	v_add3_u32 v18, v4, v5, s61
	v_add_co_u32_e32 v4, vcc, s66, v2
	v_rcp_f32_e32 v10, v10
	s_nop 0
	v_addc_co_u32_e32 v5, vcc, 0, v3, vcc
	v_add_co_u32_e32 v6, vcc, s67, v2
	v_rcp_f32_e32 v11, v11
	s_nop 0
	v_addc_co_u32_e32 v7, vcc, 0, v3, vcc
	global_store_short_d16_hi v[6:7], v18, off offset:-4096
	v_mul_f32_e32 v18, v38, v87
	v_bfe_u32 v19, v18, 16, 1
	v_add3_u32 v18, v18, v19, s61
	global_store_short_d16_hi v[4:5], v18, off offset:64
	v_mul_f32_e32 v18, v54, v87
	v_bfe_u32 v19, v18, 16, 1
	v_add3_u32 v18, v18, v19, s61
	global_store_short_d16_hi v[4:5], v18, off offset:128
	v_mul_f32_e32 v18, v70, v87
	v_bfe_u32 v19, v18, 16, 1
	v_add3_u32 v18, v18, v19, s61
	global_store_short_d16_hi v[4:5], v18, off offset:192
	v_mul_f32_e32 v4, v23, v88
	v_bfe_u32 v5, v4, 16, 1
	v_add3_u32 v4, v4, v5, s61
	global_store_short_d16_hi v[6:7], v4, off
	v_mul_f32_e32 v4, v39, v88
	v_bfe_u32 v5, v4, 16, 1
	v_add3_u32 v4, v4, v5, s61
	global_store_short_d16_hi v[6:7], v4, off offset:64
	v_mul_f32_e32 v4, v55, v88
	v_bfe_u32 v5, v4, 16, 1
	v_add3_u32 v4, v4, v5, s61
	global_store_short_d16_hi v[6:7], v4, off offset:128
	v_mul_f32_e32 v4, v71, v88
	v_bfe_u32 v5, v4, 16, 1
	v_add3_u32 v4, v4, v5, s61
	global_store_short_d16_hi v[6:7], v4, off offset:192
	v_mul_f32_e32 v4, v24, v8
	v_bfe_u32 v5, v4, 16, 1
	v_add3_u32 v18, v4, v5, s61
	v_add_co_u32_e32 v4, vcc, s68, v2
	v_rcp_f32_e32 v12, v12
	s_nop 0
	v_addc_co_u32_e32 v5, vcc, 0, v3, vcc
	v_add_co_u32_e32 v6, vcc, s69, v2
	v_rcp_f32_e32 v13, v13
	s_nop 0
	v_addc_co_u32_e32 v7, vcc, 0, v3, vcc
	global_store_short_d16_hi v[6:7], v18, off offset:-4096
	v_mul_f32_e32 v18, v40, v8
	v_bfe_u32 v19, v18, 16, 1
	v_add3_u32 v18, v18, v19, s61
	global_store_short_d16_hi v[4:5], v18, off offset:64
	v_mul_f32_e32 v18, v56, v8
	v_bfe_u32 v19, v18, 16, 1
	v_add3_u32 v18, v18, v19, s61
	v_mul_f32_e32 v8, v72, v8
	global_store_short_d16_hi v[4:5], v18, off offset:128
	v_bfe_u32 v18, v8, 16, 1
	v_add3_u32 v8, v8, v18, s61
	global_store_short_d16_hi v[4:5], v8, off offset:192
	v_mul_f32_e32 v4, v25, v9
	v_bfe_u32 v5, v4, 16, 1
	v_add3_u32 v4, v4, v5, s61
	global_store_short_d16_hi v[6:7], v4, off
	v_mul_f32_e32 v4, v41, v9
	v_bfe_u32 v5, v4, 16, 1
	v_add3_u32 v4, v4, v5, s61
	global_store_short_d16_hi v[6:7], v4, off offset:64
	v_mul_f32_e32 v4, v57, v9
	v_bfe_u32 v5, v4, 16, 1
	v_add3_u32 v4, v4, v5, s61
	global_store_short_d16_hi v[6:7], v4, off offset:128
	v_mul_f32_e32 v4, v73, v9
	v_bfe_u32 v5, v4, 16, 1
	v_add3_u32 v4, v4, v5, s61
	global_store_short_d16_hi v[6:7], v4, off offset:192
	v_mul_f32_e32 v4, v26, v10
	v_bfe_u32 v5, v4, 16, 1
	v_add3_u32 v8, v4, v5, s61
	v_add_co_u32_e32 v4, vcc, s74, v2
	v_rcp_f32_e32 v14, v14
	s_nop 0
	v_addc_co_u32_e32 v5, vcc, 0, v3, vcc
	v_add_co_u32_e32 v6, vcc, s75, v2
	v_rcp_f32_e32 v15, v15
	s_nop 0
	v_addc_co_u32_e32 v7, vcc, 0, v3, vcc
	global_store_short_d16_hi v[6:7], v8, off offset:-4096
	v_mul_f32_e32 v8, v42, v10
	v_bfe_u32 v9, v8, 16, 1
	v_add3_u32 v8, v8, v9, s61
; __device__ __forceinline__ int crow(int r, int hi) { return (r & 3) + 8 * (r >> 2) + 4 * hi; }
; #define LAS __attribute__((address_space(3)))
; __device__ __forceinline__ unsigned f2bf(float f) { unsigned u = __builtin_bit_cast(unsigned, f); return (u + 0x7fffu + ((u >> 16) & 1u)) >> 16; }
;     ...
;     att::bf16* Ow = Obase + ((size_t)b * SEQ + (size_t)qb * 256 + wave_ * 32) * 2048 + h * 128;
; #pragma unroll
;     for (int r = 0; r < 16; ++r) { const int orow = crow(r, hi);
; #pragma unroll
;         for (int d0 = 0; d0 < 4; ++d0) Ow[(size_t)orow * 2048 + d0 * 32 + r32] = (att::bf16)f2bf(o[d0][r] * rli[r]); }
; __device__ __forceinline__ void p2_attention(const Frame& F, KArgs a) {
;     ...
;     for (int L = F.vcu; L < 2048; L += F.G) {
;     ...
;         if (L >> 8 == 4 && blockIdx.x == PROBE_BLOCK && F.tid == 0) { volatile LAS unsigned* M_ = (volatile LAS unsigned*)((LAS unsigned char*)F.lds + MISC_OFF); M_[21] = (unsigned)__builtin_amdgcn_s_memrealtime() - M_[20]; }
;     ...
;         const int i = L >> 8, v = L & 255, x = v >> 5, qb = v & 31, b = x >> 1;
;     ...
;         if (i < 4) attn_unit_A(F, a, b, 4 * (x & 1) + i, qb, (att::bf16*)(a->ws + WS_XN));
	global_store_short_d16_hi v[4:5], v8, off offset:64
	v_mul_f32_e32 v8, v58, v10
	v_bfe_u32 v9, v8, 16, 1
	v_add3_u32 v8, v8, v9, s61
	global_store_short_d16_hi v[4:5], v8, off offset:128
	v_mul_f32_e32 v8, v74, v10
	v_bfe_u32 v9, v8, 16, 1
	v_add3_u32 v8, v8, v9, s61
	global_store_short_d16_hi v[4:5], v8, off offset:192
	v_mul_f32_e32 v4, v27, v11
	v_bfe_u32 v5, v4, 16, 1
	v_add3_u32 v4, v4, v5, s61
	global_store_short_d16_hi v[6:7], v4, off
	v_mul_f32_e32 v4, v43, v11
	v_bfe_u32 v5, v4, 16, 1
	v_add3_u32 v4, v4, v5, s61
	global_store_short_d16_hi v[6:7], v4, off offset:64
	v_mul_f32_e32 v4, v59, v11
	v_bfe_u32 v5, v4, 16, 1
	v_add3_u32 v4, v4, v5, s61
	global_store_short_d16_hi v[6:7], v4, off offset:128
	v_mul_f32_e32 v4, v75, v11
	v_bfe_u32 v5, v4, 16, 1
	v_add3_u32 v4, v4, v5, s61
	global_store_short_d16_hi v[6:7], v4, off offset:192
	v_mul_f32_e32 v4, v28, v12
	v_bfe_u32 v5, v4, 16, 1
	v_add3_u32 v8, v4, v5, s61
	v_add_co_u32_e32 v4, vcc, s76, v2
	v_rcp_f32_e32 v16, v16
	s_nop 0
	v_addc_co_u32_e32 v5, vcc, 0, v3, vcc
	v_add_co_u32_e32 v6, vcc, s77, v2
	v_rcp_f32_e32 v17, v17
	s_nop 0
	v_addc_co_u32_e32 v7, vcc, 0, v3, vcc
	global_store_short_d16_hi v[6:7], v8, off offset:-4096
	v_mul_f32_e32 v8, v44, v12
	v_bfe_u32 v9, v8, 16, 1
	v_add3_u32 v8, v8, v9, s61
	global_store_short_d16_hi v[4:5], v8, off offset:64
	v_mul_f32_e32 v8, v60, v12
	v_bfe_u32 v9, v8, 16, 1
	v_add3_u32 v8, v8, v9, s61
	global_store_short_d16_hi v[4:5], v8, off offset:128
	v_mul_f32_e32 v8, v76, v12
	v_bfe_u32 v9, v8, 16, 1
	v_add3_u32 v8, v8, v9, s61
	global_store_short_d16_hi v[4:5], v8, off offset:192
	v_mul_f32_e32 v4, v29, v13
	v_bfe_u32 v5, v4, 16, 1
	v_add3_u32 v4, v4, v5, s61
	global_store_short_d16_hi v[6:7], v4, off
	v_mul_f32_e32 v4, v45, v13
	v_bfe_u32 v5, v4, 16, 1
	v_add3_u32 v4, v4, v5, s61
	global_store_short_d16_hi v[6:7], v4, off offset:64
	v_mul_f32_e32 v4, v61, v13
	v_bfe_u32 v5, v4, 16, 1
	v_add3_u32 v4, v4, v5, s61
	global_store_short_d16_hi v[6:7], v4, off offset:128
	v_mul_f32_e32 v4, v77, v13
	v_bfe_u32 v5, v4, 16, 1
	v_add3_u32 v4, v4, v5, s61
	global_store_short_d16_hi v[6:7], v4, off offset:192
	v_mul_f32_e32 v4, v30, v14
	v_bfe_u32 v5, v4, 16, 1
	v_add3_u32 v8, v4, v5, s61
	v_add_co_u32_e32 v4, vcc, s78, v2
	s_nop 1
	v_addc_co_u32_e32 v5, vcc, 0, v3, vcc
	v_add_co_u32_e32 v6, vcc, s79, v2
	s_nop 1
	v_addc_co_u32_e32 v7, vcc, 0, v3, vcc
	global_store_short_d16_hi v[6:7], v8, off offset:-4096
	v_mul_f32_e32 v8, v46, v14
	v_bfe_u32 v9, v8, 16, 1
	v_add3_u32 v8, v8, v9, s61
	global_store_short_d16_hi v[4:5], v8, off offset:64
	v_mul_f32_e32 v8, v62, v14
	v_bfe_u32 v9, v8, 16, 1
	v_add3_u32 v8, v8, v9, s61
	global_store_short_d16_hi v[4:5], v8, off offset:128
	v_mul_f32_e32 v8, v78, v14
	v_bfe_u32 v9, v8, 16, 1
	v_add3_u32 v8, v8, v9, s61
	global_store_short_d16_hi v[4:5], v8, off offset:192
	v_mul_f32_e32 v4, v31, v15
	v_bfe_u32 v5, v4, 16, 1
	v_add3_u32 v4, v4, v5, s61
	global_store_short_d16_hi v[6:7], v4, off
	v_mul_f32_e32 v4, v47, v15
	v_bfe_u32 v5, v4, 16, 1
	v_add3_u32 v4, v4, v5, s61
	global_store_short_d16_hi v[6:7], v4, off offset:64
	v_mul_f32_e32 v4, v63, v15
	v_bfe_u32 v5, v4, 16, 1
	v_add3_u32 v4, v4, v5, s61
	global_store_short_d16_hi v[6:7], v4, off offset:128
	v_mul_f32_e32 v4, v79, v15
	v_bfe_u32 v5, v4, 16, 1
	v_add3_u32 v4, v4, v5, s61
	global_store_short_d16_hi v[6:7], v4, off offset:192
	v_mul_f32_e32 v4, v32, v16
	v_bfe_u32 v5, v4, 16, 1
	v_add3_u32 v6, v4, v5, s61
	v_add_co_u32_e32 v4, vcc, s80, v2
	s_nop 1
	v_addc_co_u32_e32 v5, vcc, 0, v3, vcc
	v_add_co_u32_e32 v2, vcc, s81, v2
	s_nop 1
	v_addc_co_u32_e32 v3, vcc, 0, v3, vcc
	global_store_short_d16_hi v[2:3], v6, off offset:-4096
	v_mul_f32_e32 v6, v48, v16
	v_bfe_u32 v7, v6, 16, 1
	v_add3_u32 v6, v6, v7, s61
	global_store_short_d16_hi v[4:5], v6, off offset:64
	v_mul_f32_e32 v6, v64, v16
	v_bfe_u32 v7, v6, 16, 1
	v_add3_u32 v6, v6, v7, s61
	global_store_short_d16_hi v[4:5], v6, off offset:128
	v_mul_f32_e32 v6, v80, v16
	v_bfe_u32 v7, v6, 16, 1
	v_add3_u32 v6, v6, v7, s61
	global_store_short_d16_hi v[4:5], v6, off offset:192
	v_mul_f32_e32 v4, v33, v17
	v_bfe_u32 v5, v4, 16, 1
	v_add3_u32 v4, v4, v5, s61
	global_store_short_d16_hi v[2:3], v4, off
	v_mul_f32_e32 v4, v49, v17
	v_bfe_u32 v5, v4, 16, 1
	v_add3_u32 v4, v4, v5, s61
	global_store_short_d16_hi v[2:3], v4, off offset:64
	v_mul_f32_e32 v4, v65, v17
	v_bfe_u32 v5, v4, 16, 1
	v_add3_u32 v4, v4, v5, s61
	global_store_short_d16_hi v[2:3], v4, off offset:128
	v_mul_f32_e32 v4, v81, v17
	v_bfe_u32 v5, v4, 16, 1
	v_add3_u32 v4, v4, v5, s61
	global_store_short_d16_hi v[2:3], v4, off offset:192
	s_cmp_lt_i32 s49, 4
	s_cbranch_scc1 .LBB0_260

; __device__ __forceinline__ float softmax_rowmax(const f32x16& p0, const f32x16& p1) {
;   const float m0 = p1[0] + 0.0f; float a, b;
;   asm("v_max3_f32 %0, %1, %2, %3\n\tv_max3_f32 %0, %0, %4, %5\n\tv_max3_f32 %0, %0, %6, %7\n\tv_max3_f32 %0, %0, %8, %9\n\t"
;       "v_max3_f32 %0, %0, %10, %11\n\tv_max3_f32 %0, %0, %12, %13\n\tv_max3_f32 %0, %0, %14, %15\n\tv_max3_f32 %0, %0, %16, %17"
;       : "=&v"(a) : "v"(m0), "v"(p0[0]), "v"(p0[1]), "v"(p0[2]), "v"(p0[3]), "v"(p0[4]), "v"(p0[5]), "v"(p0[6]), "v"(p0[7]), "v"(p0[8]), "v"(p0[9]), "v"(p0[10]), "v"(p0[11]), "v"(p0[12]), "v"(p0[13]), "v"(p0[14]), "v"(p0[15]));
;   asm("v_max3_f32 %0, %1, %2, %3\n\tv_max3_f32 %0, %0, %4, %5\n\tv_max3_f32 %0, %0, %6, %7\n\tv_max3_f32 %0, %0, %8, %9\n\t"
;       "v_max3_f32 %0, %0, %10, %11\n\tv_max3_f32 %0, %0, %12, %13\n\tv_max3_f32 %0, %0, %14, %15\n\tv_max_f32 %0, %0, %16"
;       : "=&v"(b) : "v"(a), "v"(p1[1]), "v"(p1[2]), "v"(p1[3]), "v"(p1[4]), "v"(p1[5]), "v"(p1[6]), "v"(p1[7]), "v"(p1[8]), "v"(p1[9]), "v"(p1[10]), "v"(p1[11]), "v"(p1[12]), "v"(p1[13]), "v"(p1[14]), "v"(p1[15]));
;   return b;
; }
; __device__ __forceinline__ float softmax_shift(f32x16& p0, f32x16& p1, f32x16& negm, float pmax, bool first) {
;   asm volatile("s_nop 4" ::: "memory");
;   { auto rr = __builtin_amdgcn_permlane32_swap(__float_as_uint(pmax), __float_as_uint(pmax), false, false);
;     pmax = fmaxf(__uint_as_float(rr[0]), __uint_as_float(rr[1])); }
;   const float delta = first ? pmax : fmaxf(pmax, 0.f);
; #pragma unroll
;   for (int r = 0; r < 16; ++r) { p0[r] -= delta; p1[r] -= delta; negm[r] -= delta; }
;   return first ? 1.f : __builtin_amdgcn_exp2f(-delta);
; }
; __device__ __forceinline__ void softmax_exp_pack(f32x16& p0, f32x16& p1, bf16x8& pa0, bf16x8& pa1, bf16x8& pa2, bf16x8& pa3) {
; #pragma unroll
;   for (int r = 0; r < 16; ++r) { p0[r] = __builtin_amdgcn_exp2f(p0[r]); p1[r] = __builtin_amdgcn_exp2f(p1[r]); }
;     ...
;   ATT_PK4(p0, 0, pa0); ATT_PK4(p0, 8, pa1); ATT_PK4(p1, 0, pa2); ATT_PK4(p1, 8, pa3);
;     ...
; }
;     ...
;   if constexpr (DQK == 64) { sk0 = ek0; sv0 = ev0; sv1 = ev1; ATT_WRITE_K(0); ATT_WRITE_V(0); sk0 = ek1; ATT_WRITE_K(SHM_K); }
;   else { ATT_LOAD_K(0); ATT_LOAD_V(0); ATT_WRITE_K(0); ATT_WRITE_V(0);
;          ATT_LOAD_K(1); ATT_WRITE_K(SHM_K); }
;   ATT_LOAD_K(2); ATT_LOAD_V(1);
;   asm volatile("s_waitcnt lgkmcnt(0)" ::: "memory"); ATT_BAR();
;   if (grp == 1) ATT_BAR();
.LBB0_281:
	v_mul_u32_u24_e32 v18, 0x90, v62
	v_add3_u32 v78, 0, v184, v18
	ds_read_b128 v[18:21], v78 offset:49152
	v_mad_u32_u24 v166, v62, s82, 0
	v_add_u32_e32 v172, v166, v184
	ds_read_b128 v[34:37], v172 offset:53760
	ds_read_b128 v[66:69], v78 offset:49184
	ds_read_b128 v[70:73], v78 offset:49216
	s_and_b32 s4, s92, 0x3fffffc0
	v_and_b32_e32 v63, 63, v63
	s_lshl_b32 s4, s4, 2
	s_add_i32 s6, s4, 0
	s_waitcnt lgkmcnt(3)
	v_mfma_f32_32x32x16_bf16 v[18:33], v[18:21], v[136:139], 0
	s_add_i32 s6, s6, 0x23080
	s_mov_b32 s97, 1
	s_waitcnt lgkmcnt(2)
	v_mfma_f32_32x32x16_bf16 v[34:49], v[34:37], v[136:139], 0
	s_waitcnt lgkmcnt(1)
	v_mfma_f32_32x32x16_bf16 v[18:33], v[66:69], v[140:143], v[18:33]
	ds_read_b128 v[66:69], v78 offset:53792
	ds_read_b128 v[74:77], v78 offset:49248
	s_waitcnt lgkmcnt(1)
	v_mfma_f32_32x32x16_bf16 v[34:49], v[66:69], v[140:143], v[34:49]
	v_mfma_f32_32x32x16_bf16 v[18:33], v[70:73], v[144:147], v[18:33]
	ds_read_b128 v[66:69], v78 offset:53824
	ds_read_b128 v[70:73], v78 offset:53856
	s_waitcnt lgkmcnt(1)
	v_mfma_f32_32x32x16_bf16 v[34:49], v[66:69], v[144:147], v[34:49]
	v_lshlrev_b32_e32 v67, 3, v63
	v_lshlrev_b32_e32 v69, 4, v63
	v_add_u32_e32 v66, 0xc000, v169
	v_and_b32_e32 v68, 24, v67
	v_and_b32_e32 v69, 0xc0, v69
	v_and_b32_e32 v67, 0x100, v67
	v_mfma_f32_32x32x16_bf16 v[18:33], v[74:77], v[148:151], v[18:33]
	v_lshlrev_b32_e32 v74, 1, v63
	v_and_b32_e32 v74, 32, v74
	s_waitcnt lgkmcnt(0)
	v_mfma_f32_32x32x16_bf16 v[34:49], v[70:73], v[148:151], v[34:49]
	s_barrier
	v_cmp_gt_u32_e64 s[4:5], 32, v63
	v_lshl_add_u32 v165, v62, 2, s6
	s_nop 9
	v_add_f32_e32 v62, 0, v34
	v_max3_f32 v63, v62, v18, v19
	v_max3_f32 v63, v63, v20, v21
	v_max3_f32 v63, v63, v22, v23
	v_max3_f32 v63, v63, v24, v25
	v_max3_f32 v63, v63, v26, v27
	v_max3_f32 v63, v63, v28, v29
	v_max3_f32 v63, v63, v30, v31
	v_max3_f32 v63, v63, v32, v33
	s_nop 4
	v_add3_u32 v68, 0, v68, v69
	v_max3_f32 v62, v63, v35, v36
	v_max3_f32 v62, v62, v37, v38
	v_max3_f32 v62, v62, v39, v40
	v_max3_f32 v62, v62, v41, v42
	v_max3_f32 v62, v62, v43, v44
	v_max3_f32 v62, v62, v45, v46
	v_max3_f32 v62, v62, v47, v48
	v_max_f32 v62, v62, v49
	v_add3_u32 v131, v68, v74, v67
	v_mov_b32_e32 v63, v62
	s_nop 1
	v_permlane32_swap_b32_e32 v62, v63
	v_max_f32_e32 v63, v63, v63
	v_max_f32_e32 v62, v62, v62
	v_max_f32_e32 v62, v62, v63
	v_sub_f32_e32 v18, v18, v62
	v_sub_f32_e32 v34, v34, v62
	v_sub_f32_e32 v19, v19, v62
	v_sub_f32_e32 v35, v35, v62
	v_sub_f32_e32 v20, v20, v62
	v_sub_f32_e32 v36, v36, v62
	v_sub_f32_e32 v21, v21, v62
	v_sub_f32_e32 v37, v37, v62
	v_sub_f32_e32 v22, v22, v62
	v_sub_f32_e32 v38, v38, v62
	v_sub_f32_e32 v23, v23, v62
	v_sub_f32_e32 v39, v39, v62
	v_sub_f32_e32 v24, v24, v62
	v_sub_f32_e32 v40, v40, v62
	v_sub_f32_e32 v25, v25, v62
	v_sub_f32_e32 v41, v41, v62
	v_sub_f32_e32 v26, v26, v62
	v_sub_f32_e32 v42, v42, v62
	v_sub_f32_e32 v27, v27, v62
	v_sub_f32_e32 v43, v43, v62
	v_sub_f32_e32 v28, v28, v62
	v_sub_f32_e32 v44, v44, v62
	v_sub_f32_e32 v29, v29, v62
	v_sub_f32_e32 v45, v45, v62
	v_sub_f32_e32 v30, v30, v62
	v_sub_f32_e32 v46, v46, v62
	v_sub_f32_e32 v31, v31, v62
	v_sub_f32_e32 v47, v47, v62
	v_sub_f32_e32 v32, v32, v62
	v_sub_f32_e32 v48, v48, v62
	v_sub_f32_e32 v33, v33, v62
	v_sub_f32_e32 v49, v49, v62
	v_exp_f32_e32 v18, v18
	v_exp_f32_e32 v34, v34
	v_exp_f32_e32 v19, v19
	v_exp_f32_e32 v35, v35
	v_exp_f32_e32 v20, v20
	v_exp_f32_e32 v36, v36
	v_exp_f32_e32 v21, v21
	v_exp_f32_e32 v37, v37
	v_exp_f32_e32 v22, v22
	v_exp_f32_e32 v38, v38
	v_exp_f32_e32 v23, v23
	v_exp_f32_e32 v39, v39
	v_exp_f32_e32 v24, v24
	v_exp_f32_e32 v40, v40
	v_exp_f32_e32 v25, v25
	v_exp_f32_e32 v41, v41
	v_exp_f32_e32 v26, v26
	v_exp_f32_e32 v42, v42
	v_exp_f32_e32 v27, v27
	v_exp_f32_e32 v43, v43
	v_exp_f32_e32 v28, v28
	v_exp_f32_e32 v44, v44
	v_exp_f32_e32 v29, v29
	v_exp_f32_e32 v45, v45
	v_exp_f32_e32 v30, v30
	v_exp_f32_e32 v46, v46
	v_exp_f32_e32 v31, v31
	v_exp_f32_e32 v47, v47
	v_exp_f32_e32 v32, v32
	v_exp_f32_e32 v48, v48
	v_exp_f32_e32 v33, v33
	v_exp_f32_e32 v49, v49
	v_sub_f32_e32 v82, 0, v62
	v_mov_b32_e32 v83, v82
	v_mov_b32_e32 v84, v82
	v_mov_b32_e32 v85, v82
	v_mov_b32_e32 v86, v82
	v_mov_b32_e32 v87, v82
	v_mov_b32_e32 v88, v82
	v_mov_b32_e32 v89, v82
	v_mov_b32_e32 v90, v82
	v_mov_b32_e32 v91, v82
	v_mov_b32_e32 v92, v82
	v_mov_b32_e32 v93, v82
	v_mov_b32_e32 v94, v82
	v_mov_b32_e32 v95, v82
	v_mov_b32_e32 v96, v82
	v_mov_b32_e32 v97, v82
	v_cvt_pk_bf16_f32 v98, v18, v19
	v_cvt_pk_bf16_f32 v99, v20, v21
	v_cvt_pk_bf16_f32 v100, v22, v23
	v_cvt_pk_bf16_f32 v101, v24, v25
	v_cvt_pk_bf16_f32 v102, v26, v27
	v_cvt_pk_bf16_f32 v103, v28, v29
	v_cvt_pk_bf16_f32 v104, v30, v31
	v_cvt_pk_bf16_f32 v105, v32, v33
	v_cvt_pk_bf16_f32 v106, v34, v35
	v_cvt_pk_bf16_f32 v107, v36, v37
	v_cvt_pk_bf16_f32 v108, v38, v39
	v_cvt_pk_bf16_f32 v109, v40, v41
	v_cvt_pk_bf16_f32 v110, v42, v43
	v_cvt_pk_bf16_f32 v111, v44, v45
	v_cvt_pk_bf16_f32 v112, v46, v47
	v_cvt_pk_bf16_f32 v113, v48, v49
	s_waitcnt vmcnt(1)
	ds_write_b128 v66, v[58:61] offset:18432
	ds_write_b128 v64, v[50:53] offset:16384
	s_waitcnt vmcnt(0)
	ds_write_b128 v65, v[54:57] offset:16384
	ds_read_b64_tr_b16 v[18:19], v131
	ds_read_b64_tr_b16 v[20:21], v131 offset:2048
	ds_read_b64_tr_b16 v[34:35], v131 offset:4096
	ds_read_b64_tr_b16 v[36:37], v131 offset:6144
	ds_read_b64_tr_b16 v[38:39], v131 offset:8192
	ds_read_b64_tr_b16 v[40:41], v131 offset:10240
	ds_read_b64_tr_b16 v[42:43], v131 offset:12288
	ds_read_b64_tr_b16 v[44:45], v131 offset:14336
	s_waitcnt lgkmcnt(8)
	s_barrier
; #define ATT_SBAR() __builtin_amdgcn_sched_barrier(0)
; __device__ __forceinline__ unsigned cvtpk(float lo, float hi) { f32x2_t v = {lo, hi}; bf16x2_t b = __builtin_convertvector(v, bf16x2_t); return __builtin_bit_cast(unsigned, b); }
; #define ATT_LOAD_K(t) do { const unsigned so_ = (unsigned)(t) * (unsigned)(KVBLK * LDK * 2); sk0 = __builtin_bit_cast(bf16x8, __builtin_amdgcn_raw_buffer_load_b128(krs, koff, so_, 0)); \
;     if constexpr (DQK == 128) sk1 = __builtin_bit_cast(bf16x8, __builtin_amdgcn_raw_buffer_load_b128(krs, koff, so_ + (unsigned)(32 * LDK * 2), 0)); } while (0)
; #define ATT_LOAD_V(t) do { const unsigned so_ = (unsigned)(t) * (unsigned)(KVBLK * LDV * 2); sv0 = __builtin_bit_cast(bf16x8, __builtin_amdgcn_raw_buffer_load_b128(vrs, voff, so_, 0)); \
;     sv1 = __builtin_bit_cast(bf16x8, __builtin_amdgcn_raw_buffer_load_b128(vrs, voff, so_ + (unsigned)(32 * LDV * 2), 0)); } while (0)
; #define ATT_WRITE_K(so) do { *(bf16x8*)(K_lds + (so) + kswz<DQK>(kr, kc * 2)) = sk0; if constexpr (DQK == 128) *(bf16x8*)(K_lds + (so) + kswz<DQK>(32 + kr, kc * 2)) = sk1; } while (0)
;     ...
;   for (int t = 0; t + 1 < NT; ++t) {
;     if constexpr (ABL & 1) { u32x4 w0 = {cvtpk(p0[0], p0[1]), cvtpk(p0[2], p0[3]), cvtpk(p0[4], p0[5]), cvtpk(p0[6], p0[7])}, w1 = {cvtpk(p0[8], p0[9]), cvtpk(p0[10], p0[11]), cvtpk(p0[12], p0[13]), cvtpk(p0[14], p0[15])};
;         u32x4 w2 = {cvtpk(p1[0], p1[1]), cvtpk(p1[2], p1[3]), cvtpk(p1[4], p1[5]), cvtpk(p1[6], p1[7])}, w3 = {cvtpk(p1[8], p1[9]), cvtpk(p1[10], p1[11]), cvtpk(p1[12], p1[13]), cvtpk(p1[14], p1[15])};
;         pa0 = *reinterpret_cast<bf16x8*>(&w0); pa1 = *reinterpret_cast<bf16x8*>(&w1); pa2 = *reinterpret_cast<bf16x8*>(&w2); pa3 = *reinterpret_cast<bf16x8*>(&w3); }
;     else { ATT_SOFTMAX(t == 0); }
;     if constexpr (!(ABL & 4)) { ATT_WRITE_K(k2); ATT_WRITE_V(v1); }
;     ATT_SBAR();
; #pragma unroll
;     for (int ks = 0; ks < 4; ++ks) ATT_VPAIR(va, v0, 0, ks);
;     asm volatile("s_waitcnt lgkmcnt(8)" ::: "memory"); ATT_BAR();
;     ATT_XSECTION(true);
;     if constexpr (!(ABL & 4)) { const int tk = (t + 3 < NT) ? t + 3 : NT - 1, tv = (t + 2 < NT) ? t + 2 : NT - 1; ATT_LOAD_K(tk); ATT_LOAD_V(tv); }
;     ATT_BAR();
;     { const int tk_ = k0; k0 = k1; k1 = k2; k2 = tk_; const int tv_ = v0; v0 = v1; v1 = v2; v2 = tv_; }
	s_setprio 2
	s_waitcnt lgkmcnt(6)
	v_mfma_f32_32x32x16_bf16 v[18:33], v[98:101], v[18:21], 0
	ds_read_b64_tr_b16 v[46:47], v131 offset:512
	ds_read_b64_tr_b16 v[48:49], v131 offset:2560
	s_waitcnt lgkmcnt(6)
	v_mfma_f32_32x32x16_bf16 v[18:33], v[102:105], v[34:37], v[18:33]
	ds_read_b64_tr_b16 v[50:51], v131 offset:4608
	ds_read_b64_tr_b16 v[52:53], v131 offset:6656
	s_waitcnt lgkmcnt(6)
	v_mfma_f32_32x32x16_bf16 v[18:33], v[106:109], v[38:41], v[18:33]
	ds_read_b64_tr_b16 v[54:55], v131 offset:8704
	ds_read_b64_tr_b16 v[56:57], v131 offset:10752
	s_waitcnt lgkmcnt(6)
	v_mfma_f32_32x32x16_bf16 v[18:33], v[110:113], v[42:45], v[18:33]
	ds_read_b64_tr_b16 v[58:59], v131 offset:12800
	ds_read_b64_tr_b16 v[60:61], v131 offset:14848
	s_waitcnt lgkmcnt(6)
	v_mfma_f32_32x32x16_bf16 v[34:49], v[98:101], v[46:49], 0
	ds_read_b64_tr_b16 v[62:63], v131 offset:1024
	ds_read_b64_tr_b16 v[64:65], v131 offset:3072
	s_waitcnt lgkmcnt(6)
	v_mfma_f32_32x32x16_bf16 v[34:49], v[102:105], v[50:53], v[34:49]
	ds_read_b64_tr_b16 v[66:67], v131 offset:5120
	ds_read_b64_tr_b16 v[68:69], v131 offset:7168
	s_waitcnt lgkmcnt(6)
	v_mfma_f32_32x32x16_bf16 v[34:49], v[106:109], v[54:57], v[34:49]
	ds_read_b64_tr_b16 v[70:71], v131 offset:9216
	ds_read_b64_tr_b16 v[72:73], v131 offset:11264
	s_waitcnt lgkmcnt(6)
	v_mfma_f32_32x32x16_bf16 v[34:49], v[110:113], v[58:61], v[34:49]
	ds_read_b64_tr_b16 v[74:75], v131 offset:13312
	ds_read_b64_tr_b16 v[76:77], v131 offset:15360
	s_waitcnt lgkmcnt(6)
	v_mfma_f32_32x32x16_bf16 v[50:65], v[98:101], v[62:65], 0
	ds_read_b64_tr_b16 v[78:79], v131 offset:1536
	ds_read_b64_tr_b16 v[80:81], v131 offset:3584
	s_waitcnt lgkmcnt(6)
	v_mfma_f32_32x32x16_bf16 v[50:65], v[102:105], v[66:69], v[50:65]
	ds_read_b64_tr_b16 v[114:115], v131 offset:5632
	ds_read_b64_tr_b16 v[116:117], v131 offset:7680
	s_waitcnt lgkmcnt(6)
	v_mfma_f32_32x32x16_bf16 v[50:65], v[106:109], v[70:73], v[50:65]
	ds_read_b64_tr_b16 v[118:119], v131 offset:9728
	ds_read_b64_tr_b16 v[120:121], v131 offset:11776
	s_waitcnt lgkmcnt(6)
	v_mfma_f32_32x32x16_bf16 v[50:65], v[110:113], v[74:77], v[50:65]
	ds_read_b64_tr_b16 v[122:123], v131 offset:13824
	ds_read_b64_tr_b16 v[124:125], v131 offset:15872
	s_waitcnt lgkmcnt(6)
	v_mfma_f32_32x32x16_bf16 v[66:81], v[98:101], v[78:81], 0
	ds_read_b128 v[126:129], v172 offset:58368
	s_waitcnt lgkmcnt(5)
	v_mfma_f32_32x32x16_bf16 v[66:81], v[102:105], v[114:117], v[66:81]
	ds_read_b128 v[152:155], v172 offset:62976
	s_waitcnt lgkmcnt(4)
	v_mfma_f32_32x32x16_bf16 v[66:81], v[106:109], v[118:121], v[66:81]
	ds_read_b128 v[156:159], v172 offset:58400
	s_waitcnt lgkmcnt(3)
	v_mfma_f32_32x32x16_bf16 v[66:81], v[110:113], v[122:125], v[66:81]
	ds_read_b128 v[160:163], v172 offset:63008
	v_mfma_f32_4x4x4_16b_bf16 v[240:243], v[98:99], v[132:133], 0
	ds_read_b128 v[174:177], v172 offset:58432
	v_mfma_f32_4x4x4_16b_bf16 v[244:247], v[100:101], v[132:133], 0
	v_mfma_f32_4x4x4_16b_bf16 v[240:243], v[102:103], v[132:133], v[240:243]
	ds_read_b128 v[178:181], v172 offset:63040
	v_mfma_f32_4x4x4_16b_bf16 v[244:247], v[104:105], v[132:133], v[244:247]
	v_mfma_f32_4x4x4_16b_bf16 v[240:243], v[106:107], v[132:133], v[240:243]
	ds_read_b128 v[186:189], v172 offset:58464
	v_mfma_f32_4x4x4_16b_bf16 v[244:247], v[108:109], v[132:133], v[244:247]
	v_mfma_f32_4x4x4_16b_bf16 v[240:243], v[110:111], v[132:133], v[240:243]
	ds_read_b128 v[190:193], v172 offset:63072
	v_mfma_f32_4x4x4_16b_bf16 v[244:247], v[112:113], v[132:133], v[244:247]
	s_waitcnt lgkmcnt(7)
	v_mfma_f32_32x32x16_bf16 v[98:113], v[126:129], v[136:139], v[82:97]
	v_mov_b64_e32 v[128:129], v[96:97]
	v_mov_b64_e32 v[126:127], v[94:95]
	v_mov_b64_e32 v[124:125], v[92:93]
	v_mov_b64_e32 v[122:123], v[90:91]
	v_mov_b64_e32 v[120:121], v[88:89]
	v_mov_b64_e32 v[118:119], v[86:87]
	v_mov_b64_e32 v[116:117], v[84:85]
	v_mov_b64_e32 v[114:115], v[82:83]
	s_waitcnt lgkmcnt(6)
	s_nop 0
	v_mfma_f32_32x32x16_bf16 v[114:129], v[152:155], v[136:139], v[114:129]
	s_waitcnt lgkmcnt(5)
	v_mfma_f32_32x32x16_bf16 v[98:113], v[156:159], v[140:143], v[98:113]
	s_waitcnt lgkmcnt(4)
	v_mfma_f32_32x32x16_bf16 v[114:129], v[160:163], v[140:143], v[114:129]
	s_waitcnt lgkmcnt(3)
	v_mfma_f32_32x32x16_bf16 v[98:113], v[174:177], v[144:147], v[98:113]
	s_waitcnt lgkmcnt(2)
	v_mfma_f32_32x32x16_bf16 v[114:129], v[178:181], v[144:147], v[114:129]
	s_waitcnt lgkmcnt(1)
	v_mfma_f32_32x32x16_bf16 v[98:113], v[186:189], v[148:151], v[98:113]
	s_waitcnt lgkmcnt(0)
	v_mfma_f32_32x32x16_bf16 v[114:129], v[190:193], v[148:151], v[114:129]
	s_setprio 0
	s_mov_b32 s14, s10
	s_mov_b32 s15, s11
	buffer_load_dwordx4 v[224:227], v170, s[8:11], s85 offen
	buffer_load_dwordx4 v[228:231], v171, s[12:15], s83 offen
	buffer_load_dwordx4 v[232:235], v171, s[12:15], s86 offen
	s_barrier
	s_mov_b32 s95, 0x8000
	s_movk_i32 s15, 0x4000
	s_movk_i32 s18, 0x2400
	s_mov_b32 s94, 0
	s_movk_i32 s14, 0x4800
	s_mov_b32 s36, 0x70000
	s_mov_b32 s93, 0
	v_add_f32_e32 v173, 0, v114
	v_max3_f32 v174, v173, v98, v99
	v_max3_f32 v174, v174, v100, v101
	v_max3_f32 v174, v174, v102, v103
	v_max3_f32 v174, v174, v104, v105
	v_max3_f32 v174, v174, v106, v107
	v_max3_f32 v174, v174, v108, v109
	v_max3_f32 v174, v174, v110, v111
	v_max3_f32 v174, v174, v112, v113
	v_max3_f32 v173, v174, v115, v116
	v_max3_f32 v173, v173, v117, v118
	v_max3_f32 v173, v173, v119, v120
	v_max3_f32 v173, v173, v121, v122
	v_max3_f32 v173, v173, v123, v124
	v_max3_f32 v173, v173, v125, v126
	v_max3_f32 v173, v173, v127, v128
	v_max_f32 v173, v173, v129
.LBB0_282:
	s_mov_b32 s37, s15
	s_mov_b32 s96, s14
	v_cmp_ge_f32_e32 vcc, s60, v173
	s_cmp_eq_u64 vcc, exec
	s_cbranch_scc0 .LBB0_285
; #define ATT_SBAR() __builtin_amdgcn_sched_barrier(0)
; __device__ __forceinline__ unsigned cvtpk(float lo, float hi) { f32x2_t v = {lo, hi}; bf16x2_t b = __builtin_convertvector(v, bf16x2_t); return __builtin_bit_cast(unsigned, b); }
; #define ATT_PK4(P, BASE, OUT) do { u32x4 w = {cvtpk(P[BASE + 0], P[BASE + 1]), cvtpk(P[BASE + 2], P[BASE + 3]), cvtpk(P[BASE + 4], P[BASE + 5]), cvtpk(P[BASE + 6], P[BASE + 7])}; \
;     OUT = *reinterpret_cast<bf16x8*>(&w); } while (0)
; #define ATT_WRITE_K(so) do { *(bf16x8*)(K_lds + (so) + kswz<DQK>(kr, kc * 2)) = sk0; if constexpr (DQK == 128) *(bf16x8*)(K_lds + (so) + kswz<DQK>(32 + kr, kc * 2)) = sk1; } while (0)
; #define ATT_WRITE_V(so) do { *(bf16x8*)(V_lds + (so) + vst0) = sv0; *(bf16x8*)(V_lds + (so) + vst1) = sv1; } while (0)
; #define ATT_BAR() do { ATT_SBAR(); asm volatile("s_barrier" ::: "memory"); ATT_SBAR(); } while (0)
; #define ATT_VPAIR(buf, so, blk, ks) do { if constexpr (!(ABL & 8) && !(ABL & 32)) { buf[2 * (ks)] = vtr(vq0 + (so) + v_rd_off(blk, ks, 0)); buf[2 * (ks) + 1] = vtr(vq0 + (so) + v_rd_off(blk, ks, 1)); } } while (0)
; __device__ __forceinline__ void softmax_exp_pack(f32x16& p0, f32x16& p1, bf16x8& pa0, bf16x8& pa1, bf16x8& pa2, bf16x8& pa3) {
; #pragma unroll
;   for (int r = 0; r < 16; ++r) { p0[r] = __builtin_amdgcn_exp2f(p0[r]); p1[r] = __builtin_amdgcn_exp2f(p1[r]); }
;     ...
;   ATT_PK4(p0, 0, pa0); ATT_PK4(p0, 8, pa1); ATT_PK4(p1, 0, pa2); ATT_PK4(p1, 8, pa3);
;     ...
; }
;     ...
;   for (int t = 0; t + 1 < NT; ++t) {
;     if constexpr (ABL & 1) { u32x4 w0 = {cvtpk(p0[0], p0[1]), cvtpk(p0[2], p0[3]), cvtpk(p0[4], p0[5]), cvtpk(p0[6], p0[7])}, w1 = {cvtpk(p0[8], p0[9]), cvtpk(p0[10], p0[11]), cvtpk(p0[12], p0[13]), cvtpk(p0[14], p0[15])};
;         u32x4 w2 = {cvtpk(p1[0], p1[1]), cvtpk(p1[2], p1[3]), cvtpk(p1[4], p1[5]), cvtpk(p1[6], p1[7])}, w3 = {cvtpk(p1[8], p1[9]), cvtpk(p1[10], p1[11]), cvtpk(p1[12], p1[13]), cvtpk(p1[14], p1[15])};
;         pa0 = *reinterpret_cast<bf16x8*>(&w0); pa1 = *reinterpret_cast<bf16x8*>(&w1); pa2 = *reinterpret_cast<bf16x8*>(&w2); pa3 = *reinterpret_cast<bf16x8*>(&w3); }
;     else { ATT_SOFTMAX(t == 0); }
;     if constexpr (!(ABL & 4)) { ATT_WRITE_K(k2); ATT_WRITE_V(v1); }
;     ATT_SBAR();
; #pragma unroll
;     for (int ks = 0; ks < 4; ++ks) ATT_VPAIR(va, v0, 0, ks);
;     asm volatile("s_waitcnt lgkmcnt(8)" ::: "memory"); ATT_BAR();
;     ATT_XSECTION(true);
.LBB0_283:
	v_exp_f32_e32 v98, v98
	v_exp_f32_e32 v114, v114
	v_exp_f32_e32 v99, v99
	v_exp_f32_e32 v115, v115
	v_exp_f32_e32 v100, v100
	v_exp_f32_e32 v101, v101
	v_exp_f32_e32 v102, v102
	v_exp_f32_e32 v103, v103
	v_exp_f32_e32 v106, v106
	v_exp_f32_e32 v107, v107
	v_exp_f32_e32 v116, v116
	v_exp_f32_e32 v117, v117
	v_exp_f32_e32 v118, v118
	v_exp_f32_e32 v119, v119
	v_exp_f32_e32 v104, v104
	v_exp_f32_e32 v120, v120
	v_exp_f32_e32 v105, v105
	v_exp_f32_e32 v121, v121
	v_exp_f32_e32 v122, v122
	v_exp_f32_e32 v123, v123
	v_exp_f32_e32 v108, v108
	v_exp_f32_e32 v124, v124
	v_exp_f32_e32 v109, v109
	v_exp_f32_e32 v125, v125
	v_exp_f32_e32 v110, v110
	v_exp_f32_e32 v126, v126
	v_exp_f32_e32 v111, v111
	v_exp_f32_e32 v127, v127
	v_exp_f32_e32 v112, v112
	v_exp_f32_e32 v128, v128
	v_exp_f32_e32 v113, v113
	v_exp_f32_e32 v129, v129
	v_cvt_pk_bf16_f32 v2, v98, v99
	v_cvt_pk_bf16_f32 v3, v100, v101
	v_cvt_pk_bf16_f32 v4, v102, v103
	v_cvt_pk_bf16_f32 v6, v106, v107
	v_cvt_pk_bf16_f32 v10, v114, v115
	v_add_u32_e32 v114, s94, v169
	s_add_i32 s14, s95, 0
	s_waitcnt vmcnt(2)
	ds_write_b128 v114, v[224:227] offset:49152
	v_add_u32_e32 v114, s14, v167
	v_cvt_pk_bf16_f32 v5, v104, v105
	v_cvt_pk_bf16_f32 v7, v108, v109
	v_cvt_pk_bf16_f32 v8, v110, v111
	v_cvt_pk_bf16_f32 v9, v112, v113
	v_cvt_pk_bf16_f32 v11, v116, v117
	v_cvt_pk_bf16_f32 v12, v118, v119
	v_cvt_pk_bf16_f32 v13, v120, v121
	v_cvt_pk_bf16_f32 v14, v122, v123
	v_cvt_pk_bf16_f32 v15, v124, v125
	v_cvt_pk_bf16_f32 v16, v126, v127
	v_cvt_pk_bf16_f32 v17, v128, v129
	s_waitcnt vmcnt(1)
	ds_write_b128 v114, v[228:231]
	v_add_u32_e32 v114, s14, v168
	s_waitcnt vmcnt(0)
	ds_write_b128 v114, v[232:235]
	v_add_u32_e32 v249, s96, v172
	ds_read_b128 v[152:155], v249 offset:49152
	ds_read_b128 v[156:159], v249 offset:53760
	ds_read_b128 v[160:163], v249 offset:49184
	ds_read_b128 v[176:179], v249 offset:53792
	s_waitcnt lgkmcnt(4)
	s_barrier
	s_setprio 2
	s_waitcnt lgkmcnt(3)
	v_mfma_f32_32x32x16_bf16 v[98:113], v[152:155], v[136:139], v[82:97]
	ds_read_b128 v[180:183], v249 offset:49216
	s_waitcnt lgkmcnt(3)
	v_mfma_f32_32x32x16_bf16 v[114:129], v[156:159], v[136:139], v[82:97]
	ds_read_b128 v[186:189], v249 offset:53824
	v_add_u32_e32 v248, s37, v131
	s_waitcnt lgkmcnt(3)
	v_mfma_f32_32x32x16_bf16 v[98:113], v[160:163], v[140:143], v[98:113]
	ds_read_b128 v[190:193], v249 offset:49248
	ds_read_b64_tr_b16 v[198:199], v248
	ds_read_b64_tr_b16 v[200:201], v248 offset:2048
	s_waitcnt lgkmcnt(5)
	v_mfma_f32_32x32x16_bf16 v[114:129], v[176:179], v[140:143], v[114:129]
	ds_read_b128 v[194:197], v249 offset:53856
	ds_read_b64_tr_b16 v[212:213], v248 offset:4096
	ds_read_b64_tr_b16 v[214:215], v248 offset:6144
	s_waitcnt lgkmcnt(7)
	v_mfma_f32_32x32x16_bf16 v[98:113], v[180:183], v[144:147], v[98:113]
	ds_read_b64_tr_b16 v[216:217], v248 offset:8192
	ds_read_b64_tr_b16 v[218:219], v248 offset:10240
	s_waitcnt lgkmcnt(8)
	v_mfma_f32_32x32x16_bf16 v[114:129], v[186:189], v[144:147], v[114:129]
	ds_read_b64_tr_b16 v[220:221], v248 offset:12288
	ds_read_b64_tr_b16 v[222:223], v248 offset:14336
	s_waitcnt lgkmcnt(9)
	v_mfma_f32_32x32x16_bf16 v[98:113], v[190:193], v[148:151], v[98:113]
	s_waitcnt lgkmcnt(6)
	v_mfma_f32_32x32x16_bf16 v[114:129], v[194:197], v[148:151], v[114:129]
	v_mfma_f32_32x32x16_bf16 v[18:33], v[2:5], v[198:201], v[18:33]
	ds_read_b64_tr_b16 v[236:237], v248 offset:512
	ds_read_b64_tr_b16 v[238:239], v248 offset:2560
	s_waitcnt lgkmcnt(6)
	v_mfma_f32_32x32x16_bf16 v[18:33], v[6:9], v[212:215], v[18:33]
	ds_read_b64_tr_b16 v[198:199], v248 offset:4608
	ds_read_b64_tr_b16 v[200:201], v248 offset:6656
	s_waitcnt lgkmcnt(6)
	v_mfma_f32_32x32x16_bf16 v[18:33], v[10:13], v[216:219], v[18:33]
	ds_read_b64_tr_b16 v[212:213], v248 offset:8704
	ds_read_b64_tr_b16 v[214:215], v248 offset:10752
	s_waitcnt lgkmcnt(6)
	v_mfma_f32_32x32x16_bf16 v[18:33], v[14:17], v[220:223], v[18:33]
	ds_read_b64_tr_b16 v[216:217], v248 offset:12800
	ds_read_b64_tr_b16 v[218:219], v248 offset:14848
	v_max3_f32 v249, v98, v99, v100
	s_waitcnt lgkmcnt(6)
	v_mfma_f32_32x32x16_bf16 v[34:49], v[2:5], v[236:239], v[34:49]
	ds_read_b64_tr_b16 v[220:221], v248 offset:1024
	ds_read_b64_tr_b16 v[222:223], v248 offset:3072
	v_max3_f32 v173, v114, v115, v116
	s_waitcnt lgkmcnt(6)
	v_mfma_f32_32x32x16_bf16 v[34:49], v[6:9], v[198:201], v[34:49]
	ds_read_b64_tr_b16 v[236:237], v248 offset:5120
	ds_read_b64_tr_b16 v[238:239], v248 offset:7168
	v_max3_f32 v249, v249, v101, v102
	s_waitcnt lgkmcnt(6)
	v_mfma_f32_32x32x16_bf16 v[34:49], v[10:13], v[212:215], v[34:49]
	ds_read_b64_tr_b16 v[198:199], v248 offset:9216
	ds_read_b64_tr_b16 v[200:201], v248 offset:11264
	v_max3_f32 v173, v173, v117, v118
	s_waitcnt lgkmcnt(6)
	v_mfma_f32_32x32x16_bf16 v[34:49], v[14:17], v[216:219], v[34:49]
	ds_read_b64_tr_b16 v[212:213], v248 offset:13312
	ds_read_b64_tr_b16 v[214:215], v248 offset:15360
	v_max3_f32 v249, v249, v103, v104
	s_waitcnt lgkmcnt(6)
	v_mfma_f32_32x32x16_bf16 v[50:65], v[2:5], v[220:223], v[50:65]
	ds_read_b64_tr_b16 v[216:217], v248 offset:1536
	ds_read_b64_tr_b16 v[218:219], v248 offset:3584
	v_max3_f32 v173, v173, v119, v120
	s_waitcnt lgkmcnt(6)
; #define ATT_SBAR() __builtin_amdgcn_sched_barrier(0)
; __device__ __forceinline__ unsigned cvtpk(float lo, float hi) { f32x2_t v = {lo, hi}; bf16x2_t b = __builtin_convertvector(v, bf16x2_t); return __builtin_bit_cast(unsigned, b); }
; #define ATT_LOAD_K(t) do { const unsigned so_ = (unsigned)(t) * (unsigned)(KVBLK * LDK * 2); sk0 = __builtin_bit_cast(bf16x8, __builtin_amdgcn_raw_buffer_load_b128(krs, koff, so_, 0)); \
;     if constexpr (DQK == 128) sk1 = __builtin_bit_cast(bf16x8, __builtin_amdgcn_raw_buffer_load_b128(krs, koff, so_ + (unsigned)(32 * LDK * 2), 0)); } while (0)
; #define ATT_LOAD_V(t) do { const unsigned so_ = (unsigned)(t) * (unsigned)(KVBLK * LDV * 2); sv0 = __builtin_bit_cast(bf16x8, __builtin_amdgcn_raw_buffer_load_b128(vrs, voff, so_, 0)); \
;     sv1 = __builtin_bit_cast(bf16x8, __builtin_amdgcn_raw_buffer_load_b128(vrs, voff, so_ + (unsigned)(32 * LDV * 2), 0)); } while (0)
; #define ATT_WRITE_K(so) do { *(bf16x8*)(K_lds + (so) + kswz<DQK>(kr, kc * 2)) = sk0; if constexpr (DQK == 128) *(bf16x8*)(K_lds + (so) + kswz<DQK>(32 + kr, kc * 2)) = sk1; } while (0)
;     ...
;   for (int t = 0; t + 1 < NT; ++t) {
;     if constexpr (ABL & 1) { u32x4 w0 = {cvtpk(p0[0], p0[1]), cvtpk(p0[2], p0[3]), cvtpk(p0[4], p0[5]), cvtpk(p0[6], p0[7])}, w1 = {cvtpk(p0[8], p0[9]), cvtpk(p0[10], p0[11]), cvtpk(p0[12], p0[13]), cvtpk(p0[14], p0[15])};
;         u32x4 w2 = {cvtpk(p1[0], p1[1]), cvtpk(p1[2], p1[3]), cvtpk(p1[4], p1[5]), cvtpk(p1[6], p1[7])}, w3 = {cvtpk(p1[8], p1[9]), cvtpk(p1[10], p1[11]), cvtpk(p1[12], p1[13]), cvtpk(p1[14], p1[15])};
;         pa0 = *reinterpret_cast<bf16x8*>(&w0); pa1 = *reinterpret_cast<bf16x8*>(&w1); pa2 = *reinterpret_cast<bf16x8*>(&w2); pa3 = *reinterpret_cast<bf16x8*>(&w3); }
;     else { ATT_SOFTMAX(t == 0); }
;     if constexpr (!(ABL & 4)) { ATT_WRITE_K(k2); ATT_WRITE_V(v1); }
;     ATT_SBAR();
; #pragma unroll
;     for (int ks = 0; ks < 4; ++ks) ATT_VPAIR(va, v0, 0, ks);
;     asm volatile("s_waitcnt lgkmcnt(8)" ::: "memory"); ATT_BAR();
;     ATT_XSECTION(true);
;     if constexpr (!(ABL & 4)) { const int tk = (t + 3 < NT) ? t + 3 : NT - 1, tv = (t + 2 < NT) ? t + 2 : NT - 1; ATT_LOAD_K(tk); ATT_LOAD_V(tv); }
;     ATT_BAR();
;     { const int tk_ = k0; k0 = k1; k1 = k2; k2 = tk_; const int tv_ = v0; v0 = v1; v1 = v2; v2 = tv_; }
	v_mfma_f32_32x32x16_bf16 v[50:65], v[6:9], v[236:239], v[50:65]
	ds_read_b64_tr_b16 v[220:221], v248 offset:5632
	ds_read_b64_tr_b16 v[222:223], v248 offset:7680
	v_max3_f32 v249, v249, v105, v106
	s_waitcnt lgkmcnt(6)
	v_mfma_f32_32x32x16_bf16 v[50:65], v[10:13], v[198:201], v[50:65]
	ds_read_b64_tr_b16 v[236:237], v248 offset:9728
	ds_read_b64_tr_b16 v[238:239], v248 offset:11776
	v_max3_f32 v173, v173, v121, v122
	s_waitcnt lgkmcnt(6)
	v_mfma_f32_32x32x16_bf16 v[50:65], v[14:17], v[212:215], v[50:65]
	ds_read_b64_tr_b16 v[198:199], v248 offset:13824
	ds_read_b64_tr_b16 v[200:201], v248 offset:15872
	v_max3_f32 v249, v249, v107, v108
	s_waitcnt lgkmcnt(6)
	v_mfma_f32_32x32x16_bf16 v[66:81], v[2:5], v[216:219], v[66:81]
	v_max3_f32 v173, v173, v123, v124
	s_min_u32 s14, s97, 0x7c
	s_lshl_b32 s14, s14, 17
	s_add_i32 s14, s14, 0x60000
	buffer_load_dwordx4 v[224:227], v170, s[8:11], s14 offen
	s_waitcnt lgkmcnt(4)
	v_mfma_f32_32x32x16_bf16 v[66:81], v[6:9], v[220:223], v[66:81]
	v_max3_f32 v249, v249, v109, v110
	s_add_i32 s19, s36, 0xffff0000
	s_mov_b32 s14, s10
	s_mov_b32 s15, s11
	buffer_load_dwordx4 v[228:231], v171, s[12:15], s19 offen
	s_waitcnt lgkmcnt(2)
	v_mfma_f32_32x32x16_bf16 v[66:81], v[10:13], v[236:239], v[66:81]
	v_max3_f32 v173, v173, v125, v126
	buffer_load_dwordx4 v[232:235], v171, s[12:15], s36 offen
	s_waitcnt lgkmcnt(0)
	v_mfma_f32_32x32x16_bf16 v[66:81], v[14:17], v[198:201], v[66:81]
	v_max3_f32 v249, v249, v111, v112
	v_mfma_f32_4x4x4_16b_bf16 v[240:243], v[2:3], v[132:133], v[240:243]
	v_max3_f32 v173, v173, v127, v128
	v_mfma_f32_4x4x4_16b_bf16 v[244:247], v[4:5], v[132:133], v[244:247]
	v_mfma_f32_4x4x4_16b_bf16 v[240:243], v[6:7], v[132:133], v[240:243]
	v_max_f32 v249, v249, v113
	v_mfma_f32_4x4x4_16b_bf16 v[244:247], v[8:9], v[132:133], v[244:247]
	v_mfma_f32_4x4x4_16b_bf16 v[240:243], v[10:11], v[132:133], v[240:243]
	v_max_f32 v173, v173, v129
	v_mfma_f32_4x4x4_16b_bf16 v[244:247], v[12:13], v[132:133], v[244:247]
	v_mfma_f32_4x4x4_16b_bf16 v[240:243], v[14:15], v[132:133], v[240:243]
	v_max_f32 v173, v173, v249
	v_mfma_f32_4x4x4_16b_bf16 v[244:247], v[16:17], v[132:133], v[244:247]
	s_setprio 0
	s_barrier
	s_add_i32 s36, s36, 0x20000
	s_add_i32 s97, s97, 1
	s_cmpk_eq_i32 s97, 0x7e
	s_cbranch_scc1 .LBB0_290
	s_mov_b32 s14, s94
	s_mov_b32 s94, s18
	s_mov_b32 s18, s96
	s_mov_b32 s15, s95
	s_mov_b32 s95, s93
	s_mov_b32 s93, s37
	s_branch .LBB0_282
.LBB0_285:
	v_mov_b32_e32 v174, v173
	s_nop 1
	v_permlane32_swap_b32_e32 v173, v174
	v_max3_f32 v173, v173, v174, 0
	v_exp_f32_e64 v174, -v173
	s_nop 4
	s_nop 0
	v_cmp_gt_f32_e32 vcc, 1.0, v174
	s_cbranch_vccz .LBB0_289
	v_mul_f32_dpp v240, v174, v240 quad_perm:[0,0,0,0] row_mask:0xf bank_mask:0xf
	v_mul_f32_dpp v241, v174, v241 quad_perm:[1,1,1,1] row_mask:0xf bank_mask:0xf
	v_mul_f32_dpp v242, v174, v242 quad_perm:[2,2,2,2] row_mask:0xf bank_mask:0xf
	v_mul_f32_dpp v243, v174, v243 quad_perm:[3,3,3,3] row_mask:0xf bank_mask:0xf
	v_mul_f32_dpp v244, v174, v244 quad_perm:[0,0,0,0] row_mask:0xf bank_mask:0xf
	v_mul_f32_dpp v245, v174, v245 quad_perm:[1,1,1,1] row_mask:0xf bank_mask:0xf
	v_mul_f32_dpp v246, v174, v246 quad_perm:[2,2,2,2] row_mask:0xf bank_mask:0xf
	v_mul_f32_dpp v247, v174, v247 quad_perm:[3,3,3,3] row_mask:0xf bank_mask:0xf
	s_and_saveexec_b64 s[14:15], s[4:5]
	ds_write_b32 v165, v174
	s_or_b64 exec, exec, s[14:15]
	s_waitcnt lgkmcnt(0)
	v_add_u32_e32 v182, s6, v184
	ds_read_b128 v[174:177], v182 offset:96
	ds_read_b128 v[178:181], v182 offset:64
	ds_read_b128 v[186:189], v182 offset:32
	ds_read_b128 v[190:193], v182
	s_waitcnt lgkmcnt(3)
	v_pk_mul_f32 v[30:31], v[30:31], v[174:175]
	s_waitcnt lgkmcnt(2)
	v_pk_mul_f32 v[26:27], v[26:27], v[178:179]
	s_waitcnt lgkmcnt(1)
	v_pk_mul_f32 v[22:23], v[22:23], v[186:187]
	v_pk_mul_f32 v[32:33], v[32:33], v[176:177]
	v_pk_mul_f32 v[28:29], v[28:29], v[180:181]
	v_pk_mul_f32 v[24:25], v[24:25], v[188:189]
	s_waitcnt lgkmcnt(0)
	v_pk_mul_f32 v[20:21], v[20:21], v[192:193]
	v_pk_mul_f32 v[18:19], v[18:19], v[190:191]
	v_pk_mul_f32 v[46:47], v[46:47], v[174:175]
	v_pk_mul_f32 v[42:43], v[42:43], v[178:179]
	v_pk_mul_f32 v[38:39], v[38:39], v[186:187]
	v_pk_mul_f32 v[48:49], v[48:49], v[176:177]
	v_pk_mul_f32 v[44:45], v[44:45], v[180:181]
	v_pk_mul_f32 v[40:41], v[40:41], v[188:189]
	v_pk_mul_f32 v[36:37], v[36:37], v[192:193]
	v_pk_mul_f32 v[34:35], v[34:35], v[190:191]
	v_pk_mul_f32 v[62:63], v[62:63], v[174:175]
	v_pk_mul_f32 v[58:59], v[58:59], v[178:179]
	v_pk_mul_f32 v[54:55], v[54:55], v[186:187]
	v_pk_mul_f32 v[64:65], v[64:65], v[176:177]
	v_pk_mul_f32 v[60:61], v[60:61], v[180:181]
	v_pk_mul_f32 v[56:57], v[56:57], v[188:189]
	v_pk_mul_f32 v[52:53], v[52:53], v[192:193]
	v_pk_mul_f32 v[50:51], v[50:51], v[190:191]
	v_pk_mul_f32 v[78:79], v[78:79], v[174:175]
	v_pk_mul_f32 v[74:75], v[74:75], v[178:179]
	v_pk_mul_f32 v[70:71], v[70:71], v[186:187]
	v_pk_mul_f32 v[80:81], v[80:81], v[176:177]
	v_pk_mul_f32 v[76:77], v[76:77], v[180:181]
	v_pk_mul_f32 v[72:73], v[72:73], v[188:189]
	v_pk_mul_f32 v[68:69], v[68:69], v[192:193]
	v_pk_mul_f32 v[66:67], v[66:67], v[190:191]

; #define ATT_SBAR() __builtin_amdgcn_sched_barrier(0)
; __device__ __forceinline__ unsigned cvtpk(float lo, float hi) { f32x2_t v = {lo, hi}; bf16x2_t b = __builtin_convertvector(v, bf16x2_t); return __builtin_bit_cast(unsigned, b); }
; #define ATT_PK4(P, BASE, OUT) do { u32x4 w = {cvtpk(P[BASE + 0], P[BASE + 1]), cvtpk(P[BASE + 2], P[BASE + 3]), cvtpk(P[BASE + 4], P[BASE + 5]), cvtpk(P[BASE + 6], P[BASE + 7])}; \
;     OUT = *reinterpret_cast<bf16x8*>(&w); } while (0)
; #define ATT_LOAD_K(t) do { const unsigned so_ = (unsigned)(t) * (unsigned)(KVBLK * LDK * 2); sk0 = __builtin_bit_cast(bf16x8, __builtin_amdgcn_raw_buffer_load_b128(krs, koff, so_, 0)); \
;     if constexpr (DQK == 128) sk1 = __builtin_bit_cast(bf16x8, __builtin_amdgcn_raw_buffer_load_b128(krs, koff, so_ + (unsigned)(32 * LDK * 2), 0)); } while (0)
; __device__ __forceinline__ void softmax_exp_pack(f32x16& p0, f32x16& p1, bf16x8& pa0, bf16x8& pa1, bf16x8& pa2, bf16x8& pa3) {
; #pragma unroll
;   for (int r = 0; r < 16; ++r) { p0[r] = __builtin_amdgcn_exp2f(p0[r]); p1[r] = __builtin_amdgcn_exp2f(p1[r]); }
;     ...
;   ATT_PK4(p0, 0, pa0); ATT_PK4(p0, 8, pa1); ATT_PK4(p1, 0, pa2); ATT_PK4(p1, 8, pa3);
;     ...
; }
;     ...
;   for (int t = 0; t + 1 < NT; ++t) {
;     if constexpr (ABL & 1) { u32x4 w0 = {cvtpk(p0[0], p0[1]), cvtpk(p0[2], p0[3]), cvtpk(p0[4], p0[5]), cvtpk(p0[6], p0[7])}, w1 = {cvtpk(p0[8], p0[9]), cvtpk(p0[10], p0[11]), cvtpk(p0[12], p0[13]), cvtpk(p0[14], p0[15])};
;         u32x4 w2 = {cvtpk(p1[0], p1[1]), cvtpk(p1[2], p1[3]), cvtpk(p1[4], p1[5]), cvtpk(p1[6], p1[7])}, w3 = {cvtpk(p1[8], p1[9]), cvtpk(p1[10], p1[11]), cvtpk(p1[12], p1[13]), cvtpk(p1[14], p1[15])};
;         pa0 = *reinterpret_cast<bf16x8*>(&w0); pa1 = *reinterpret_cast<bf16x8*>(&w1); pa2 = *reinterpret_cast<bf16x8*>(&w2); pa3 = *reinterpret_cast<bf16x8*>(&w3); }
;     else { ATT_SOFTMAX(t == 0); }
;     if constexpr (!(ABL & 4)) { ATT_WRITE_K(k2); ATT_WRITE_V(v1); }
;     ATT_SBAR();
; #pragma unroll
;     for (int ks = 0; ks < 4; ++ks) ATT_VPAIR(va, v0, 0, ks);
;     asm volatile("s_waitcnt lgkmcnt(8)" ::: "memory"); ATT_BAR();
;     ATT_XSECTION(true);
;     if constexpr (!(ABL & 4)) { const int tk = (t + 3 < NT) ? t + 3 : NT - 1, tv = (t + 2 < NT) ? t + 2 : NT - 1; ATT_LOAD_K(tk); ATT_LOAD_V(tv); }
;     ATT_BAR();
;     { const int tk_ = k0; k0 = k1; k1 = k2; k2 = tk_; const int tv_ = v0; v0 = v1; v1 = v2; v2 = tv_; }
.LBB0_291:
	v_exp_f32_e32 v98, v98
	v_exp_f32_e32 v114, v114
	v_exp_f32_e32 v99, v99
	v_exp_f32_e32 v115, v115
	v_exp_f32_e32 v100, v100
	v_exp_f32_e32 v101, v101
	v_exp_f32_e32 v102, v102
	v_exp_f32_e32 v103, v103
	v_exp_f32_e32 v106, v106
	v_exp_f32_e32 v107, v107
	v_exp_f32_e32 v116, v116
	v_exp_f32_e32 v117, v117
	v_exp_f32_e32 v118, v118
	v_exp_f32_e32 v119, v119
	v_exp_f32_e32 v104, v104
	v_exp_f32_e32 v120, v120
	v_exp_f32_e32 v105, v105
	v_exp_f32_e32 v121, v121
	v_exp_f32_e32 v122, v122
	v_exp_f32_e32 v123, v123
	v_exp_f32_e32 v108, v108
	v_exp_f32_e32 v124, v124
	v_exp_f32_e32 v109, v109
	v_exp_f32_e32 v125, v125
	v_exp_f32_e32 v110, v110
	v_exp_f32_e32 v126, v126
	v_exp_f32_e32 v111, v111
	v_exp_f32_e32 v127, v127
	v_exp_f32_e32 v112, v112
	v_exp_f32_e32 v128, v128
	v_exp_f32_e32 v113, v113
	v_exp_f32_e32 v129, v129
	v_cvt_pk_bf16_f32 v98, v98, v99
	v_cvt_pk_bf16_f32 v99, v100, v101
	v_cvt_pk_bf16_f32 v100, v102, v103
	v_cvt_pk_bf16_f32 v102, v106, v107
	v_cvt_pk_bf16_f32 v106, v114, v115
	v_add_u32_e32 v114, s18, v169
	s_add_i32 s9, s93, 0
	s_waitcnt vmcnt(2)
	ds_write_b128 v114, v[224:227] offset:49152
	v_add_u32_e32 v114, s9, v167
	v_cvt_pk_bf16_f32 v101, v104, v105
	v_cvt_pk_bf16_f32 v103, v108, v109
	v_cvt_pk_bf16_f32 v104, v110, v111
	v_cvt_pk_bf16_f32 v105, v112, v113
	v_cvt_pk_bf16_f32 v107, v116, v117
	v_cvt_pk_bf16_f32 v108, v118, v119
	v_cvt_pk_bf16_f32 v109, v120, v121
	v_cvt_pk_bf16_f32 v110, v122, v123
	v_cvt_pk_bf16_f32 v111, v124, v125
	v_cvt_pk_bf16_f32 v112, v126, v127
	v_cvt_pk_bf16_f32 v113, v128, v129
	s_waitcnt vmcnt(1)
	ds_write_b128 v114, v[228:231]
	v_add_u32_e32 v114, s9, v168
	s_waitcnt vmcnt(0)
	ds_write_b128 v114, v[232:235]
	v_add_u32_e32 v156, s95, v131
	ds_read_b64_tr_b16 v[114:115], v156
	ds_read_b64_tr_b16 v[116:117], v156 offset:2048
	ds_read_b64_tr_b16 v[118:119], v156 offset:4096
	ds_read_b64_tr_b16 v[120:121], v156 offset:6144
	ds_read_b64_tr_b16 v[122:123], v156 offset:8192
	ds_read_b64_tr_b16 v[124:125], v156 offset:10240
	ds_read_b64_tr_b16 v[126:127], v156 offset:12288
	ds_read_b64_tr_b16 v[128:129], v156 offset:14336
	s_waitcnt lgkmcnt(8)
	s_barrier
	s_setprio 2
	s_waitcnt lgkmcnt(6)
	v_mfma_f32_32x32x16_bf16 v[18:33], v[98:101], v[114:117], v[18:33]
	ds_read_b64_tr_b16 v[152:153], v156 offset:512
	ds_read_b64_tr_b16 v[154:155], v156 offset:2560
	s_waitcnt lgkmcnt(6)
	v_mfma_f32_32x32x16_bf16 v[18:33], v[102:105], v[118:121], v[18:33]
	ds_read_b64_tr_b16 v[114:115], v156 offset:4608
	ds_read_b64_tr_b16 v[116:117], v156 offset:6656
	s_waitcnt lgkmcnt(6)
	v_mfma_f32_32x32x16_bf16 v[18:33], v[106:109], v[122:125], v[18:33]
	ds_read_b64_tr_b16 v[118:119], v156 offset:8704
	ds_read_b64_tr_b16 v[120:121], v156 offset:10752
	s_waitcnt lgkmcnt(6)
	v_mfma_f32_32x32x16_bf16 v[18:33], v[110:113], v[126:129], v[18:33]
	ds_read_b64_tr_b16 v[122:123], v156 offset:12800
	ds_read_b64_tr_b16 v[124:125], v156 offset:14848
	s_waitcnt lgkmcnt(6)
	v_mfma_f32_32x32x16_bf16 v[34:49], v[98:101], v[152:155], v[34:49]
	ds_read_b64_tr_b16 v[126:127], v156 offset:1024
	ds_read_b64_tr_b16 v[128:129], v156 offset:3072
	s_waitcnt lgkmcnt(6)
	v_mfma_f32_32x32x16_bf16 v[34:49], v[102:105], v[114:117], v[34:49]
	ds_read_b64_tr_b16 v[152:153], v156 offset:5120
	ds_read_b64_tr_b16 v[154:155], v156 offset:7168
	s_waitcnt lgkmcnt(6)
	v_mfma_f32_32x32x16_bf16 v[34:49], v[106:109], v[118:121], v[34:49]
	ds_read_b64_tr_b16 v[114:115], v156 offset:9216
	ds_read_b64_tr_b16 v[116:117], v156 offset:11264
	s_waitcnt lgkmcnt(6)
	v_mfma_f32_32x32x16_bf16 v[34:49], v[110:113], v[122:125], v[34:49]
	ds_read_b64_tr_b16 v[118:119], v156 offset:13312
	ds_read_b64_tr_b16 v[120:121], v156 offset:15360
	s_waitcnt lgkmcnt(6)
	v_mfma_f32_32x32x16_bf16 v[50:65], v[98:101], v[126:129], v[50:65]
	ds_read_b64_tr_b16 v[122:123], v156 offset:1536
	ds_read_b64_tr_b16 v[124:125], v156 offset:3584
	s_waitcnt lgkmcnt(6)
	v_mfma_f32_32x32x16_bf16 v[50:65], v[102:105], v[152:155], v[50:65]
	ds_read_b64_tr_b16 v[126:127], v156 offset:5632
	ds_read_b64_tr_b16 v[128:129], v156 offset:7680
	s_waitcnt lgkmcnt(6)
	v_mfma_f32_32x32x16_bf16 v[50:65], v[106:109], v[114:117], v[50:65]
	ds_read_b64_tr_b16 v[152:153], v156 offset:9728
	ds_read_b64_tr_b16 v[154:155], v156 offset:11776
	s_waitcnt lgkmcnt(6)
	v_mfma_f32_32x32x16_bf16 v[50:65], v[110:113], v[118:121], v[50:65]
	ds_read_b64_tr_b16 v[114:115], v156 offset:13824
	ds_read_b64_tr_b16 v[116:117], v156 offset:15872
	s_waitcnt lgkmcnt(6)
	v_mfma_f32_32x32x16_bf16 v[66:81], v[98:101], v[122:125], v[66:81]
	v_add3_u32 v166, v166, s94, v184
	ds_read_b128 v[118:121], v166 offset:49152
	s_waitcnt lgkmcnt(5)
	v_mfma_f32_32x32x16_bf16 v[66:81], v[102:105], v[126:129], v[66:81]
	ds_read_b128 v[122:125], v166 offset:53760
	s_waitcnt lgkmcnt(4)
	v_mfma_f32_32x32x16_bf16 v[66:81], v[106:109], v[152:155], v[66:81]
	ds_read_b128 v[126:129], v166 offset:49184
	s_waitcnt lgkmcnt(3)
	v_mfma_f32_32x32x16_bf16 v[66:81], v[110:113], v[114:117], v[66:81]
	ds_read_b128 v[152:155], v166 offset:53792
	v_mfma_f32_4x4x4_16b_bf16 v[240:243], v[98:99], v[132:133], v[240:243]
	ds_read_b128 v[114:117], v166 offset:49216
	v_mfma_f32_4x4x4_16b_bf16 v[244:247], v[100:101], v[132:133], v[244:247]
	v_mfma_f32_4x4x4_16b_bf16 v[240:243], v[102:103], v[132:133], v[240:243]
	ds_read_b128 v[156:159], v166 offset:53824
	v_mfma_f32_4x4x4_16b_bf16 v[244:247], v[104:105], v[132:133], v[244:247]
	v_mfma_f32_4x4x4_16b_bf16 v[240:243], v[106:107], v[132:133], v[240:243]
	ds_read_b128 v[160:163], v166 offset:49248
	v_mfma_f32_4x4x4_16b_bf16 v[244:247], v[108:109], v[132:133], v[244:247]
	v_mfma_f32_4x4x4_16b_bf16 v[240:243], v[110:111], v[132:133], v[240:243]
	ds_read_b128 v[166:169], v166 offset:53856
	v_mfma_f32_4x4x4_16b_bf16 v[244:247], v[112:113], v[132:133], v[244:247]
	s_waitcnt lgkmcnt(7)
	v_mfma_f32_32x32x16_bf16 v[98:113], v[118:121], v[136:139], v[82:97]
	s_waitcnt lgkmcnt(6)
	v_mfma_f32_32x32x16_bf16 v[82:97], v[122:125], v[136:139], v[82:97]
	s_waitcnt lgkmcnt(5)
	v_mfma_f32_32x32x16_bf16 v[98:113], v[126:129], v[140:143], v[98:113]
	s_waitcnt lgkmcnt(4)
	v_mfma_f32_32x32x16_bf16 v[82:97], v[152:155], v[140:143], v[82:97]
	s_waitcnt lgkmcnt(3)
	v_mfma_f32_32x32x16_bf16 v[98:113], v[114:117], v[144:147], v[98:113]
	s_waitcnt lgkmcnt(2)
	v_mfma_f32_32x32x16_bf16 v[82:97], v[156:159], v[144:147], v[82:97]
	s_waitcnt lgkmcnt(1)
	v_mfma_f32_32x32x16_bf16 v[98:113], v[160:163], v[148:151], v[98:113]
	s_waitcnt lgkmcnt(0)
	v_mfma_f32_32x32x16_bf16 v[82:97], v[166:169], v[148:151], v[82:97]
	s_setprio 0
	s_barrier
; #define ATT_BAR() do { ATT_SBAR(); asm volatile("s_barrier" ::: "memory"); ATT_SBAR(); } while (0)
; #define ATT_SOFTMAX(first_) do { const float pm_ = softmax_rowmax(p0, p1); \
;     if (__builtin_expect((first_) || !__all(pm_ <= THRL), 0)) { const float al_ = softmax_shift(p0, p1, negm, pm_, (first_)); ATT_RESC(al_); } \
;     softmax_exp_pack(p0, p1, pa0, pa1, pa2, pa3); } while (0)
; #define ATT_VPAIR(buf, so, blk, ks) do { if constexpr (!(ABL & 8) && !(ABL & 32)) { buf[2 * (ks)] = vtr(vq0 + (so) + v_rd_off(blk, ks, 0)); buf[2 * (ks) + 1] = vtr(vq0 + (so) + v_rd_off(blk, ks, 1)); } } while (0)
;     ...
;   ATT_SOFTMAX(false);
; #pragma unroll
;   for (int ks = 0; ks < 4; ++ks) ATT_VPAIR(va, v0, 0, ks);
;   asm volatile("s_waitcnt lgkmcnt(0)" ::: "memory"); ATT_BAR();
;   ATT_XSECTION(false);
;   ATT_BAR();
;   if (grp == 0) ATT_BAR();
	s_nop 10
	v_add_f32_e32 v114, 0, v82
	v_max3_f32 v115, v114, v98, v99
	v_max3_f32 v115, v115, v100, v101
	v_max3_f32 v115, v115, v102, v103
	v_max3_f32 v115, v115, v104, v105
	v_max3_f32 v115, v115, v106, v107
	v_max3_f32 v115, v115, v108, v109
	v_max3_f32 v115, v115, v110, v111
	v_max3_f32 v115, v115, v112, v113
	s_nop 0
	v_max3_f32 v114, v115, v83, v84
	v_max3_f32 v114, v114, v85, v86
	v_max3_f32 v114, v114, v87, v88
	v_max3_f32 v114, v114, v89, v90
	v_max3_f32 v114, v114, v91, v92
	v_max3_f32 v114, v114, v93, v94
	v_max3_f32 v114, v114, v95, v96
	v_max_f32 v114, v114, v97
	s_nop 0
	v_cmp_ge_f32_e32 vcc, s60, v114
	s_cmp_lg_u64 vcc, exec
	s_cbranch_scc1 .LBB0_324
.LBB0_292:
	v_exp_f32_e32 v98, v98
	v_exp_f32_e32 v114, v82
	v_exp_f32_e32 v82, v99
	v_exp_f32_e32 v99, v83
	v_exp_f32_e32 v83, v100
	v_exp_f32_e32 v100, v84
	v_exp_f32_e32 v84, v101
	v_exp_f32_e32 v101, v85
	v_exp_f32_e32 v85, v102
	v_exp_f32_e32 v102, v86
	v_exp_f32_e32 v86, v103
	v_exp_f32_e32 v103, v87
	v_exp_f32_e32 v87, v104
	v_exp_f32_e32 v104, v88
	v_exp_f32_e32 v88, v105
	v_exp_f32_e32 v105, v89
	v_exp_f32_e32 v89, v106
	v_exp_f32_e32 v106, v90
	v_exp_f32_e32 v90, v107
	v_exp_f32_e32 v107, v91
	v_exp_f32_e32 v91, v108
	v_exp_f32_e32 v108, v92
	v_exp_f32_e32 v92, v109
	v_exp_f32_e32 v109, v93
	v_exp_f32_e32 v93, v110
	v_exp_f32_e32 v110, v94
	v_exp_f32_e32 v94, v111
	v_exp_f32_e32 v111, v95
	v_exp_f32_e32 v95, v112
	v_exp_f32_e32 v112, v96
	v_exp_f32_e32 v96, v113
	v_exp_f32_e32 v97, v97
	v_add_u32_e32 v118, s93, v131
	v_cvt_pk_bf16_f32 v82, v98, v82
	v_cvt_pk_bf16_f32 v83, v83, v84
	v_cvt_pk_bf16_f32 v84, v85, v86
	v_cvt_pk_bf16_f32 v85, v87, v88
	v_cvt_pk_bf16_f32 v86, v89, v90
	v_cvt_pk_bf16_f32 v87, v91, v92
	v_cvt_pk_bf16_f32 v88, v93, v94
	v_cvt_pk_bf16_f32 v89, v95, v96
	v_cvt_pk_bf16_f32 v90, v114, v99
	v_cvt_pk_bf16_f32 v91, v100, v101
	v_cvt_pk_bf16_f32 v92, v102, v103
	v_cvt_pk_bf16_f32 v93, v104, v105
	v_cvt_pk_bf16_f32 v94, v106, v107
	v_cvt_pk_bf16_f32 v95, v108, v109
	v_cvt_pk_bf16_f32 v96, v110, v111
	v_cvt_pk_bf16_f32 v97, v112, v97
	ds_read_b64_tr_b16 v[98:99], v118
	ds_read_b64_tr_b16 v[100:101], v118 offset:2048
	ds_read_b64_tr_b16 v[102:103], v118 offset:4096
	ds_read_b64_tr_b16 v[104:105], v118 offset:6144
	ds_read_b64_tr_b16 v[106:107], v118 offset:8192
	ds_read_b64_tr_b16 v[108:109], v118 offset:10240
	ds_read_b64_tr_b16 v[110:111], v118 offset:12288
	ds_read_b64_tr_b16 v[112:113], v118 offset:14336
	s_waitcnt lgkmcnt(0)
	s_barrier
	s_setprio 2
	s_waitcnt lgkmcnt(6)
	v_mfma_f32_32x32x16_bf16 v[18:33], v[82:85], v[98:101], v[18:33]
	ds_read_b64_tr_b16 v[114:115], v118 offset:512
	ds_read_b64_tr_b16 v[116:117], v118 offset:2560
	s_waitcnt lgkmcnt(6)
	v_mfma_f32_32x32x16_bf16 v[18:33], v[86:89], v[102:105], v[18:33]
	ds_read_b64_tr_b16 v[98:99], v118 offset:4608
	ds_read_b64_tr_b16 v[100:101], v118 offset:6656
	s_waitcnt lgkmcnt(6)
	v_mfma_f32_32x32x16_bf16 v[18:33], v[90:93], v[106:109], v[18:33]
	ds_read_b64_tr_b16 v[102:103], v118 offset:8704
	ds_read_b64_tr_b16 v[104:105], v118 offset:10752
	s_waitcnt lgkmcnt(6)
	v_mfma_f32_32x32x16_bf16 v[18:33], v[94:97], v[110:113], v[18:33]
	ds_read_b64_tr_b16 v[106:107], v118 offset:12800
	ds_read_b64_tr_b16 v[108:109], v118 offset:14848
	s_waitcnt lgkmcnt(6)
	v_mfma_f32_32x32x16_bf16 v[34:49], v[82:85], v[114:117], v[34:49]
	ds_read_b64_tr_b16 v[110:111], v118 offset:1024
	ds_read_b64_tr_b16 v[112:113], v118 offset:3072
	s_waitcnt lgkmcnt(6)
	v_mfma_f32_32x32x16_bf16 v[34:49], v[86:89], v[98:101], v[34:49]
	ds_read_b64_tr_b16 v[114:115], v118 offset:5120
	ds_read_b64_tr_b16 v[116:117], v118 offset:7168
	s_waitcnt lgkmcnt(6)
	v_mfma_f32_32x32x16_bf16 v[34:49], v[90:93], v[102:105], v[34:49]
	ds_read_b64_tr_b16 v[98:99], v118 offset:9216
	ds_read_b64_tr_b16 v[100:101], v118 offset:11264
	s_waitcnt lgkmcnt(6)
	v_mfma_f32_32x32x16_bf16 v[34:49], v[94:97], v[106:109], v[34:49]
	ds_read_b64_tr_b16 v[102:103], v118 offset:13312
	ds_read_b64_tr_b16 v[104:105], v118 offset:15360
	s_waitcnt lgkmcnt(6)
	v_mfma_f32_32x32x16_bf16 v[50:65], v[82:85], v[110:113], v[50:65]
	ds_read_b64_tr_b16 v[106:107], v118 offset:1536
	ds_read_b64_tr_b16 v[108:109], v118 offset:3584
	s_waitcnt lgkmcnt(6)
	v_mfma_f32_32x32x16_bf16 v[50:65], v[86:89], v[114:117], v[50:65]
	ds_read_b64_tr_b16 v[110:111], v118 offset:5632
	ds_read_b64_tr_b16 v[112:113], v118 offset:7680
	s_waitcnt lgkmcnt(6)
	v_mfma_f32_32x32x16_bf16 v[50:65], v[90:93], v[98:101], v[50:65]
	ds_read_b64_tr_b16 v[114:115], v118 offset:9728
	ds_read_b64_tr_b16 v[116:117], v118 offset:11776
	s_waitcnt lgkmcnt(6)
	v_mfma_f32_32x32x16_bf16 v[50:65], v[94:97], v[102:105], v[50:65]
	ds_read_b64_tr_b16 v[98:99], v118 offset:13824
	ds_read_b64_tr_b16 v[100:101], v118 offset:15872
	s_waitcnt lgkmcnt(6)
	v_mfma_f32_32x32x16_bf16 v[66:81], v[82:85], v[106:109], v[66:81]
	s_waitcnt lgkmcnt(4)
	v_mfma_f32_32x32x16_bf16 v[66:81], v[86:89], v[110:113], v[66:81]
	s_waitcnt lgkmcnt(2)
	v_mfma_f32_32x32x16_bf16 v[66:81], v[90:93], v[114:117], v[66:81]
	s_waitcnt lgkmcnt(0)
	v_mfma_f32_32x32x16_bf16 v[66:81], v[94:97], v[98:101], v[66:81]
	v_mfma_f32_4x4x4_16b_bf16 v[240:243], v[82:83], v[132:133], v[240:243]
	v_mfma_f32_4x4x4_16b_bf16 v[244:247], v[84:85], v[132:133], v[244:247]
	s_nop 0
	v_mfma_f32_4x4x4_16b_bf16 v[240:243], v[86:87], v[132:133], v[240:243]
	v_mfma_f32_4x4x4_16b_bf16 v[244:247], v[88:89], v[132:133], v[244:247]
	s_nop 0
	v_mfma_f32_4x4x4_16b_bf16 v[240:243], v[90:91], v[132:133], v[240:243]
	v_mfma_f32_4x4x4_16b_bf16 v[244:247], v[92:93], v[132:133], v[244:247]
	s_nop 0
	v_mfma_f32_4x4x4_16b_bf16 v[240:243], v[94:95], v[132:133], v[240:243]
	v_mfma_f32_4x4x4_16b_bf16 v[244:247], v[96:97], v[132:133], v[244:247]
	s_nop 0
	s_setprio 0
	s_barrier
	s_cmpk_gt_u32 s89, 0xff
	s_cbranch_scc1 .LBB0_294
	s_barrier
; __device__ __forceinline__ unsigned cvtpk(float lo, float hi) { f32x2_t v = {lo, hi}; bf16x2_t b = __builtin_convertvector(v, bf16x2_t); return __builtin_bit_cast(unsigned, b); }
;     ...
;   for (int r = 0; r < 16; ++r) rli[r] = __builtin_amdgcn_rcpf(lacc[r]);
;     ...
; #pragma unroll
;     for (int d0 = 0; d0 < 4; ++d0)
; #pragma unroll
;         for (int r = 0; r < 16; r += 2) stash[(d0 * 8 + (r >> 1)) * 64 + lane_] = att::cvtpk(o[d0][r] * rli[r], o[d0][r + 1] * rli[r + 1]);
.LBB0_294:
	s_nop 4
	v_add_f32_e32 v240, v240, v244
	v_add_f32_e32 v241, v241, v245
	v_add_f32_e32 v242, v242, v246
	v_add_f32_e32 v243, v243, v247
	v_and_b32_e32 v244, 3, v0
	v_cmp_eq_u32_e64 s[98:99], 1, v244
	s_nop 1
	v_cndmask_b32_e64 v240, v240, v241, s[98:99]
	v_cmp_eq_u32_e64 s[98:99], 2, v244
	s_nop 1
	v_cndmask_b32_e64 v240, v240, v242, s[98:99]
	v_cmp_eq_u32_e64 s[98:99], 3, v244
	s_nop 1
	v_cndmask_b32_e64 v240, v240, v243, s[98:99]
	v_mov_b32_e32 v245, v240
	s_nop 1
	v_permlane32_swap_b32_e32 v245, v240
	s_nop 1
	v_add_f32_e32 v240, v240, v245
	ds_write_b32 v165, v240
	v_add_u32_e32 v245, s6, v184
	s_waitcnt lgkmcnt(0)
	ds_read_b128 v[2:5], v245
	ds_read_b128 v[6:9], v245 offset:32
	ds_read_b128 v[10:13], v245 offset:64
	ds_read_b128 v[14:17], v245 offset:96
	s_waitcnt lgkmcnt(0)
	s_nop 8
	v_rcp_f32_e32 v2, v2
	v_rcp_f32_e32 v3, v3
	v_rcp_f32_e32 v4, v4
	v_rcp_f32_e32 v5, v5
	s_ashr_i32 s89, s92, 6
	s_lshl_b32 s4, s89, 13
	v_rcp_f32_e32 v6, v6
	v_rcp_f32_e32 v7, v7
	v_and_b32_e32 v82, 63, v164
	s_add_i32 s4, s4, 0
	v_rcp_f32_e32 v8, v8
	v_rcp_f32_e32 v9, v9
	v_pk_mul_f32 v[18:19], v[18:19], v[2:3]
	v_lshl_add_u32 v82, v82, 2, s4
	v_cvt_pk_bf16_f32 v83, v18, v19
	v_pk_mul_f32 v[18:19], v[20:21], v[4:5]
	v_rcp_f32_e32 v10, v10
	v_rcp_f32_e32 v11, v11
	v_add_u32_e32 v165, 0x12c00, v82
	v_cvt_pk_bf16_f32 v18, v18, v19
	v_rcp_f32_e32 v12, v12
	v_rcp_f32_e32 v13, v13
	ds_write2st64_b32 v165, v83, v18 offset1:1
	v_pk_mul_f32 v[18:19], v[22:23], v[6:7]
	v_rcp_f32_e32 v14, v14
	v_cvt_pk_bf16_f32 v20, v18, v19
	v_pk_mul_f32 v[18:19], v[24:25], v[8:9]
	v_rcp_f32_e32 v15, v15
	v_cvt_pk_bf16_f32 v18, v18, v19
	v_rcp_f32_e32 v16, v16
	v_rcp_f32_e32 v17, v17
	ds_write2st64_b32 v165, v20, v18 offset0:2 offset1:3
	v_pk_mul_f32 v[18:19], v[26:27], v[10:11]
	s_add_u32 s8, s8, 0x80
	v_cvt_pk_bf16_f32 v20, v18, v19
	v_pk_mul_f32 v[18:19], v[28:29], v[12:13]
	s_addc_u32 s4, s91, 0
	v_cvt_pk_bf16_f32 v18, v18, v19
	ds_write2st64_b32 v165, v20, v18 offset0:4 offset1:5
	v_pk_mul_f32 v[18:19], v[30:31], v[14:15]
	s_mov_b32 s14, s10
	v_cvt_pk_bf16_f32 v20, v18, v19
	v_pk_mul_f32 v[18:19], v[32:33], v[16:17]
	s_mov_b32 s15, s11
	v_cvt_pk_bf16_f32 v18, v18, v19
	ds_write2st64_b32 v165, v20, v18 offset0:6 offset1:7
	v_pk_mul_f32 v[18:19], v[34:35], v[2:3]
	v_mov_b32_e32 v132, v130
	v_cvt_pk_bf16_f32 v20, v18, v19
	v_pk_mul_f32 v[18:19], v[36:37], v[4:5]
	v_mov_b32_e32 v133, v130
	v_cvt_pk_bf16_f32 v18, v18, v19
	ds_write2st64_b32 v165, v20, v18 offset0:8 offset1:9
	v_pk_mul_f32 v[18:19], v[38:39], v[6:7]
	v_mov_b32_e32 v131, v130
	v_cvt_pk_bf16_f32 v20, v18, v19
	v_pk_mul_f32 v[18:19], v[40:41], v[8:9]
	v_mov_b64_e32 v[134:135], v[132:133]
	v_cvt_pk_bf16_f32 v18, v18, v19
	ds_write2st64_b32 v165, v20, v18 offset0:10 offset1:11
	v_pk_mul_f32 v[18:19], v[42:43], v[10:11]
	v_mov_b64_e32 v[132:133], v[130:131]
	v_cvt_pk_bf16_f32 v20, v18, v19
	v_pk_mul_f32 v[18:19], v[44:45], v[12:13]
	s_nop 0
	v_cvt_pk_bf16_f32 v18, v18, v19
	ds_write2st64_b32 v165, v20, v18 offset0:12 offset1:13
	v_pk_mul_f32 v[18:19], v[46:47], v[14:15]
	s_nop 0
	v_cvt_pk_bf16_f32 v20, v18, v19
	v_pk_mul_f32 v[18:19], v[48:49], v[16:17]
	s_nop 0
	v_cvt_pk_bf16_f32 v18, v18, v19
	ds_write2st64_b32 v165, v20, v18 offset0:14 offset1:15
	v_pk_mul_f32 v[18:19], v[50:51], v[2:3]
	v_pk_mul_f32 v[2:3], v[66:67], v[2:3]
	v_cvt_pk_bf16_f32 v20, v18, v19
	v_pk_mul_f32 v[18:19], v[52:53], v[4:5]
	s_nop 0
	v_cvt_pk_bf16_f32 v18, v18, v19
	ds_write2st64_b32 v165, v20, v18 offset0:16 offset1:17
	v_pk_mul_f32 v[18:19], v[54:55], v[6:7]
	s_nop 0
	v_cvt_pk_bf16_f32 v20, v18, v19
	v_pk_mul_f32 v[18:19], v[56:57], v[8:9]
	s_nop 0
	v_cvt_pk_bf16_f32 v18, v18, v19
	ds_write2st64_b32 v165, v20, v18 offset0:18 offset1:19
	v_pk_mul_f32 v[18:19], v[58:59], v[10:11]
	s_nop 0
	v_cvt_pk_bf16_f32 v20, v18, v19
	v_pk_mul_f32 v[18:19], v[60:61], v[12:13]
	s_nop 0
	v_cvt_pk_bf16_f32 v18, v18, v19
	ds_write2st64_b32 v165, v20, v18 offset0:20 offset1:21
	v_pk_mul_f32 v[18:19], v[62:63], v[14:15]
	v_mov_b32_e32 v63, v0
	v_cvt_pk_bf16_f32 v20, v18, v19
	v_pk_mul_f32 v[18:19], v[64:65], v[16:17]
	s_nop 0
	v_cvt_pk_bf16_f32 v18, v18, v19
	ds_write2st64_b32 v165, v20, v18 offset0:22 offset1:23
	v_cvt_pk_bf16_f32 v18, v2, v3
	v_pk_mul_f32 v[2:3], v[68:69], v[4:5]
	v_mov_b32_e32 v5, v185
	v_cvt_pk_bf16_f32 v2, v2, v3
	ds_write2st64_b32 v165, v18, v2 offset0:24 offset1:25
	v_pk_mul_f32 v[2:3], v[70:71], v[6:7]
	s_nop 0
	v_cvt_pk_bf16_f32 v4, v2, v3
	v_pk_mul_f32 v[2:3], v[72:73], v[8:9]
	s_nop 0
	v_cvt_pk_bf16_f32 v2, v2, v3
	ds_write2st64_b32 v165, v4, v2 offset0:26 offset1:27
	v_pk_mul_f32 v[2:3], v[74:75], v[10:11]
	s_nop 0
	v_cvt_pk_bf16_f32 v4, v2, v3
	v_pk_mul_f32 v[2:3], v[76:77], v[12:13]
	s_nop 0
	v_cvt_pk_bf16_f32 v2, v2, v3
	ds_write2st64_b32 v165, v4, v2 offset0:28 offset1:29
	v_pk_mul_f32 v[2:3], v[78:79], v[14:15]
	s_nop 0
	v_cvt_pk_bf16_f32 v4, v2, v3
	v_pk_mul_f32 v[2:3], v[80:81], v[16:17]
	s_nop 0
	v_cvt_pk_bf16_f32 v2, v2, v3
	ds_write2st64_b32 v165, v4, v2 offset0:30 offset1:31
	s_nop 0
	v_readfirstlane_b32 s91, v63
	s_ashr_i32 s5, s91, 1
	v_mov_b32_e32 v2, s5
	v_bfi_b32 v2, s3, v2, v63
	v_ashrrev_i32_e32 v3, 31, v2
	v_bfe_u32 v4, v63, 5, 1
	v_lshlrev_b64 v[2:3], 11, v[2:3]
	v_and_b32_e32 v62, 31, v63
	v_lshl_add_u64 v[2:3], s[50:51], 0, v[2:3]
	v_lshlrev_b32_e32 v184, 4, v4
	s_and_b32 s9, s5, 0xffffffe0
	v_lshl_add_u64 v[54:55], v[2:3], 0, v[184:185]
	v_or_b32_e32 v2, s90, v62
	v_add_u32_e32 v2, s9, v2
	global_load_dwordx4 v[18:21], v[54:55], off offset:128
	v_ashrrev_i32_e32 v3, 31, v2
	v_lshlrev_b64 v[2:3], 8, v[2:3]
	v_and_b32_e32 v4, 32, v63
	v_lshl_add_u64 v[2:3], s[48:49], 0, v[2:3]
	v_lshl_add_u64 v[64:65], v[2:3], 0, v[4:5]
	global_load_dwordx4 v[22:25], v[64:65], off
	global_load_dwordx4 v[26:29], v[64:65], off offset:16
	global_load_dwordx4 v[30:33], v[54:55], off offset:160
	global_load_dwordx4 v[34:37], v[64:65], off offset:64
	global_load_dwordx4 v[38:41], v[64:65], off offset:80
	global_load_dwordx4 v[42:45], v[54:55], off offset:192
	global_load_dwordx4 v[46:49], v[64:65], off offset:144
	global_load_dwordx4 v[50:53], v[64:65], off offset:128
	v_lshlrev_b32_e32 v77, 3, v63
	v_lshlrev_b32_e32 v2, 4, v63
	v_ashrrev_i32_e32 v79, 4, v63
	v_and_b32_e32 v78, 0x70, v2
	v_and_b32_e32 v2, 0x78, v77
	v_lshlrev_b32_e32 v3, 11, v79
	v_ashrrev_i32_e32 v76, 3, v63
	v_lshl_or_b32 v172, v2, 1, v3
	v_lshl_or_b32 v171, v76, 11, v78
	s_and_b32 s9, s4, 0xffff
	buffer_load_dwordx4 v[6:9], v172, s[12:15], 0 offen
	buffer_load_dwordx4 v[2:5], v172, s[12:15], s57 offen
	buffer_load_dwordx4 v[14:17], v171, s[8:11], 0 offen
	buffer_load_dwordx4 v[10:13], v171, s[8:11], s11 offen
	s_nop 0
	global_load_dwordx4 v[54:57], v[54:55], off offset:224
	s_nop 0
	global_load_dwordx4 v[58:61], v[64:65], off offset:208
	s_nop 0
	global_load_dwordx4 v[64:67], v[64:65], off offset:192
	s_waitcnt vmcnt(15)
; __device__ __forceinline__ unsigned cvtpk(float lo, float hi) { f32x2_t v = {lo, hi}; bf16x2_t b = __builtin_convertvector(v, bf16x2_t); return __builtin_bit_cast(unsigned, b); }
; #define ATT_WRITE_V(so) do { *(bf16x8*)(V_lds + (so) + vst0) = sv0; *(bf16x8*)(V_lds + (so) + vst1) = sv1; } while (0)
; template <int DQK> __device__ __forceinline__ void q_prepare(bf16x8 (&qr)[DQK / 16], const float* rope, const float* gain, int s, int hi) {
;     ...
;   if constexpr (DQK == 64) {
; #pragma unroll
;     for (int d0 = 0; d0 < 4; ++d0) {
;       const f32x4q* tp = (const f32x4q*)(rope + ((size_t)s * 32 + 8 * d0 + 4 * hi) * 2);
;       const f32x4q t0 = tp[0], t1 = tp[1];
;       const float cs[4] = {t0.x, t0.z, t1.x, t1.z}, sn[4] = {t0.y, t0.w, t1.y, t1.w};
; #pragma unroll
;       for (int e = 0; e < 4; ++e) { const float x1 = v[d0][e], x2 = v[d0][4 + e]; v[d0][e] = x1 * cs[e] - x2 * sn[e]; v[d0][4 + e] = x2 * cs[e] + x1 * sn[e]; }
;     }
;   } else
; #pragma unroll
;   for (int blk = 0; blk < DQK / 64; ++blk) {
;     const int pos = (DQK == 128) ? (blk == 0 ? (s >> 6) : (s & 63)) : s;
; #pragma unroll
;     for (int dd = 0; dd < 2; ++dd) {
;       const f32x4q* tp = (const f32x4q*)(rope + ((size_t)pos * 32 + 16 * dd + 8 * hi) * 2);
;       const f32x4q t0 = tp[0], t1 = tp[1], t2 = tp[2], t3 = tp[3];
;       const float cs[8] = {t0.x, t0.z, t1.x, t1.z, t2.x, t2.z, t3.x, t3.z}, sn[8] = {t0.y, t0.w, t1.y, t1.w, t2.y, t2.w, t3.y, t3.w};
; #pragma unroll
;       for (int j = 0; j < 8; ++j) { const float x1 = v[4 * blk + dd][j], x2 = v[4 * blk + dd + 2][j];
;         v[4 * blk + dd][j] = x1 * cs[j] - x2 * sn[j]; v[4 * blk + dd + 2][j] = x2 * cs[j] + x1 * sn[j]; }
;     }
;   }
; #pragma unroll
;   for (int d0 = 0; d0 < DQK / 16; ++d0) { u32x4 w = {cvtpk(v[d0][0] * mul, v[d0][1] * mul), cvtpk(v[d0][2] * mul, v[d0][3] * mul), cvtpk(v[d0][4] * mul, v[d0][5] * mul), cvtpk(v[d0][6] * mul, v[d0][7] * mul)};
;     qr[d0] = *reinterpret_cast<bf16x8*>(&w); }
;     ...
;   if constexpr (DQK == 64) { sk0 = ek0; sv0 = ev0; sv1 = ev1; ATT_WRITE_K(0); ATT_WRITE_V(0); sk0 = ek1; ATT_WRITE_K(SHM_K); }
;   else { ATT_LOAD_K(0); ATT_LOAD_V(0); ATT_WRITE_K(0); ATT_WRITE_V(0);
;          ATT_LOAD_K(1); ATT_WRITE_K(SHM_K); }
;   ATT_LOAD_K(2); ATT_LOAD_V(1);
;   asm volatile("s_waitcnt lgkmcnt(0)" ::: "memory"); ATT_BAR();
;   if (grp == 1) ATT_BAR();
	v_lshlrev_b32_e32 v70, 16, v20
	v_and_b32_e32 v71, 0xffff0000, v20
	s_waitcnt vmcnt(14)
	v_mov_b32_e32 v72, v22
	v_mov_b32_e32 v73, v24
	v_lshlrev_b32_e32 v68, 16, v18
	v_and_b32_e32 v69, 0xffff0000, v18
	v_pk_mul_f32 v[74:75], v[72:73], v[70:71]
	v_mov_b32_e32 v24, v23
	v_pk_fma_f32 v[22:23], v[24:25], v[68:69], v[74:75]
	v_pk_mul_f32 v[24:25], v[24:25], v[70:71]
	v_pk_mul_f32 v[22:23], v[22:23], s[40:41] op_sel_hi:[1,0]
	v_pk_fma_f32 v[24:25], v[72:73], v[68:69], v[24:25] neg_lo:[0,0,1] neg_hi:[0,0,1]
	v_cvt_pk_bf16_f32 v138, v22, v23
	v_pk_mul_f32 v[24:25], v[24:25], s[40:41] op_sel_hi:[1,0]
	v_lshlrev_b32_e32 v20, 16, v21
	v_and_b32_e32 v21, 0xffff0000, v21
	s_waitcnt vmcnt(13)
	v_mov_b32_e32 v22, v26
	v_mov_b32_e32 v23, v28
	v_mov_b32_e32 v28, v27
	v_cvt_pk_bf16_f32 v136, v24, v25
	v_lshlrev_b32_e32 v18, 16, v19
	v_and_b32_e32 v19, 0xffff0000, v19
	v_pk_mul_f32 v[24:25], v[22:23], v[20:21]
	v_pk_mul_f32 v[20:21], v[28:29], v[20:21]
	v_pk_fma_f32 v[24:25], v[28:29], v[18:19], v[24:25]
	v_pk_fma_f32 v[18:19], v[22:23], v[18:19], v[20:21] neg_lo:[0,0,1] neg_hi:[0,0,1]
	s_waitcnt vmcnt(12)
	v_lshlrev_b32_e32 v20, 16, v32
	v_pk_mul_f32 v[18:19], v[18:19], s[40:41] op_sel_hi:[1,0]
	v_and_b32_e32 v21, 0xffff0000, v32
	v_cvt_pk_bf16_f32 v137, v18, v19
	v_pk_mul_f32 v[18:19], v[24:25], s[40:41] op_sel_hi:[1,0]
	s_waitcnt vmcnt(11)
	v_mov_b32_e32 v22, v34
	v_mov_b32_e32 v23, v36
	v_mov_b32_e32 v36, v35
	v_cvt_pk_bf16_f32 v139, v18, v19
	v_lshlrev_b32_e32 v18, 16, v30
	v_and_b32_e32 v19, 0xffff0000, v30
	v_pk_mul_f32 v[24:25], v[22:23], v[20:21]
	v_pk_mul_f32 v[20:21], v[36:37], v[20:21]
	v_pk_fma_f32 v[24:25], v[36:37], v[18:19], v[24:25]
	v_pk_fma_f32 v[18:19], v[22:23], v[18:19], v[20:21] neg_lo:[0,0,1] neg_hi:[0,0,1]
	v_lshlrev_b32_e32 v20, 16, v33
	v_pk_mul_f32 v[18:19], v[18:19], s[40:41] op_sel_hi:[1,0]
	v_and_b32_e32 v21, 0xffff0000, v33
	v_cvt_pk_bf16_f32 v140, v18, v19
	v_pk_mul_f32 v[18:19], v[24:25], s[40:41] op_sel_hi:[1,0]
	s_waitcnt vmcnt(10)
	v_mov_b32_e32 v22, v38
	v_mov_b32_e32 v23, v40
	v_mov_b32_e32 v40, v39
	v_cvt_pk_bf16_f32 v142, v18, v19
	v_lshlrev_b32_e32 v18, 16, v31
	v_and_b32_e32 v19, 0xffff0000, v31
	v_pk_mul_f32 v[24:25], v[22:23], v[20:21]
	v_pk_mul_f32 v[20:21], v[40:41], v[20:21]
	v_pk_fma_f32 v[24:25], v[40:41], v[18:19], v[24:25]
	v_pk_fma_f32 v[18:19], v[22:23], v[18:19], v[20:21] neg_lo:[0,0,1] neg_hi:[0,0,1]
	s_waitcnt vmcnt(9)
	v_lshlrev_b32_e32 v20, 16, v44
	v_pk_mul_f32 v[18:19], v[18:19], s[40:41] op_sel_hi:[1,0]
	v_and_b32_e32 v21, 0xffff0000, v44
	v_cvt_pk_bf16_f32 v141, v18, v19
	v_pk_mul_f32 v[18:19], v[24:25], s[40:41] op_sel_hi:[1,0]
	s_waitcnt vmcnt(7)
	v_mov_b32_e32 v22, v50
	v_mov_b32_e32 v23, v52
	v_mov_b32_e32 v52, v51
	v_cvt_pk_bf16_f32 v143, v18, v19
	v_lshlrev_b32_e32 v18, 16, v42
	v_and_b32_e32 v19, 0xffff0000, v42
	v_pk_mul_f32 v[24:25], v[22:23], v[20:21]
	v_pk_mul_f32 v[20:21], v[52:53], v[20:21]
	v_pk_fma_f32 v[24:25], v[52:53], v[18:19], v[24:25]
	v_pk_fma_f32 v[18:19], v[22:23], v[18:19], v[20:21] neg_lo:[0,0,1] neg_hi:[0,0,1]
	v_lshlrev_b32_e32 v20, 16, v45
	v_pk_mul_f32 v[18:19], v[18:19], s[40:41] op_sel_hi:[1,0]
	v_and_b32_e32 v21, 0xffff0000, v45
	v_cvt_pk_bf16_f32 v144, v18, v19
	v_pk_mul_f32 v[18:19], v[24:25], s[40:41] op_sel_hi:[1,0]
	v_mov_b32_e32 v22, v46
	v_mov_b32_e32 v23, v48
	v_mov_b32_e32 v48, v47
	v_cvt_pk_bf16_f32 v146, v18, v19
	v_lshlrev_b32_e32 v18, 16, v43
	v_and_b32_e32 v19, 0xffff0000, v43
	v_pk_mul_f32 v[24:25], v[22:23], v[20:21]
	v_pk_mul_f32 v[20:21], v[48:49], v[20:21]
	v_pk_fma_f32 v[24:25], v[48:49], v[18:19], v[24:25]
	v_pk_fma_f32 v[18:19], v[22:23], v[18:19], v[20:21] neg_lo:[0,0,1] neg_hi:[0,0,1]
	s_waitcnt vmcnt(2)
	v_lshlrev_b32_e32 v20, 16, v56
	v_pk_mul_f32 v[18:19], v[18:19], s[40:41] op_sel_hi:[1,0]
	v_and_b32_e32 v21, 0xffff0000, v56
	v_cvt_pk_bf16_f32 v145, v18, v19
	v_pk_mul_f32 v[18:19], v[24:25], s[40:41] op_sel_hi:[1,0]
	s_waitcnt vmcnt(0)
	v_mov_b32_e32 v22, v64
	v_mov_b32_e32 v23, v66
	v_mov_b32_e32 v66, v65
	v_cvt_pk_bf16_f32 v147, v18, v19
	v_lshlrev_b32_e32 v18, 16, v54
	v_and_b32_e32 v19, 0xffff0000, v54
	v_pk_mul_f32 v[24:25], v[22:23], v[20:21]
	v_pk_mul_f32 v[20:21], v[66:67], v[20:21]
	v_pk_fma_f32 v[24:25], v[66:67], v[18:19], v[24:25]
	v_pk_fma_f32 v[18:19], v[22:23], v[18:19], v[20:21] neg_lo:[0,0,1] neg_hi:[0,0,1]
	v_lshlrev_b32_e32 v20, 16, v57
	v_pk_mul_f32 v[18:19], v[18:19], s[40:41] op_sel_hi:[1,0]
	v_and_b32_e32 v21, 0xffff0000, v57
	v_cvt_pk_bf16_f32 v148, v18, v19
	v_pk_mul_f32 v[18:19], v[24:25], s[40:41] op_sel_hi:[1,0]
	v_mov_b32_e32 v22, v58
	v_mov_b32_e32 v23, v60
	v_mov_b32_e32 v60, v59
	v_cvt_pk_bf16_f32 v150, v18, v19
	v_lshlrev_b32_e32 v18, 16, v55
	v_and_b32_e32 v19, 0xffff0000, v55
	v_pk_mul_f32 v[24:25], v[22:23], v[20:21]
	v_pk_mul_f32 v[20:21], v[60:61], v[20:21]
	v_pk_fma_f32 v[24:25], v[60:61], v[18:19], v[24:25]
	v_pk_fma_f32 v[18:19], v[22:23], v[18:19], v[20:21] neg_lo:[0,0,1] neg_hi:[0,0,1]
	v_mov_b32_e32 v20, v185
	v_pk_mul_f32 v[18:19], v[18:19], s[40:41] op_sel_hi:[1,0]
	v_mov_b32_e32 v21, v185
	v_cvt_pk_bf16_f32 v149, v18, v19
	v_pk_mul_f32 v[18:19], v[24:25], s[40:41] op_sel_hi:[1,0]
	v_mov_b32_e32 v22, v185
	v_cvt_pk_bf16_f32 v151, v18, v19
	v_mov_b32_e32 v18, v185
	v_mov_b32_e32 v19, v185
	v_mov_b32_e32 v23, v185
	v_mov_b32_e32 v24, v185
	v_mov_b32_e32 v25, v185
	v_mov_b32_e32 v26, v185
	v_mov_b32_e32 v27, v185
	v_mov_b32_e32 v28, v185
	v_mov_b32_e32 v29, v185
	v_mov_b32_e32 v30, v185
	v_mov_b32_e32 v31, v185
	v_mov_b32_e32 v32, v185
	v_mov_b32_e32 v33, v185
	buffer_load_dwordx4 v[50:53], v172, s[12:15], s11 offen
	buffer_load_dwordx4 v[58:61], v171, s[8:11], s83 offen
	buffer_load_dwordx4 v[54:57], v172, s[12:15], s84 offen
	v_lshlrev_b32_e32 v36, 5, v79
	v_and_b32_e32 v37, 24, v77
	v_lshrrev_b32_e32 v34, 5, v63
	v_bfe_u32 v35, v77, 5, 2
	v_and_or_b32 v36, v36, s52, v37
	v_and_or_b32 v34, v34, s41, v35
	v_lshlrev_b32_e32 v36, 1, v36
	v_lshl_or_b32 v168, v34, 9, v36
	v_add_u32_e32 v34, 32, v79
	v_lshrrev_b32_e32 v34, 1, v34
	v_and_or_b32 v34, v34, s41, v35
	v_lshl_or_b32 v169, v34, 9, v36
	v_mul_lo_u32 v34, v76, s82
	v_add3_u32 v170, v34, v78, 0
	v_add_u32_e32 v64, 0, v168
	v_add_u32_e32 v65, 0, v169
	ds_write_b128 v170, v[14:17] offset:49152
	ds_write_b128 v64, v[6:9]
	ds_write_b128 v65, v[2:5]
	ds_write_b128 v170, v[10:13] offset:58368
	s_waitcnt lgkmcnt(0)
	s_barrier
	s_and_b32 s4, s91, 0xffffff00
	s_cmpk_lg_i32 s4, 0x100
	s_cbranch_scc1 .LBB0_296
	s_barrier
; #define ATT_SBAR() __builtin_amdgcn_sched_barrier(0)
; __device__ __forceinline__ unsigned cvtpk(float lo, float hi) { f32x2_t v = {lo, hi}; bf16x2_t b = __builtin_convertvector(v, bf16x2_t); return __builtin_bit_cast(unsigned, b); }
; __device__ __forceinline__ int v_rd_base(int lane) { return ((lane & 3) << 3) | (((lane >> 2) & 3) << 6) | (((lane >> 4) & 1) << 5) | (((lane >> 5) & 1) << 8); }
; #define ATT_WRITE_K(so) do { *(bf16x8*)(K_lds + (so) + kswz<DQK>(kr, kc * 2)) = sk0; if constexpr (DQK == 128) *(bf16x8*)(K_lds + (so) + kswz<DQK>(32 + kr, kc * 2)) = sk1; } while (0)
; #define ATT_WRITE_V(so) do { *(bf16x8*)(V_lds + (so) + vst0) = sv0; *(bf16x8*)(V_lds + (so) + vst1) = sv1; } while (0)
; #define ATT_BAR() do { ATT_SBAR(); asm volatile("s_barrier" ::: "memory"); ATT_SBAR(); } while (0)
; #define ATT_SOFTMAX(first_) do { const float pm_ = softmax_rowmax(p0, p1); \
;     if (__builtin_expect((first_) || !__all(pm_ <= THRL), 0)) { const float al_ = softmax_shift(p0, p1, negm, pm_, (first_)); ATT_RESC(al_); } \
;     softmax_exp_pack(p0, p1, pa0, pa1, pa2, pa3); } while (0)
;     ...
;   qkt<DQK>(p0, p1, K_lds, qr, r32, hi);
;   ATT_BAR();
;   int k1 = SHM_K, k2 = 2 * SHM_K, k0 = 0, v0 = 0, v1 = SHM_V, v2 = 2 * SHM_V;
;   const lds_cptr kq0 = (lds_cptr)K_lds, vq0 = (lds_cptr)V_lds + v_rd_base(lane);
;   bf16x8 kf[8]; s16x4 va[8], vc[8];
;     ...
;   for (int t = 0; t + 1 < NT; ++t) {
;     if constexpr (ABL & 1) { u32x4 w0 = {cvtpk(p0[0], p0[1]), cvtpk(p0[2], p0[3]), cvtpk(p0[4], p0[5]), cvtpk(p0[6], p0[7])}, w1 = {cvtpk(p0[8], p0[9]), cvtpk(p0[10], p0[11]), cvtpk(p0[12], p0[13]), cvtpk(p0[14], p0[15])};
;         u32x4 w2 = {cvtpk(p1[0], p1[1]), cvtpk(p1[2], p1[3]), cvtpk(p1[4], p1[5]), cvtpk(p1[6], p1[7])}, w3 = {cvtpk(p1[8], p1[9]), cvtpk(p1[10], p1[11]), cvtpk(p1[12], p1[13]), cvtpk(p1[14], p1[15])};
;         pa0 = *reinterpret_cast<bf16x8*>(&w0); pa1 = *reinterpret_cast<bf16x8*>(&w1); pa2 = *reinterpret_cast<bf16x8*>(&w2); pa3 = *reinterpret_cast<bf16x8*>(&w3); }
;     else { ATT_SOFTMAX(t == 0); }
;     if constexpr (!(ABL & 4)) { ATT_WRITE_K(k2); ATT_WRITE_V(v1); }
;     ATT_SBAR();
; #pragma unroll
;     for (int ks = 0; ks < 4; ++ks) ATT_VPAIR(va, v0, 0, ks);
;     asm volatile("s_waitcnt lgkmcnt(8)" ::: "memory"); ATT_BAR();
.LBB0_296:
	v_mul_u32_u24_e32 v2, 0x90, v62
	v_add3_u32 v78, 0, v184, v2
	ds_read_b128 v[2:5], v78 offset:49152
	v_mad_u32_u24 v167, v62, s82, 0
	v_add_u32_e32 v173, v167, v184
	ds_read_b128 v[34:37], v173 offset:53760
	ds_read_b128 v[66:69], v78 offset:49184
	ds_read_b128 v[70:73], v78 offset:49216
	v_and_b32_e32 v63, 63, v63
	s_mov_b32 s90, 1
	s_waitcnt lgkmcnt(3)
	v_mfma_f32_32x32x16_bf16 v[2:17], v[2:5], v[136:139], 0
	s_waitcnt lgkmcnt(2)
	v_mfma_f32_32x32x16_bf16 v[34:49], v[34:37], v[136:139], 0
	s_waitcnt lgkmcnt(1)
	v_mfma_f32_32x32x16_bf16 v[2:17], v[66:69], v[140:143], v[2:17]
	ds_read_b128 v[66:69], v78 offset:53792
	ds_read_b128 v[74:77], v78 offset:49248
	s_waitcnt lgkmcnt(1)
	v_mfma_f32_32x32x16_bf16 v[34:49], v[66:69], v[140:143], v[34:49]
	v_mfma_f32_32x32x16_bf16 v[2:17], v[70:73], v[144:147], v[2:17]
	ds_read_b128 v[66:69], v78 offset:53824
	ds_read_b128 v[70:73], v78 offset:53856
	s_waitcnt lgkmcnt(1)
	v_mfma_f32_32x32x16_bf16 v[34:49], v[66:69], v[144:147], v[34:49]
	v_lshlrev_b32_e32 v67, 3, v63
	v_lshlrev_b32_e32 v69, 4, v63
	v_add_u32_e32 v66, 0xc000, v170
	v_and_b32_e32 v68, 24, v67
	v_and_b32_e32 v69, 0xc0, v69
	v_and_b32_e32 v67, 0x100, v67
	v_mfma_f32_32x32x16_bf16 v[2:17], v[74:77], v[148:151], v[2:17]
	v_lshlrev_b32_e32 v74, 1, v63
	v_and_b32_e32 v74, 32, v74
	s_waitcnt lgkmcnt(0)
	v_mfma_f32_32x32x16_bf16 v[34:49], v[70:73], v[148:151], v[34:49]
	s_barrier
	v_cmp_gt_u32_e64 s[4:5], 32, v63
	v_lshl_add_u32 v166, v62, 2, s6
	s_nop 9
	v_add_f32_e32 v62, 0, v34
	v_max3_f32 v63, v62, v2, v3
	v_max3_f32 v63, v63, v4, v5
	v_max3_f32 v63, v63, v6, v7
	v_max3_f32 v63, v63, v8, v9
	v_max3_f32 v63, v63, v10, v11
	v_max3_f32 v63, v63, v12, v13
	v_max3_f32 v63, v63, v14, v15
	v_max3_f32 v63, v63, v16, v17
	s_nop 4
	v_add3_u32 v68, 0, v68, v69
	v_max3_f32 v62, v63, v35, v36
	v_max3_f32 v62, v62, v37, v38
	v_max3_f32 v62, v62, v39, v40
	v_max3_f32 v62, v62, v41, v42
	v_max3_f32 v62, v62, v43, v44
	v_max3_f32 v62, v62, v45, v46
	v_max3_f32 v62, v62, v47, v48
	v_max_f32 v62, v62, v49
	v_add3_u32 v131, v68, v74, v67
	v_mov_b32_e32 v63, v62
	s_nop 1
	v_permlane32_swap_b32_e32 v62, v63
	v_max_f32_e32 v63, v63, v63
	v_max_f32_e32 v62, v62, v62
	v_max_f32_e32 v62, v62, v63
	v_sub_f32_e32 v2, v2, v62
	v_sub_f32_e32 v34, v34, v62
	v_sub_f32_e32 v3, v3, v62
	v_sub_f32_e32 v35, v35, v62
	v_sub_f32_e32 v4, v4, v62
	v_sub_f32_e32 v36, v36, v62
	v_sub_f32_e32 v5, v5, v62
	v_sub_f32_e32 v37, v37, v62
	v_sub_f32_e32 v6, v6, v62
	v_sub_f32_e32 v38, v38, v62
	v_sub_f32_e32 v7, v7, v62
	v_sub_f32_e32 v39, v39, v62
	v_sub_f32_e32 v8, v8, v62
	v_sub_f32_e32 v40, v40, v62
	v_sub_f32_e32 v9, v9, v62
	v_sub_f32_e32 v41, v41, v62
	v_sub_f32_e32 v10, v10, v62
	v_sub_f32_e32 v42, v42, v62
	v_sub_f32_e32 v11, v11, v62
	v_sub_f32_e32 v43, v43, v62
	v_sub_f32_e32 v12, v12, v62
	v_sub_f32_e32 v44, v44, v62
	v_sub_f32_e32 v13, v13, v62
	v_sub_f32_e32 v45, v45, v62
	v_sub_f32_e32 v14, v14, v62
	v_sub_f32_e32 v46, v46, v62
	v_sub_f32_e32 v15, v15, v62
	v_sub_f32_e32 v47, v47, v62
	v_sub_f32_e32 v16, v16, v62
	v_sub_f32_e32 v48, v48, v62
	v_sub_f32_e32 v17, v17, v62
	v_sub_f32_e32 v49, v49, v62
	v_exp_f32_e32 v2, v2
	v_exp_f32_e32 v34, v34
	v_exp_f32_e32 v3, v3
	v_exp_f32_e32 v35, v35
	v_exp_f32_e32 v4, v4
	v_exp_f32_e32 v36, v36
	v_exp_f32_e32 v5, v5
	v_exp_f32_e32 v37, v37
	v_exp_f32_e32 v6, v6
	v_exp_f32_e32 v38, v38
	v_exp_f32_e32 v7, v7
	v_exp_f32_e32 v39, v39
	v_exp_f32_e32 v8, v8
	v_exp_f32_e32 v40, v40
	v_exp_f32_e32 v9, v9
	v_exp_f32_e32 v41, v41
	v_exp_f32_e32 v10, v10
	v_exp_f32_e32 v42, v42
	v_exp_f32_e32 v11, v11
	v_exp_f32_e32 v43, v43
	v_exp_f32_e32 v12, v12
	v_exp_f32_e32 v44, v44
	v_exp_f32_e32 v13, v13
	v_exp_f32_e32 v45, v45
	v_exp_f32_e32 v14, v14
	v_exp_f32_e32 v46, v46
	v_exp_f32_e32 v15, v15
	v_exp_f32_e32 v47, v47
	v_exp_f32_e32 v16, v16
	v_exp_f32_e32 v48, v48
	v_exp_f32_e32 v17, v17
	v_exp_f32_e32 v49, v49
	v_sub_f32_e32 v82, 0, v62
	v_mov_b32_e32 v83, v82
	v_mov_b32_e32 v84, v82
	v_mov_b32_e32 v85, v82
	v_mov_b32_e32 v86, v82
	v_mov_b32_e32 v87, v82
	v_mov_b32_e32 v88, v82
	v_mov_b32_e32 v89, v82
	v_mov_b32_e32 v90, v82
	v_mov_b32_e32 v91, v82
	v_mov_b32_e32 v92, v82
	v_mov_b32_e32 v93, v82
	v_mov_b32_e32 v94, v82
	v_mov_b32_e32 v95, v82
	v_mov_b32_e32 v96, v82
	v_mov_b32_e32 v97, v82
	v_cvt_pk_bf16_f32 v98, v2, v3
	v_cvt_pk_bf16_f32 v99, v4, v5
	v_cvt_pk_bf16_f32 v100, v6, v7
	v_cvt_pk_bf16_f32 v101, v8, v9
	v_cvt_pk_bf16_f32 v102, v10, v11
	v_cvt_pk_bf16_f32 v103, v12, v13
	v_cvt_pk_bf16_f32 v104, v14, v15
	v_cvt_pk_bf16_f32 v105, v16, v17
	v_cvt_pk_bf16_f32 v106, v34, v35
	v_cvt_pk_bf16_f32 v107, v36, v37
	v_cvt_pk_bf16_f32 v108, v38, v39
	v_cvt_pk_bf16_f32 v109, v40, v41
	v_cvt_pk_bf16_f32 v110, v42, v43
	v_cvt_pk_bf16_f32 v111, v44, v45
	v_cvt_pk_bf16_f32 v112, v46, v47
	v_cvt_pk_bf16_f32 v113, v48, v49
	s_waitcnt vmcnt(1)
	ds_write_b128 v66, v[58:61] offset:18432
	ds_write_b128 v64, v[50:53] offset:16384
	s_waitcnt vmcnt(0)
	ds_write_b128 v65, v[54:57] offset:16384
	ds_read_b64_tr_b16 v[2:3], v131
	ds_read_b64_tr_b16 v[4:5], v131 offset:2048
	ds_read_b64_tr_b16 v[6:7], v131 offset:4096
	ds_read_b64_tr_b16 v[8:9], v131 offset:6144
	ds_read_b64_tr_b16 v[10:11], v131 offset:8192
	ds_read_b64_tr_b16 v[12:13], v131 offset:10240
	ds_read_b64_tr_b16 v[14:15], v131 offset:12288
	ds_read_b64_tr_b16 v[16:17], v131 offset:14336
	s_waitcnt lgkmcnt(8)
	s_barrier
; #define ATT_SBAR() __builtin_amdgcn_sched_barrier(0)
; __device__ __forceinline__ unsigned cvtpk(float lo, float hi) { f32x2_t v = {lo, hi}; bf16x2_t b = __builtin_convertvector(v, bf16x2_t); return __builtin_bit_cast(unsigned, b); }
; #define ATT_LOAD_K(t) do { const unsigned so_ = (unsigned)(t) * (unsigned)(KVBLK * LDK * 2); sk0 = __builtin_bit_cast(bf16x8, __builtin_amdgcn_raw_buffer_load_b128(krs, koff, so_, 0)); \
;     if constexpr (DQK == 128) sk1 = __builtin_bit_cast(bf16x8, __builtin_amdgcn_raw_buffer_load_b128(krs, koff, so_ + (unsigned)(32 * LDK * 2), 0)); } while (0)
; #define ATT_LOAD_V(t) do { const unsigned so_ = (unsigned)(t) * (unsigned)(KVBLK * LDV * 2); sv0 = __builtin_bit_cast(bf16x8, __builtin_amdgcn_raw_buffer_load_b128(vrs, voff, so_, 0)); \
;     sv1 = __builtin_bit_cast(bf16x8, __builtin_amdgcn_raw_buffer_load_b128(vrs, voff, so_ + (unsigned)(32 * LDV * 2), 0)); } while (0)
; #define ATT_WRITE_K(so) do { *(bf16x8*)(K_lds + (so) + kswz<DQK>(kr, kc * 2)) = sk0; if constexpr (DQK == 128) *(bf16x8*)(K_lds + (so) + kswz<DQK>(32 + kr, kc * 2)) = sk1; } while (0)
; #define ATT_WRITE_V(so) do { *(bf16x8*)(V_lds + (so) + vst0) = sv0; *(bf16x8*)(V_lds + (so) + vst1) = sv1; } while (0)
;     ...
;   for (int t = 0; t + 1 < NT; ++t) {
;     if constexpr (ABL & 1) { u32x4 w0 = {cvtpk(p0[0], p0[1]), cvtpk(p0[2], p0[3]), cvtpk(p0[4], p0[5]), cvtpk(p0[6], p0[7])}, w1 = {cvtpk(p0[8], p0[9]), cvtpk(p0[10], p0[11]), cvtpk(p0[12], p0[13]), cvtpk(p0[14], p0[15])};
;         u32x4 w2 = {cvtpk(p1[0], p1[1]), cvtpk(p1[2], p1[3]), cvtpk(p1[4], p1[5]), cvtpk(p1[6], p1[7])}, w3 = {cvtpk(p1[8], p1[9]), cvtpk(p1[10], p1[11]), cvtpk(p1[12], p1[13]), cvtpk(p1[14], p1[15])};
;         pa0 = *reinterpret_cast<bf16x8*>(&w0); pa1 = *reinterpret_cast<bf16x8*>(&w1); pa2 = *reinterpret_cast<bf16x8*>(&w2); pa3 = *reinterpret_cast<bf16x8*>(&w3); }
;     else { ATT_SOFTMAX(t == 0); }
;     if constexpr (!(ABL & 4)) { ATT_WRITE_K(k2); ATT_WRITE_V(v1); }
;     ATT_SBAR();
; #pragma unroll
;     for (int ks = 0; ks < 4; ++ks) ATT_VPAIR(va, v0, 0, ks);
;     asm volatile("s_waitcnt lgkmcnt(8)" ::: "memory"); ATT_BAR();
;     ATT_XSECTION(true);
;     if constexpr (!(ABL & 4)) { const int tk = (t + 3 < NT) ? t + 3 : NT - 1, tv = (t + 2 < NT) ? t + 2 : NT - 1; ATT_LOAD_K(tk); ATT_LOAD_V(tv); }
	s_setprio 2
	s_waitcnt lgkmcnt(6)
	v_mfma_f32_32x32x16_bf16 v[66:81], v[98:101], v[2:5], 0
	ds_read_b64_tr_b16 v[34:35], v131 offset:512
	ds_read_b64_tr_b16 v[36:37], v131 offset:2560
	s_waitcnt lgkmcnt(6)
	v_mfma_f32_32x32x16_bf16 v[66:81], v[102:105], v[6:9], v[66:81]
	ds_read_b64_tr_b16 v[2:3], v131 offset:4608
	ds_read_b64_tr_b16 v[4:5], v131 offset:6656
	s_waitcnt lgkmcnt(6)
	v_mfma_f32_32x32x16_bf16 v[66:81], v[106:109], v[10:13], v[66:81]
	ds_read_b64_tr_b16 v[6:7], v131 offset:8704
	ds_read_b64_tr_b16 v[8:9], v131 offset:10752
	s_waitcnt lgkmcnt(6)
	v_mfma_f32_32x32x16_bf16 v[66:81], v[110:113], v[14:17], v[66:81]
	ds_read_b64_tr_b16 v[10:11], v131 offset:12800
	ds_read_b64_tr_b16 v[12:13], v131 offset:14848
	s_waitcnt lgkmcnt(6)
	v_mfma_f32_32x32x16_bf16 v[50:65], v[98:101], v[34:37], 0
	ds_read_b64_tr_b16 v[14:15], v131 offset:1024
	ds_read_b64_tr_b16 v[16:17], v131 offset:3072
	s_waitcnt lgkmcnt(6)
	v_mfma_f32_32x32x16_bf16 v[50:65], v[102:105], v[2:5], v[50:65]
	ds_read_b64_tr_b16 v[114:115], v131 offset:5120
	ds_read_b64_tr_b16 v[116:117], v131 offset:7168
	s_waitcnt lgkmcnt(6)
	v_mfma_f32_32x32x16_bf16 v[50:65], v[106:109], v[6:9], v[50:65]
	ds_read_b64_tr_b16 v[2:3], v131 offset:9216
	ds_read_b64_tr_b16 v[4:5], v131 offset:11264
	s_waitcnt lgkmcnt(6)
	v_mfma_f32_32x32x16_bf16 v[50:65], v[110:113], v[10:13], v[50:65]
	ds_read_b64_tr_b16 v[6:7], v131 offset:13312
	ds_read_b64_tr_b16 v[8:9], v131 offset:15360
	s_waitcnt lgkmcnt(6)
	v_mfma_f32_32x32x16_bf16 v[34:49], v[98:101], v[14:17], 0
	ds_read_b64_tr_b16 v[10:11], v131 offset:1536
	ds_read_b64_tr_b16 v[12:13], v131 offset:3584
	s_waitcnt lgkmcnt(6)
	v_mfma_f32_32x32x16_bf16 v[34:49], v[102:105], v[114:117], v[34:49]
	ds_read_b64_tr_b16 v[118:119], v131 offset:5632
	ds_read_b64_tr_b16 v[120:121], v131 offset:7680
	s_waitcnt lgkmcnt(6)
	v_mfma_f32_32x32x16_bf16 v[34:49], v[106:109], v[2:5], v[34:49]
	ds_read_b64_tr_b16 v[114:115], v131 offset:9728
	ds_read_b64_tr_b16 v[116:117], v131 offset:11776
	s_waitcnt lgkmcnt(6)
	v_mfma_f32_32x32x16_bf16 v[34:49], v[110:113], v[6:9], v[34:49]
	ds_read_b64_tr_b16 v[122:123], v131 offset:13824
	ds_read_b64_tr_b16 v[124:125], v131 offset:15872
	s_waitcnt lgkmcnt(6)
	v_mfma_f32_32x32x16_bf16 v[2:17], v[98:101], v[10:13], 0
	ds_read_b128 v[126:129], v173 offset:58368
	s_waitcnt lgkmcnt(5)
	v_mfma_f32_32x32x16_bf16 v[2:17], v[102:105], v[118:121], v[2:17]
	ds_read_b128 v[152:155], v173 offset:62976
	s_waitcnt lgkmcnt(4)
	v_mfma_f32_32x32x16_bf16 v[2:17], v[106:109], v[114:117], v[2:17]
	ds_read_b128 v[156:159], v173 offset:58400
	s_waitcnt lgkmcnt(3)
	v_mfma_f32_32x32x16_bf16 v[2:17], v[110:113], v[122:125], v[2:17]
	ds_read_b128 v[160:163], v173 offset:63008
	v_mfma_f32_4x4x4_16b_bf16 v[240:243], v[98:99], v[132:133], 0
	ds_read_b128 v[174:177], v173 offset:58432
	v_mfma_f32_4x4x4_16b_bf16 v[244:247], v[100:101], v[132:133], 0
	v_mfma_f32_4x4x4_16b_bf16 v[240:243], v[102:103], v[132:133], v[240:243]
	ds_read_b128 v[178:181], v173 offset:63040
	v_mfma_f32_4x4x4_16b_bf16 v[244:247], v[104:105], v[132:133], v[244:247]
	v_mfma_f32_4x4x4_16b_bf16 v[240:243], v[106:107], v[132:133], v[240:243]
	ds_read_b128 v[186:189], v173 offset:58464
	v_mfma_f32_4x4x4_16b_bf16 v[244:247], v[108:109], v[132:133], v[244:247]
	v_mfma_f32_4x4x4_16b_bf16 v[240:243], v[110:111], v[132:133], v[240:243]
	ds_read_b128 v[190:193], v173 offset:63072
	v_mfma_f32_4x4x4_16b_bf16 v[244:247], v[112:113], v[132:133], v[244:247]
	s_waitcnt lgkmcnt(7)
	v_mfma_f32_32x32x16_bf16 v[98:113], v[126:129], v[136:139], v[82:97]
	v_mov_b64_e32 v[128:129], v[96:97]
	v_mov_b64_e32 v[126:127], v[94:95]
	v_mov_b64_e32 v[124:125], v[92:93]
	v_mov_b64_e32 v[122:123], v[90:91]
	v_mov_b64_e32 v[120:121], v[88:89]
	v_mov_b64_e32 v[118:119], v[86:87]
	v_mov_b64_e32 v[116:117], v[84:85]
	v_mov_b64_e32 v[114:115], v[82:83]
	s_waitcnt lgkmcnt(6)
	s_nop 0
	v_mfma_f32_32x32x16_bf16 v[114:129], v[152:155], v[136:139], v[114:129]
	s_waitcnt lgkmcnt(5)
	v_mfma_f32_32x32x16_bf16 v[98:113], v[156:159], v[140:143], v[98:113]
	s_waitcnt lgkmcnt(4)
	v_mfma_f32_32x32x16_bf16 v[114:129], v[160:163], v[140:143], v[114:129]
	s_waitcnt lgkmcnt(3)
	v_mfma_f32_32x32x16_bf16 v[98:113], v[174:177], v[144:147], v[98:113]
	s_waitcnt lgkmcnt(2)
	v_mfma_f32_32x32x16_bf16 v[114:129], v[178:181], v[144:147], v[114:129]
	s_waitcnt lgkmcnt(1)
	v_mfma_f32_32x32x16_bf16 v[98:113], v[186:189], v[148:151], v[98:113]
	s_waitcnt lgkmcnt(0)
	v_mfma_f32_32x32x16_bf16 v[114:129], v[190:193], v[148:151], v[114:129]
	s_setprio 0
	buffer_load_dwordx4 v[224:227], v171, s[8:11], s85 offen
	buffer_load_dwordx4 v[228:231], v172, s[12:15], s83 offen
	buffer_load_dwordx4 v[232:235], v172, s[12:15], s86 offen
	s_barrier
	s_mov_b32 s50, 0x8000
	s_movk_i32 s15, 0x4000
	s_movk_i32 s51, 0x2400
	s_mov_b32 s49, 0
	s_movk_i32 s14, 0x4800
	s_mov_b32 s36, 0x70000
	s_mov_b32 s48, 0
	s_nop 0
	v_add_f32_e32 v174, 0, v114
	v_max3_f32 v175, v174, v98, v99
	v_max3_f32 v175, v175, v100, v101
	v_max3_f32 v175, v175, v102, v103
	v_max3_f32 v175, v175, v104, v105
	v_max3_f32 v175, v175, v106, v107
	v_max3_f32 v175, v175, v108, v109
	v_max3_f32 v175, v175, v110, v111
	v_max3_f32 v175, v175, v112, v113
	v_max3_f32 v174, v175, v115, v116
	v_max3_f32 v174, v174, v117, v118
	v_max3_f32 v174, v174, v119, v120
	v_max3_f32 v174, v174, v121, v122
	v_max3_f32 v174, v174, v123, v124
	v_max3_f32 v174, v174, v125, v126
	v_max3_f32 v174, v174, v127, v128
	v_max_f32 v174, v174, v129
.LBB0_297:
	s_mov_b32 s37, s15
	s_mov_b32 s18, s14
	v_cmp_ge_f32_e32 vcc, s60, v174
	s_cmp_eq_u64 vcc, exec
	s_cbranch_scc0 .LBB0_300
; #define ATT_SBAR() __builtin_amdgcn_sched_barrier(0)
; __device__ __forceinline__ unsigned cvtpk(float lo, float hi) { f32x2_t v = {lo, hi}; bf16x2_t b = __builtin_convertvector(v, bf16x2_t); return __builtin_bit_cast(unsigned, b); }
; #define ATT_PK4(P, BASE, OUT) do { u32x4 w = {cvtpk(P[BASE + 0], P[BASE + 1]), cvtpk(P[BASE + 2], P[BASE + 3]), cvtpk(P[BASE + 4], P[BASE + 5]), cvtpk(P[BASE + 6], P[BASE + 7])}; \
;     OUT = *reinterpret_cast<bf16x8*>(&w); } while (0)
; #define ATT_WRITE_K(so) do { *(bf16x8*)(K_lds + (so) + kswz<DQK>(kr, kc * 2)) = sk0; if constexpr (DQK == 128) *(bf16x8*)(K_lds + (so) + kswz<DQK>(32 + kr, kc * 2)) = sk1; } while (0)
; #define ATT_WRITE_V(so) do { *(bf16x8*)(V_lds + (so) + vst0) = sv0; *(bf16x8*)(V_lds + (so) + vst1) = sv1; } while (0)
; #define ATT_BAR() do { ATT_SBAR(); asm volatile("s_barrier" ::: "memory"); ATT_SBAR(); } while (0)
; #define ATT_VPAIR(buf, so, blk, ks) do { if constexpr (!(ABL & 8) && !(ABL & 32)) { buf[2 * (ks)] = vtr(vq0 + (so) + v_rd_off(blk, ks, 0)); buf[2 * (ks) + 1] = vtr(vq0 + (so) + v_rd_off(blk, ks, 1)); } } while (0)
; __device__ __forceinline__ void softmax_exp_pack(f32x16& p0, f32x16& p1, bf16x8& pa0, bf16x8& pa1, bf16x8& pa2, bf16x8& pa3) {
; #pragma unroll
;   for (int r = 0; r < 16; ++r) { p0[r] = __builtin_amdgcn_exp2f(p0[r]); p1[r] = __builtin_amdgcn_exp2f(p1[r]); }
;     ...
;   ATT_PK4(p0, 0, pa0); ATT_PK4(p0, 8, pa1); ATT_PK4(p1, 0, pa2); ATT_PK4(p1, 8, pa3);
;     ...
;   for (int t = 0; t + 1 < NT; ++t) {
;     if constexpr (ABL & 1) { u32x4 w0 = {cvtpk(p0[0], p0[1]), cvtpk(p0[2], p0[3]), cvtpk(p0[4], p0[5]), cvtpk(p0[6], p0[7])}, w1 = {cvtpk(p0[8], p0[9]), cvtpk(p0[10], p0[11]), cvtpk(p0[12], p0[13]), cvtpk(p0[14], p0[15])};
;         u32x4 w2 = {cvtpk(p1[0], p1[1]), cvtpk(p1[2], p1[3]), cvtpk(p1[4], p1[5]), cvtpk(p1[6], p1[7])}, w3 = {cvtpk(p1[8], p1[9]), cvtpk(p1[10], p1[11]), cvtpk(p1[12], p1[13]), cvtpk(p1[14], p1[15])};
;         pa0 = *reinterpret_cast<bf16x8*>(&w0); pa1 = *reinterpret_cast<bf16x8*>(&w1); pa2 = *reinterpret_cast<bf16x8*>(&w2); pa3 = *reinterpret_cast<bf16x8*>(&w3); }
;     else { ATT_SOFTMAX(t == 0); }
;     if constexpr (!(ABL & 4)) { ATT_WRITE_K(k2); ATT_WRITE_V(v1); }
;     ATT_SBAR();
; #pragma unroll
;     for (int ks = 0; ks < 4; ++ks) ATT_VPAIR(va, v0, 0, ks);
;     asm volatile("s_waitcnt lgkmcnt(8)" ::: "memory"); ATT_BAR();
.LBB0_298:
	v_exp_f32_e32 v98, v98
	v_exp_f32_e32 v114, v114
	v_exp_f32_e32 v99, v99
	v_exp_f32_e32 v115, v115
	v_exp_f32_e32 v100, v100
	v_exp_f32_e32 v101, v101
	v_exp_f32_e32 v102, v102
	v_exp_f32_e32 v103, v103
	v_exp_f32_e32 v106, v106
	v_exp_f32_e32 v107, v107
	v_exp_f32_e32 v116, v116
	v_exp_f32_e32 v117, v117
	v_exp_f32_e32 v118, v118
	v_exp_f32_e32 v119, v119
	v_exp_f32_e32 v104, v104
	v_exp_f32_e32 v120, v120
	v_exp_f32_e32 v105, v105
	v_exp_f32_e32 v121, v121
	v_exp_f32_e32 v122, v122
	v_exp_f32_e32 v123, v123
	v_exp_f32_e32 v108, v108
	v_exp_f32_e32 v124, v124
	v_exp_f32_e32 v109, v109
	v_exp_f32_e32 v125, v125
	v_exp_f32_e32 v110, v110
	v_exp_f32_e32 v126, v126
	v_exp_f32_e32 v111, v111
	v_exp_f32_e32 v127, v127
	v_exp_f32_e32 v112, v112
	v_exp_f32_e32 v128, v128
	v_exp_f32_e32 v113, v113
	v_exp_f32_e32 v129, v129
	v_cvt_pk_bf16_f32 v18, v98, v99
	v_cvt_pk_bf16_f32 v19, v100, v101
	v_cvt_pk_bf16_f32 v20, v102, v103
	v_cvt_pk_bf16_f32 v22, v106, v107
	v_cvt_pk_bf16_f32 v26, v114, v115
	v_add_u32_e32 v114, s49, v170
	s_add_i32 s14, s50, 0
	s_waitcnt vmcnt(2)
	ds_write_b128 v114, v[224:227] offset:49152
	v_add_u32_e32 v114, s14, v168
	v_cvt_pk_bf16_f32 v21, v104, v105
	v_cvt_pk_bf16_f32 v23, v108, v109
	v_cvt_pk_bf16_f32 v24, v110, v111
	v_cvt_pk_bf16_f32 v25, v112, v113
	v_cvt_pk_bf16_f32 v27, v116, v117
	v_cvt_pk_bf16_f32 v28, v118, v119
	v_cvt_pk_bf16_f32 v29, v120, v121
	v_cvt_pk_bf16_f32 v30, v122, v123
	v_cvt_pk_bf16_f32 v31, v124, v125
	v_cvt_pk_bf16_f32 v32, v126, v127
	v_cvt_pk_bf16_f32 v33, v128, v129
	s_waitcnt vmcnt(1)
	ds_write_b128 v114, v[228:231]
	v_add_u32_e32 v114, s14, v169
	s_waitcnt vmcnt(0)
	ds_write_b128 v114, v[232:235]
	v_add_u32_e32 v249, s18, v173
	ds_read_b128 v[152:155], v249 offset:49152
	ds_read_b128 v[156:159], v249 offset:53760
	ds_read_b128 v[160:163], v249 offset:49184
	ds_read_b128 v[176:179], v249 offset:53792
	s_waitcnt lgkmcnt(4)
	s_barrier
	s_setprio 2
	s_waitcnt lgkmcnt(3)
	v_mfma_f32_32x32x16_bf16 v[98:113], v[152:155], v[136:139], v[82:97]
	ds_read_b128 v[180:183], v249 offset:49216
	s_waitcnt lgkmcnt(3)
	v_mfma_f32_32x32x16_bf16 v[114:129], v[156:159], v[136:139], v[82:97]
	ds_read_b128 v[186:189], v249 offset:53824
	v_add_u32_e32 v248, s37, v131
	s_waitcnt lgkmcnt(3)
	v_mfma_f32_32x32x16_bf16 v[98:113], v[160:163], v[140:143], v[98:113]
	ds_read_b128 v[190:193], v249 offset:49248
	ds_read_b64_tr_b16 v[198:199], v248
	ds_read_b64_tr_b16 v[200:201], v248 offset:2048
	s_waitcnt lgkmcnt(5)
	v_mfma_f32_32x32x16_bf16 v[114:129], v[176:179], v[140:143], v[114:129]
	ds_read_b128 v[194:197], v249 offset:53856
	ds_read_b64_tr_b16 v[212:213], v248 offset:4096
	ds_read_b64_tr_b16 v[214:215], v248 offset:6144
	s_waitcnt lgkmcnt(7)
	v_mfma_f32_32x32x16_bf16 v[98:113], v[180:183], v[144:147], v[98:113]
	ds_read_b64_tr_b16 v[216:217], v248 offset:8192
	ds_read_b64_tr_b16 v[218:219], v248 offset:10240
	s_waitcnt lgkmcnt(8)
	v_mfma_f32_32x32x16_bf16 v[114:129], v[186:189], v[144:147], v[114:129]
	ds_read_b64_tr_b16 v[220:221], v248 offset:12288
	ds_read_b64_tr_b16 v[222:223], v248 offset:14336
	s_waitcnt lgkmcnt(9)
	v_mfma_f32_32x32x16_bf16 v[98:113], v[190:193], v[148:151], v[98:113]
	s_waitcnt lgkmcnt(6)
	v_mfma_f32_32x32x16_bf16 v[114:129], v[194:197], v[148:151], v[114:129]
	v_mfma_f32_32x32x16_bf16 v[66:81], v[18:21], v[198:201], v[66:81]
	ds_read_b64_tr_b16 v[236:237], v248 offset:512
	ds_read_b64_tr_b16 v[238:239], v248 offset:2560
	s_waitcnt lgkmcnt(6)
	v_mfma_f32_32x32x16_bf16 v[66:81], v[22:25], v[212:215], v[66:81]
	ds_read_b64_tr_b16 v[198:199], v248 offset:4608
	ds_read_b64_tr_b16 v[200:201], v248 offset:6656
	s_waitcnt lgkmcnt(6)
	v_mfma_f32_32x32x16_bf16 v[66:81], v[26:29], v[216:219], v[66:81]
	ds_read_b64_tr_b16 v[212:213], v248 offset:8704
	ds_read_b64_tr_b16 v[214:215], v248 offset:10752
	s_waitcnt lgkmcnt(6)
	v_mfma_f32_32x32x16_bf16 v[66:81], v[30:33], v[220:223], v[66:81]
	ds_read_b64_tr_b16 v[216:217], v248 offset:12800
	ds_read_b64_tr_b16 v[218:219], v248 offset:14848
	v_max3_f32 v249, v98, v99, v100
	s_waitcnt lgkmcnt(6)
	v_mfma_f32_32x32x16_bf16 v[50:65], v[18:21], v[236:239], v[50:65]
	ds_read_b64_tr_b16 v[220:221], v248 offset:1024
	ds_read_b64_tr_b16 v[222:223], v248 offset:3072
	v_max3_f32 v174, v114, v115, v116
	s_waitcnt lgkmcnt(6)
	v_mfma_f32_32x32x16_bf16 v[50:65], v[22:25], v[198:201], v[50:65]
	ds_read_b64_tr_b16 v[236:237], v248 offset:5120
	ds_read_b64_tr_b16 v[238:239], v248 offset:7168
	v_max3_f32 v249, v249, v101, v102
	s_waitcnt lgkmcnt(6)
	v_mfma_f32_32x32x16_bf16 v[50:65], v[26:29], v[212:215], v[50:65]
	ds_read_b64_tr_b16 v[198:199], v248 offset:9216
	ds_read_b64_tr_b16 v[200:201], v248 offset:11264
	v_max3_f32 v174, v174, v117, v118
	s_waitcnt lgkmcnt(6)
	v_mfma_f32_32x32x16_bf16 v[50:65], v[30:33], v[216:219], v[50:65]
	ds_read_b64_tr_b16 v[212:213], v248 offset:13312
	ds_read_b64_tr_b16 v[214:215], v248 offset:15360
	v_max3_f32 v249, v249, v103, v104
	s_waitcnt lgkmcnt(6)
	v_mfma_f32_32x32x16_bf16 v[34:49], v[18:21], v[220:223], v[34:49]
	ds_read_b64_tr_b16 v[216:217], v248 offset:1536
	ds_read_b64_tr_b16 v[218:219], v248 offset:3584
	v_max3_f32 v174, v174, v119, v120
	s_waitcnt lgkmcnt(6)
; #define ATT_SBAR() __builtin_amdgcn_sched_barrier(0)
; __device__ __forceinline__ unsigned cvtpk(float lo, float hi) { f32x2_t v = {lo, hi}; bf16x2_t b = __builtin_convertvector(v, bf16x2_t); return __builtin_bit_cast(unsigned, b); }
; #define ATT_LOAD_K(t) do { const unsigned so_ = (unsigned)(t) * (unsigned)(KVBLK * LDK * 2); sk0 = __builtin_bit_cast(bf16x8, __builtin_amdgcn_raw_buffer_load_b128(krs, koff, so_, 0)); \
;     if constexpr (DQK == 128) sk1 = __builtin_bit_cast(bf16x8, __builtin_amdgcn_raw_buffer_load_b128(krs, koff, so_ + (unsigned)(32 * LDK * 2), 0)); } while (0)
; #define ATT_LOAD_V(t) do { const unsigned so_ = (unsigned)(t) * (unsigned)(KVBLK * LDV * 2); sv0 = __builtin_bit_cast(bf16x8, __builtin_amdgcn_raw_buffer_load_b128(vrs, voff, so_, 0)); \
;     sv1 = __builtin_bit_cast(bf16x8, __builtin_amdgcn_raw_buffer_load_b128(vrs, voff, so_ + (unsigned)(32 * LDV * 2), 0)); } while (0)
; #define ATT_WRITE_K(so) do { *(bf16x8*)(K_lds + (so) + kswz<DQK>(kr, kc * 2)) = sk0; if constexpr (DQK == 128) *(bf16x8*)(K_lds + (so) + kswz<DQK>(32 + kr, kc * 2)) = sk1; } while (0)
;     ...
;   for (int t = 0; t + 1 < NT; ++t) {
;     if constexpr (ABL & 1) { u32x4 w0 = {cvtpk(p0[0], p0[1]), cvtpk(p0[2], p0[3]), cvtpk(p0[4], p0[5]), cvtpk(p0[6], p0[7])}, w1 = {cvtpk(p0[8], p0[9]), cvtpk(p0[10], p0[11]), cvtpk(p0[12], p0[13]), cvtpk(p0[14], p0[15])};
;         u32x4 w2 = {cvtpk(p1[0], p1[1]), cvtpk(p1[2], p1[3]), cvtpk(p1[4], p1[5]), cvtpk(p1[6], p1[7])}, w3 = {cvtpk(p1[8], p1[9]), cvtpk(p1[10], p1[11]), cvtpk(p1[12], p1[13]), cvtpk(p1[14], p1[15])};
;         pa0 = *reinterpret_cast<bf16x8*>(&w0); pa1 = *reinterpret_cast<bf16x8*>(&w1); pa2 = *reinterpret_cast<bf16x8*>(&w2); pa3 = *reinterpret_cast<bf16x8*>(&w3); }
;     else { ATT_SOFTMAX(t == 0); }
;     if constexpr (!(ABL & 4)) { ATT_WRITE_K(k2); ATT_WRITE_V(v1); }
;     ATT_SBAR();
; #pragma unroll
;     for (int ks = 0; ks < 4; ++ks) ATT_VPAIR(va, v0, 0, ks);
;     asm volatile("s_waitcnt lgkmcnt(8)" ::: "memory"); ATT_BAR();
;     ATT_XSECTION(true);
;     if constexpr (!(ABL & 4)) { const int tk = (t + 3 < NT) ? t + 3 : NT - 1, tv = (t + 2 < NT) ? t + 2 : NT - 1; ATT_LOAD_K(tk); ATT_LOAD_V(tv); }
;     ATT_BAR();
;     { const int tk_ = k0; k0 = k1; k1 = k2; k2 = tk_; const int tv_ = v0; v0 = v1; v1 = v2; v2 = tv_; }
	v_mfma_f32_32x32x16_bf16 v[34:49], v[22:25], v[236:239], v[34:49]
	ds_read_b64_tr_b16 v[220:221], v248 offset:5632
	ds_read_b64_tr_b16 v[222:223], v248 offset:7680
	v_max3_f32 v249, v249, v105, v106
	s_waitcnt lgkmcnt(6)
	v_mfma_f32_32x32x16_bf16 v[34:49], v[26:29], v[198:201], v[34:49]
	ds_read_b64_tr_b16 v[236:237], v248 offset:9728
	ds_read_b64_tr_b16 v[238:239], v248 offset:11776
	v_max3_f32 v174, v174, v121, v122
	s_waitcnt lgkmcnt(6)
	v_mfma_f32_32x32x16_bf16 v[34:49], v[30:33], v[212:215], v[34:49]
	ds_read_b64_tr_b16 v[198:199], v248 offset:13824
	ds_read_b64_tr_b16 v[200:201], v248 offset:15872
	v_max3_f32 v249, v249, v107, v108
	s_waitcnt lgkmcnt(6)
	v_mfma_f32_32x32x16_bf16 v[2:17], v[18:21], v[216:219], v[2:17]
	v_max3_f32 v174, v174, v123, v124
	s_min_u32 s14, s90, 0x7c
	s_lshl_b32 s14, s14, 17
	s_add_i32 s19, s14, 0x60000
	s_add_i32 s92, s36, 0xffff0000
	s_mov_b32 s14, s10
	s_mov_b32 s15, s11
	buffer_load_dwordx4 v[224:227], v171, s[8:11], s19 offen
	s_waitcnt lgkmcnt(4)
	v_mfma_f32_32x32x16_bf16 v[2:17], v[22:25], v[220:223], v[2:17]
	v_max3_f32 v249, v249, v109, v110
	buffer_load_dwordx4 v[228:231], v172, s[12:15], s92 offen
	s_waitcnt lgkmcnt(2)
	v_mfma_f32_32x32x16_bf16 v[2:17], v[26:29], v[236:239], v[2:17]
	v_max3_f32 v174, v174, v125, v126
	buffer_load_dwordx4 v[232:235], v172, s[12:15], s36 offen
	s_waitcnt lgkmcnt(0)
	v_mfma_f32_32x32x16_bf16 v[2:17], v[30:33], v[198:201], v[2:17]
	v_max3_f32 v249, v249, v111, v112
	v_mfma_f32_4x4x4_16b_bf16 v[240:243], v[18:19], v[132:133], v[240:243]
	v_max3_f32 v174, v174, v127, v128
	v_mfma_f32_4x4x4_16b_bf16 v[244:247], v[20:21], v[132:133], v[244:247]
	v_mfma_f32_4x4x4_16b_bf16 v[240:243], v[22:23], v[132:133], v[240:243]
	v_max_f32 v249, v249, v113
	v_mfma_f32_4x4x4_16b_bf16 v[244:247], v[24:25], v[132:133], v[244:247]
	v_mfma_f32_4x4x4_16b_bf16 v[240:243], v[26:27], v[132:133], v[240:243]
	v_max_f32 v174, v174, v129
	v_mfma_f32_4x4x4_16b_bf16 v[244:247], v[28:29], v[132:133], v[244:247]
	v_mfma_f32_4x4x4_16b_bf16 v[240:243], v[30:31], v[132:133], v[240:243]
	v_max_f32 v174, v174, v249
	v_mfma_f32_4x4x4_16b_bf16 v[244:247], v[32:33], v[132:133], v[244:247]
	s_setprio 0
	s_barrier
	s_add_i32 s36, s36, 0x20000
	s_add_i32 s90, s90, 1
	s_cmpk_eq_i32 s90, 0x7e
	s_cbranch_scc1 .LBB0_305
	s_mov_b32 s14, s49
	s_mov_b32 s49, s51
	s_mov_b32 s51, s18
	s_mov_b32 s15, s50
	s_mov_b32 s50, s48
	s_mov_b32 s48, s37
	s_branch .LBB0_297
.LBB0_300:
	v_mov_b32_e32 v175, v174
	s_nop 1
	v_permlane32_swap_b32_e32 v174, v175
	v_max3_f32 v174, v174, v175, 0
	v_exp_f32_e64 v175, -v174
	s_nop 4
	s_nop 0
	v_cmp_gt_f32_e32 vcc, 1.0, v175
	s_cbranch_vccz .LBB0_304
	v_mul_f32_dpp v240, v175, v240 quad_perm:[0,0,0,0] row_mask:0xf bank_mask:0xf
	v_mul_f32_dpp v241, v175, v241 quad_perm:[1,1,1,1] row_mask:0xf bank_mask:0xf
	v_mul_f32_dpp v242, v175, v242 quad_perm:[2,2,2,2] row_mask:0xf bank_mask:0xf
	v_mul_f32_dpp v243, v175, v243 quad_perm:[3,3,3,3] row_mask:0xf bank_mask:0xf
	v_mul_f32_dpp v244, v175, v244 quad_perm:[0,0,0,0] row_mask:0xf bank_mask:0xf
	v_mul_f32_dpp v245, v175, v245 quad_perm:[1,1,1,1] row_mask:0xf bank_mask:0xf
	v_mul_f32_dpp v246, v175, v246 quad_perm:[2,2,2,2] row_mask:0xf bank_mask:0xf
	v_mul_f32_dpp v247, v175, v247 quad_perm:[3,3,3,3] row_mask:0xf bank_mask:0xf
	s_and_saveexec_b64 s[14:15], s[4:5]
	ds_write_b32 v166, v175
	s_or_b64 exec, exec, s[14:15]
	s_waitcnt lgkmcnt(0)
	v_add_u32_e32 v175, s6, v184
	ds_read_b128 v[176:179], v175 offset:96
	ds_read_b128 v[180:183], v175 offset:64
	ds_read_b128 v[186:189], v175 offset:32
	ds_read_b128 v[190:193], v175
	s_waitcnt lgkmcnt(3)
	v_pk_mul_f32 v[78:79], v[78:79], v[176:177]
	s_waitcnt lgkmcnt(2)
	v_pk_mul_f32 v[74:75], v[74:75], v[180:181]
	s_waitcnt lgkmcnt(1)
	v_pk_mul_f32 v[70:71], v[70:71], v[186:187]
	v_pk_mul_f32 v[80:81], v[80:81], v[178:179]
	v_pk_mul_f32 v[76:77], v[76:77], v[182:183]
	v_pk_mul_f32 v[72:73], v[72:73], v[188:189]
	s_waitcnt lgkmcnt(0)
	v_pk_mul_f32 v[68:69], v[68:69], v[192:193]
	v_pk_mul_f32 v[66:67], v[66:67], v[190:191]
	v_pk_mul_f32 v[62:63], v[62:63], v[176:177]
	v_pk_mul_f32 v[58:59], v[58:59], v[180:181]
	v_pk_mul_f32 v[54:55], v[54:55], v[186:187]
	v_pk_mul_f32 v[64:65], v[64:65], v[178:179]
	v_pk_mul_f32 v[60:61], v[60:61], v[182:183]
	v_pk_mul_f32 v[56:57], v[56:57], v[188:189]
	v_pk_mul_f32 v[52:53], v[52:53], v[192:193]
	v_pk_mul_f32 v[50:51], v[50:51], v[190:191]
	v_pk_mul_f32 v[46:47], v[46:47], v[176:177]
	v_pk_mul_f32 v[42:43], v[42:43], v[180:181]
	v_pk_mul_f32 v[38:39], v[38:39], v[186:187]
	v_pk_mul_f32 v[48:49], v[48:49], v[178:179]
	v_pk_mul_f32 v[44:45], v[44:45], v[182:183]
	v_pk_mul_f32 v[40:41], v[40:41], v[188:189]
	v_pk_mul_f32 v[36:37], v[36:37], v[192:193]
	v_pk_mul_f32 v[34:35], v[34:35], v[190:191]
	v_pk_mul_f32 v[14:15], v[14:15], v[176:177]
	v_pk_mul_f32 v[10:11], v[10:11], v[180:181]
	v_pk_mul_f32 v[6:7], v[6:7], v[186:187]
	v_pk_mul_f32 v[16:17], v[16:17], v[178:179]
	v_pk_mul_f32 v[12:13], v[12:13], v[182:183]
	v_pk_mul_f32 v[8:9], v[8:9], v[188:189]
	v_pk_mul_f32 v[4:5], v[4:5], v[192:193]
	v_pk_mul_f32 v[2:3], v[2:3], v[190:191]

; #define ATT_SBAR() __builtin_amdgcn_sched_barrier(0)
; __device__ __forceinline__ unsigned cvtpk(float lo, float hi) { f32x2_t v = {lo, hi}; bf16x2_t b = __builtin_convertvector(v, bf16x2_t); return __builtin_bit_cast(unsigned, b); }
; #define ATT_LOAD_K(t) do { const unsigned so_ = (unsigned)(t) * (unsigned)(KVBLK * LDK * 2); sk0 = __builtin_bit_cast(bf16x8, __builtin_amdgcn_raw_buffer_load_b128(krs, koff, so_, 0)); \
;     if constexpr (DQK == 128) sk1 = __builtin_bit_cast(bf16x8, __builtin_amdgcn_raw_buffer_load_b128(krs, koff, so_ + (unsigned)(32 * LDK * 2), 0)); } while (0)
; #define ATT_LOAD_V(t) do { const unsigned so_ = (unsigned)(t) * (unsigned)(KVBLK * LDV * 2); sv0 = __builtin_bit_cast(bf16x8, __builtin_amdgcn_raw_buffer_load_b128(vrs, voff, so_, 0)); \
;     sv1 = __builtin_bit_cast(bf16x8, __builtin_amdgcn_raw_buffer_load_b128(vrs, voff, so_ + (unsigned)(32 * LDV * 2), 0)); } while (0)
; #define ATT_WRITE_K(so) do { *(bf16x8*)(K_lds + (so) + kswz<DQK>(kr, kc * 2)) = sk0; if constexpr (DQK == 128) *(bf16x8*)(K_lds + (so) + kswz<DQK>(32 + kr, kc * 2)) = sk1; } while (0)
;     ...
;   for (int t = 0; t + 1 < NT; ++t) {
;     if constexpr (ABL & 1) { u32x4 w0 = {cvtpk(p0[0], p0[1]), cvtpk(p0[2], p0[3]), cvtpk(p0[4], p0[5]), cvtpk(p0[6], p0[7])}, w1 = {cvtpk(p0[8], p0[9]), cvtpk(p0[10], p0[11]), cvtpk(p0[12], p0[13]), cvtpk(p0[14], p0[15])};
;         u32x4 w2 = {cvtpk(p1[0], p1[1]), cvtpk(p1[2], p1[3]), cvtpk(p1[4], p1[5]), cvtpk(p1[6], p1[7])}, w3 = {cvtpk(p1[8], p1[9]), cvtpk(p1[10], p1[11]), cvtpk(p1[12], p1[13]), cvtpk(p1[14], p1[15])};
;         pa0 = *reinterpret_cast<bf16x8*>(&w0); pa1 = *reinterpret_cast<bf16x8*>(&w1); pa2 = *reinterpret_cast<bf16x8*>(&w2); pa3 = *reinterpret_cast<bf16x8*>(&w3); }
;     else { ATT_SOFTMAX(t == 0); }
;     if constexpr (!(ABL & 4)) { ATT_WRITE_K(k2); ATT_WRITE_V(v1); }
;     ATT_SBAR();
; #pragma unroll
;     for (int ks = 0; ks < 4; ++ks) ATT_VPAIR(va, v0, 0, ks);
;     asm volatile("s_waitcnt lgkmcnt(8)" ::: "memory"); ATT_BAR();
;     ATT_XSECTION(true);
;     if constexpr (!(ABL & 4)) { const int tk = (t + 3 < NT) ? t + 3 : NT - 1, tv = (t + 2 < NT) ? t + 2 : NT - 1; ATT_LOAD_K(tk); ATT_LOAD_V(tv); }
;     ATT_BAR();
;     { const int tk_ = k0; k0 = k1; k1 = k2; k2 = tk_; const int tv_ = v0; v0 = v1; v1 = v2; v2 = tv_; }
.LBB0_306:
	v_exp_f32_e32 v98, v98
	v_exp_f32_e32 v114, v114
	v_exp_f32_e32 v99, v99
	v_exp_f32_e32 v115, v115
	v_exp_f32_e32 v100, v100
	v_exp_f32_e32 v101, v101
	v_exp_f32_e32 v102, v102
	v_exp_f32_e32 v103, v103
	v_exp_f32_e32 v106, v106
	v_exp_f32_e32 v107, v107
	v_exp_f32_e32 v116, v116
	v_exp_f32_e32 v117, v117
	v_exp_f32_e32 v118, v118
	v_exp_f32_e32 v119, v119
	v_exp_f32_e32 v104, v104
	v_exp_f32_e32 v120, v120
	v_exp_f32_e32 v105, v105
	v_exp_f32_e32 v121, v121
	v_exp_f32_e32 v122, v122
	v_exp_f32_e32 v123, v123
	v_exp_f32_e32 v108, v108
	v_exp_f32_e32 v124, v124
	v_exp_f32_e32 v109, v109
	v_exp_f32_e32 v125, v125
	v_exp_f32_e32 v110, v110
	v_exp_f32_e32 v126, v126
	v_exp_f32_e32 v111, v111
	v_exp_f32_e32 v127, v127
	v_exp_f32_e32 v112, v112
	v_exp_f32_e32 v128, v128
	v_exp_f32_e32 v113, v113
	v_exp_f32_e32 v129, v129
	v_cvt_pk_bf16_f32 v98, v98, v99
	v_cvt_pk_bf16_f32 v99, v100, v101
	v_cvt_pk_bf16_f32 v100, v102, v103
	v_cvt_pk_bf16_f32 v102, v106, v107
	v_cvt_pk_bf16_f32 v106, v114, v115
	v_add_u32_e32 v114, s51, v170
	s_add_i32 s8, s48, 0
	s_waitcnt vmcnt(2)
	ds_write_b128 v114, v[224:227] offset:49152
	v_add_u32_e32 v114, s8, v168
	v_cvt_pk_bf16_f32 v101, v104, v105
	v_cvt_pk_bf16_f32 v103, v108, v109
	v_cvt_pk_bf16_f32 v104, v110, v111
	v_cvt_pk_bf16_f32 v105, v112, v113
	v_cvt_pk_bf16_f32 v107, v116, v117
	v_cvt_pk_bf16_f32 v108, v118, v119
	v_cvt_pk_bf16_f32 v109, v120, v121
	v_cvt_pk_bf16_f32 v110, v122, v123
	v_cvt_pk_bf16_f32 v111, v124, v125
	v_cvt_pk_bf16_f32 v112, v126, v127
	v_cvt_pk_bf16_f32 v113, v128, v129
	s_waitcnt vmcnt(1)
	ds_write_b128 v114, v[228:231]
	v_add_u32_e32 v114, s8, v169
	s_waitcnt vmcnt(0)
	ds_write_b128 v114, v[232:235]
	v_add_u32_e32 v156, s50, v131
	ds_read_b64_tr_b16 v[114:115], v156
	ds_read_b64_tr_b16 v[116:117], v156 offset:2048
	ds_read_b64_tr_b16 v[118:119], v156 offset:4096
	ds_read_b64_tr_b16 v[120:121], v156 offset:6144
	ds_read_b64_tr_b16 v[122:123], v156 offset:8192
	ds_read_b64_tr_b16 v[124:125], v156 offset:10240
	ds_read_b64_tr_b16 v[126:127], v156 offset:12288
	ds_read_b64_tr_b16 v[128:129], v156 offset:14336
	s_waitcnt lgkmcnt(8)
	s_barrier
	s_setprio 2
	s_waitcnt lgkmcnt(6)
	v_mfma_f32_32x32x16_bf16 v[66:81], v[98:101], v[114:117], v[66:81]
	ds_read_b64_tr_b16 v[152:153], v156 offset:512
	ds_read_b64_tr_b16 v[154:155], v156 offset:2560
	s_waitcnt lgkmcnt(6)
	v_mfma_f32_32x32x16_bf16 v[66:81], v[102:105], v[118:121], v[66:81]
	ds_read_b64_tr_b16 v[114:115], v156 offset:4608
	ds_read_b64_tr_b16 v[116:117], v156 offset:6656
	s_waitcnt lgkmcnt(6)
	v_mfma_f32_32x32x16_bf16 v[66:81], v[106:109], v[122:125], v[66:81]
	ds_read_b64_tr_b16 v[118:119], v156 offset:8704
	ds_read_b64_tr_b16 v[120:121], v156 offset:10752
	s_waitcnt lgkmcnt(6)
	v_mfma_f32_32x32x16_bf16 v[66:81], v[110:113], v[126:129], v[66:81]
	ds_read_b64_tr_b16 v[122:123], v156 offset:12800
	ds_read_b64_tr_b16 v[124:125], v156 offset:14848
	s_waitcnt lgkmcnt(6)
	v_mfma_f32_32x32x16_bf16 v[50:65], v[98:101], v[152:155], v[50:65]
	ds_read_b64_tr_b16 v[126:127], v156 offset:1024
	ds_read_b64_tr_b16 v[128:129], v156 offset:3072
	s_waitcnt lgkmcnt(6)
	v_mfma_f32_32x32x16_bf16 v[50:65], v[102:105], v[114:117], v[50:65]
	ds_read_b64_tr_b16 v[152:153], v156 offset:5120
	ds_read_b64_tr_b16 v[154:155], v156 offset:7168
	s_waitcnt lgkmcnt(6)
	v_mfma_f32_32x32x16_bf16 v[50:65], v[106:109], v[118:121], v[50:65]
	ds_read_b64_tr_b16 v[114:115], v156 offset:9216
	ds_read_b64_tr_b16 v[116:117], v156 offset:11264
	s_waitcnt lgkmcnt(6)
	v_mfma_f32_32x32x16_bf16 v[50:65], v[110:113], v[122:125], v[50:65]
	ds_read_b64_tr_b16 v[118:119], v156 offset:13312
	ds_read_b64_tr_b16 v[120:121], v156 offset:15360
	s_waitcnt lgkmcnt(6)
	v_mfma_f32_32x32x16_bf16 v[34:49], v[98:101], v[126:129], v[34:49]
	ds_read_b64_tr_b16 v[122:123], v156 offset:1536
	ds_read_b64_tr_b16 v[124:125], v156 offset:3584
	s_waitcnt lgkmcnt(6)
	v_mfma_f32_32x32x16_bf16 v[34:49], v[102:105], v[152:155], v[34:49]
	ds_read_b64_tr_b16 v[126:127], v156 offset:5632
	ds_read_b64_tr_b16 v[128:129], v156 offset:7680
	s_waitcnt lgkmcnt(6)
	v_mfma_f32_32x32x16_bf16 v[34:49], v[106:109], v[114:117], v[34:49]
	ds_read_b64_tr_b16 v[152:153], v156 offset:9728
	ds_read_b64_tr_b16 v[154:155], v156 offset:11776
	s_waitcnt lgkmcnt(6)
	v_mfma_f32_32x32x16_bf16 v[34:49], v[110:113], v[118:121], v[34:49]
	ds_read_b64_tr_b16 v[114:115], v156 offset:13824
	ds_read_b64_tr_b16 v[116:117], v156 offset:15872
	s_waitcnt lgkmcnt(6)
	v_mfma_f32_32x32x16_bf16 v[2:17], v[98:101], v[122:125], v[2:17]
	v_add3_u32 v167, v167, s49, v184
	ds_read_b128 v[118:121], v167 offset:49152
	s_waitcnt lgkmcnt(5)
	v_mfma_f32_32x32x16_bf16 v[2:17], v[102:105], v[126:129], v[2:17]
	ds_read_b128 v[122:125], v167 offset:53760
	s_waitcnt lgkmcnt(4)
	v_mfma_f32_32x32x16_bf16 v[2:17], v[106:109], v[152:155], v[2:17]
	ds_read_b128 v[126:129], v167 offset:49184
	s_waitcnt lgkmcnt(3)
	v_mfma_f32_32x32x16_bf16 v[2:17], v[110:113], v[114:117], v[2:17]
	ds_read_b128 v[152:155], v167 offset:53792
	v_mfma_f32_4x4x4_16b_bf16 v[240:243], v[98:99], v[132:133], v[240:243]
	ds_read_b128 v[114:117], v167 offset:49216
	v_mfma_f32_4x4x4_16b_bf16 v[244:247], v[100:101], v[132:133], v[244:247]
	v_mfma_f32_4x4x4_16b_bf16 v[240:243], v[102:103], v[132:133], v[240:243]
	ds_read_b128 v[156:159], v167 offset:53824
	v_mfma_f32_4x4x4_16b_bf16 v[244:247], v[104:105], v[132:133], v[244:247]
	v_mfma_f32_4x4x4_16b_bf16 v[240:243], v[106:107], v[132:133], v[240:243]
	ds_read_b128 v[160:163], v167 offset:49248
	v_mfma_f32_4x4x4_16b_bf16 v[244:247], v[108:109], v[132:133], v[244:247]
	v_mfma_f32_4x4x4_16b_bf16 v[240:243], v[110:111], v[132:133], v[240:243]
	ds_read_b128 v[168:171], v167 offset:53856
	v_mfma_f32_4x4x4_16b_bf16 v[244:247], v[112:113], v[132:133], v[244:247]
	s_waitcnt lgkmcnt(7)
	v_mfma_f32_32x32x16_bf16 v[98:113], v[118:121], v[136:139], v[82:97]
	s_waitcnt lgkmcnt(6)
	v_mfma_f32_32x32x16_bf16 v[82:97], v[122:125], v[136:139], v[82:97]
	s_waitcnt lgkmcnt(5)
	v_mfma_f32_32x32x16_bf16 v[98:113], v[126:129], v[140:143], v[98:113]
	s_waitcnt lgkmcnt(4)
	v_mfma_f32_32x32x16_bf16 v[82:97], v[152:155], v[140:143], v[82:97]
	s_waitcnt lgkmcnt(3)
	v_mfma_f32_32x32x16_bf16 v[98:113], v[114:117], v[144:147], v[98:113]
	s_waitcnt lgkmcnt(2)
	v_mfma_f32_32x32x16_bf16 v[82:97], v[156:159], v[144:147], v[82:97]
	s_waitcnt lgkmcnt(1)
	v_mfma_f32_32x32x16_bf16 v[98:113], v[160:163], v[148:151], v[98:113]
	s_waitcnt lgkmcnt(0)
	v_mfma_f32_32x32x16_bf16 v[82:97], v[168:171], v[148:151], v[82:97]
	s_setprio 0
	s_barrier
; #define ATT_BAR() do { ATT_SBAR(); asm volatile("s_barrier" ::: "memory"); ATT_SBAR(); } while (0)
; #define ATT_SOFTMAX(first_) do { const float pm_ = softmax_rowmax(p0, p1); \
;     if (__builtin_expect((first_) || !__all(pm_ <= THRL), 0)) { const float al_ = softmax_shift(p0, p1, negm, pm_, (first_)); ATT_RESC(al_); } \
;     softmax_exp_pack(p0, p1, pa0, pa1, pa2, pa3); } while (0)
; #define ATT_VPAIR(buf, so, blk, ks) do { if constexpr (!(ABL & 8) && !(ABL & 32)) { buf[2 * (ks)] = vtr(vq0 + (so) + v_rd_off(blk, ks, 0)); buf[2 * (ks) + 1] = vtr(vq0 + (so) + v_rd_off(blk, ks, 1)); } } while (0)
;     ...
;   ATT_SOFTMAX(false);
; #pragma unroll
;   for (int ks = 0; ks < 4; ++ks) ATT_VPAIR(va, v0, 0, ks);
;   asm volatile("s_waitcnt lgkmcnt(0)" ::: "memory"); ATT_BAR();
;   ATT_XSECTION(false);
;   ATT_BAR();
;   if (grp == 0) ATT_BAR();
	s_nop 10
	v_add_f32_e32 v114, 0, v82
	v_max3_f32 v115, v114, v98, v99
	v_max3_f32 v115, v115, v100, v101
	v_max3_f32 v115, v115, v102, v103
	v_max3_f32 v115, v115, v104, v105
	v_max3_f32 v115, v115, v106, v107
	v_max3_f32 v115, v115, v108, v109
	v_max3_f32 v115, v115, v110, v111
	v_max3_f32 v115, v115, v112, v113
	s_nop 0
	v_max3_f32 v114, v115, v83, v84
	v_max3_f32 v114, v114, v85, v86
	v_max3_f32 v114, v114, v87, v88
	v_max3_f32 v114, v114, v89, v90
	v_max3_f32 v114, v114, v91, v92
	v_max3_f32 v114, v114, v93, v94
	v_max3_f32 v114, v114, v95, v96
	v_max_f32 v114, v114, v97
	s_nop 0
	v_cmp_ge_f32_e32 vcc, s60, v114
	s_cmp_lg_u64 vcc, exec
	s_cbranch_scc1 .LBB0_334
.LBB0_307:
	v_exp_f32_e32 v98, v98
	v_exp_f32_e32 v114, v82
	v_exp_f32_e32 v82, v99
	v_exp_f32_e32 v99, v83
	v_exp_f32_e32 v83, v100
	v_exp_f32_e32 v100, v84
	v_exp_f32_e32 v84, v101
	v_exp_f32_e32 v101, v85
	v_exp_f32_e32 v85, v102
	v_exp_f32_e32 v102, v86
	v_exp_f32_e32 v86, v103
	v_exp_f32_e32 v103, v87
	v_exp_f32_e32 v87, v104
	v_exp_f32_e32 v104, v88
	v_exp_f32_e32 v88, v105
	v_exp_f32_e32 v105, v89
	v_exp_f32_e32 v89, v106
	v_exp_f32_e32 v106, v90
	v_exp_f32_e32 v90, v107
	v_exp_f32_e32 v107, v91
	v_exp_f32_e32 v91, v108
	v_exp_f32_e32 v108, v92
	v_exp_f32_e32 v92, v109
	v_exp_f32_e32 v109, v93
	v_exp_f32_e32 v93, v110
	v_exp_f32_e32 v110, v94
	v_exp_f32_e32 v94, v111
	v_exp_f32_e32 v111, v95
	v_exp_f32_e32 v95, v112
	v_exp_f32_e32 v112, v96
	v_exp_f32_e32 v96, v113
	v_exp_f32_e32 v97, v97
	v_add_u32_e32 v118, s48, v131
	v_cvt_pk_bf16_f32 v82, v98, v82
	v_cvt_pk_bf16_f32 v83, v83, v84
	v_cvt_pk_bf16_f32 v84, v85, v86
	v_cvt_pk_bf16_f32 v85, v87, v88
	v_cvt_pk_bf16_f32 v86, v89, v90
	v_cvt_pk_bf16_f32 v87, v91, v92
	v_cvt_pk_bf16_f32 v88, v93, v94
	v_cvt_pk_bf16_f32 v89, v95, v96
	v_cvt_pk_bf16_f32 v90, v114, v99
	v_cvt_pk_bf16_f32 v91, v100, v101
	v_cvt_pk_bf16_f32 v92, v102, v103
	v_cvt_pk_bf16_f32 v93, v104, v105
	v_cvt_pk_bf16_f32 v94, v106, v107
	v_cvt_pk_bf16_f32 v95, v108, v109
	v_cvt_pk_bf16_f32 v96, v110, v111
	v_cvt_pk_bf16_f32 v97, v112, v97
	ds_read_b64_tr_b16 v[98:99], v118
	ds_read_b64_tr_b16 v[100:101], v118 offset:2048
	ds_read_b64_tr_b16 v[102:103], v118 offset:4096
	ds_read_b64_tr_b16 v[104:105], v118 offset:6144
	ds_read_b64_tr_b16 v[106:107], v118 offset:8192
	ds_read_b64_tr_b16 v[108:109], v118 offset:10240
	ds_read_b64_tr_b16 v[110:111], v118 offset:12288
	ds_read_b64_tr_b16 v[112:113], v118 offset:14336
	s_waitcnt lgkmcnt(0)
	s_barrier
	s_setprio 2
	s_waitcnt lgkmcnt(6)
	v_mfma_f32_32x32x16_bf16 v[66:81], v[82:85], v[98:101], v[66:81]
	ds_read_b64_tr_b16 v[114:115], v118 offset:512
	ds_read_b64_tr_b16 v[116:117], v118 offset:2560
	s_waitcnt lgkmcnt(6)
	v_mfma_f32_32x32x16_bf16 v[66:81], v[86:89], v[102:105], v[66:81]
	ds_read_b64_tr_b16 v[98:99], v118 offset:4608
	ds_read_b64_tr_b16 v[100:101], v118 offset:6656
	s_waitcnt lgkmcnt(6)
	v_mfma_f32_32x32x16_bf16 v[66:81], v[90:93], v[106:109], v[66:81]
	ds_read_b64_tr_b16 v[102:103], v118 offset:8704
	ds_read_b64_tr_b16 v[104:105], v118 offset:10752
	s_waitcnt lgkmcnt(6)
	v_mfma_f32_32x32x16_bf16 v[66:81], v[94:97], v[110:113], v[66:81]
	ds_read_b64_tr_b16 v[106:107], v118 offset:12800
	ds_read_b64_tr_b16 v[108:109], v118 offset:14848
	s_waitcnt lgkmcnt(6)
	v_mfma_f32_32x32x16_bf16 v[50:65], v[82:85], v[114:117], v[50:65]
	ds_read_b64_tr_b16 v[110:111], v118 offset:1024
	ds_read_b64_tr_b16 v[112:113], v118 offset:3072
	s_waitcnt lgkmcnt(6)
	v_mfma_f32_32x32x16_bf16 v[50:65], v[86:89], v[98:101], v[50:65]
	ds_read_b64_tr_b16 v[114:115], v118 offset:5120
	ds_read_b64_tr_b16 v[116:117], v118 offset:7168
	s_waitcnt lgkmcnt(6)
	v_mfma_f32_32x32x16_bf16 v[50:65], v[90:93], v[102:105], v[50:65]
	ds_read_b64_tr_b16 v[98:99], v118 offset:9216
	ds_read_b64_tr_b16 v[100:101], v118 offset:11264
	s_waitcnt lgkmcnt(6)
	v_mfma_f32_32x32x16_bf16 v[50:65], v[94:97], v[106:109], v[50:65]
	ds_read_b64_tr_b16 v[102:103], v118 offset:13312
	ds_read_b64_tr_b16 v[104:105], v118 offset:15360
	s_waitcnt lgkmcnt(6)
	v_mfma_f32_32x32x16_bf16 v[34:49], v[82:85], v[110:113], v[34:49]
	ds_read_b64_tr_b16 v[106:107], v118 offset:1536
	ds_read_b64_tr_b16 v[108:109], v118 offset:3584
	s_waitcnt lgkmcnt(6)
	v_mfma_f32_32x32x16_bf16 v[34:49], v[86:89], v[114:117], v[34:49]
	ds_read_b64_tr_b16 v[110:111], v118 offset:5632
	ds_read_b64_tr_b16 v[112:113], v118 offset:7680
	s_waitcnt lgkmcnt(6)
	v_mfma_f32_32x32x16_bf16 v[34:49], v[90:93], v[98:101], v[34:49]
	ds_read_b64_tr_b16 v[114:115], v118 offset:9728
	ds_read_b64_tr_b16 v[116:117], v118 offset:11776
	s_waitcnt lgkmcnt(6)
	v_mfma_f32_32x32x16_bf16 v[34:49], v[94:97], v[102:105], v[34:49]
	ds_read_b64_tr_b16 v[98:99], v118 offset:13824
	ds_read_b64_tr_b16 v[100:101], v118 offset:15872
	s_waitcnt lgkmcnt(6)
	v_mfma_f32_32x32x16_bf16 v[2:17], v[82:85], v[106:109], v[2:17]
	s_waitcnt lgkmcnt(4)
	v_mfma_f32_32x32x16_bf16 v[2:17], v[86:89], v[110:113], v[2:17]
	s_waitcnt lgkmcnt(2)
	v_mfma_f32_32x32x16_bf16 v[2:17], v[90:93], v[114:117], v[2:17]
	s_waitcnt lgkmcnt(0)
	v_mfma_f32_32x32x16_bf16 v[2:17], v[94:97], v[98:101], v[2:17]
	v_mfma_f32_4x4x4_16b_bf16 v[240:243], v[82:83], v[132:133], v[240:243]
	v_mfma_f32_4x4x4_16b_bf16 v[244:247], v[84:85], v[132:133], v[244:247]
	s_nop 0
	v_mfma_f32_4x4x4_16b_bf16 v[240:243], v[86:87], v[132:133], v[240:243]
	v_mfma_f32_4x4x4_16b_bf16 v[244:247], v[88:89], v[132:133], v[244:247]
	s_nop 0
	v_mfma_f32_4x4x4_16b_bf16 v[240:243], v[90:91], v[132:133], v[240:243]
	v_mfma_f32_4x4x4_16b_bf16 v[244:247], v[92:93], v[132:133], v[244:247]
	s_nop 0
	v_mfma_f32_4x4x4_16b_bf16 v[240:243], v[94:95], v[132:133], v[240:243]
	v_mfma_f32_4x4x4_16b_bf16 v[244:247], v[96:97], v[132:133], v[244:247]
	s_nop 0
	s_setprio 0
	s_barrier
	s_cmpk_gt_u32 s91, 0xff
	s_cbranch_scc1 .LBB0_259
	s_barrier
	s_branch .LBB0_259
; __device__ __forceinline__ float softmax_shift(f32x16& p0, f32x16& p1, f32x16& negm, float pmax, bool first) {
;   asm volatile("s_nop 4" ::: "memory");
;   { auto rr = __builtin_amdgcn_permlane32_swap(__float_as_uint(pmax), __float_as_uint(pmax), false, false);
;     pmax = fmaxf(__uint_as_float(rr[0]), __uint_as_float(rr[1])); }
;   const float delta = first ? pmax : fmaxf(pmax, 0.f);
; #pragma unroll
;   for (int r = 0; r < 16; ++r) { p0[r] -= delta; p1[r] -= delta; negm[r] -= delta; }
;   return first ? 1.f : __builtin_amdgcn_exp2f(-delta);
; }
.LBB0_309:
	v_mov_b32_e32 v192, v191
	s_nop 1
	v_permlane32_swap_b32_e32 v191, v192
	v_max3_f32 v191, v191, v192, 0
	v_exp_f32_e64 v192, -v191
	s_nop 4
	s_nop 0
	v_cmp_gt_f32_e32 vcc, 1.0, v192
	s_cbranch_vccz .LBB0_313
	v_mul_f32_dpp v240, v192, v240 quad_perm:[0,0,0,0] row_mask:0xf bank_mask:0xf
	v_mul_f32_dpp v241, v192, v241 quad_perm:[1,1,1,1] row_mask:0xf bank_mask:0xf
	v_mul_f32_dpp v242, v192, v242 quad_perm:[2,2,2,2] row_mask:0xf bank_mask:0xf
	v_mul_f32_dpp v243, v192, v243 quad_perm:[3,3,3,3] row_mask:0xf bank_mask:0xf
	v_mul_f32_dpp v244, v192, v244 quad_perm:[0,0,0,0] row_mask:0xf bank_mask:0xf
	v_mul_f32_dpp v245, v192, v245 quad_perm:[1,1,1,1] row_mask:0xf bank_mask:0xf
	v_mul_f32_dpp v246, v192, v246 quad_perm:[2,2,2,2] row_mask:0xf bank_mask:0xf
	v_mul_f32_dpp v247, v192, v247 quad_perm:[3,3,3,3] row_mask:0xf bank_mask:0xf
	s_and_saveexec_b64 s[8:9], s[4:5]
	ds_write_b32 v187, v192
	s_or_b64 exec, exec, s[8:9]
	s_waitcnt lgkmcnt(0)
	v_add_u32_e32 v200, s90, v184
	ds_read_b128 v[192:195], v200 offset:96
	ds_read_b128 v[196:199], v200 offset:64
	ds_read_b128 v[212:215], v200 offset:32
	ds_read_b128 v[216:219], v200
	s_waitcnt lgkmcnt(3)
	v_pk_mul_f32 v[30:31], v[30:31], v[192:193]
	s_waitcnt lgkmcnt(2)
	v_pk_mul_f32 v[26:27], v[26:27], v[196:197]
	s_waitcnt lgkmcnt(1)
	v_pk_mul_f32 v[22:23], v[22:23], v[212:213]
	v_pk_mul_f32 v[32:33], v[32:33], v[194:195]
	v_pk_mul_f32 v[28:29], v[28:29], v[198:199]
	v_pk_mul_f32 v[24:25], v[24:25], v[214:215]
	s_waitcnt lgkmcnt(0)
	v_pk_mul_f32 v[20:21], v[20:21], v[218:219]
	v_pk_mul_f32 v[18:19], v[18:19], v[216:217]
	v_pk_mul_f32 v[46:47], v[46:47], v[192:193]
	v_pk_mul_f32 v[42:43], v[42:43], v[196:197]
	v_pk_mul_f32 v[38:39], v[38:39], v[212:213]
	v_pk_mul_f32 v[48:49], v[48:49], v[194:195]
	v_pk_mul_f32 v[44:45], v[44:45], v[198:199]
	v_pk_mul_f32 v[40:41], v[40:41], v[214:215]
	v_pk_mul_f32 v[36:37], v[36:37], v[218:219]
	v_pk_mul_f32 v[34:35], v[34:35], v[216:217]
	v_pk_mul_f32 v[62:63], v[62:63], v[192:193]
	v_pk_mul_f32 v[58:59], v[58:59], v[196:197]
	v_pk_mul_f32 v[54:55], v[54:55], v[212:213]
	v_pk_mul_f32 v[64:65], v[64:65], v[194:195]
	v_pk_mul_f32 v[60:61], v[60:61], v[198:199]
	v_pk_mul_f32 v[56:57], v[56:57], v[214:215]
	v_pk_mul_f32 v[52:53], v[52:53], v[218:219]
	v_pk_mul_f32 v[50:51], v[50:51], v[216:217]
	v_pk_mul_f32 v[78:79], v[78:79], v[192:193]
	v_pk_mul_f32 v[74:75], v[74:75], v[196:197]
	v_pk_mul_f32 v[70:71], v[70:71], v[212:213]
	v_pk_mul_f32 v[80:81], v[80:81], v[194:195]
	v_pk_mul_f32 v[76:77], v[76:77], v[198:199]
	v_pk_mul_f32 v[72:73], v[72:73], v[214:215]
	v_pk_mul_f32 v[68:69], v[68:69], v[218:219]
	v_pk_mul_f32 v[66:67], v[66:67], v[216:217]

; __device__ __forceinline__ float softmax_shift(f32x16& p0, f32x16& p1, f32x16& negm, float pmax, bool first) {
;   asm volatile("s_nop 4" ::: "memory");
;   { auto rr = __builtin_amdgcn_permlane32_swap(__float_as_uint(pmax), __float_as_uint(pmax), false, false);
;     pmax = fmaxf(__uint_as_float(rr[0]), __uint_as_float(rr[1])); }
;   const float delta = first ? pmax : fmaxf(pmax, 0.f);
; #pragma unroll
;   for (int r = 0; r < 16; ++r) { p0[r] -= delta; p1[r] -= delta; negm[r] -= delta; }
;   return first ? 1.f : __builtin_amdgcn_exp2f(-delta);
; }
.LBB0_314:
	v_mov_b32_e32 v115, v114
	s_nop 1
	v_permlane32_swap_b32_e32 v114, v115
	v_max3_f32 v114, v114, v115, 0
	v_exp_f32_e64 v115, -v114
	s_nop 4
	s_nop 0
	v_cmp_gt_f32_e32 vcc, 1.0, v115
	s_cbranch_vccz .LBB0_318
	v_mul_f32_dpp v240, v115, v240 quad_perm:[0,0,0,0] row_mask:0xf bank_mask:0xf
	v_mul_f32_dpp v241, v115, v241 quad_perm:[1,1,1,1] row_mask:0xf bank_mask:0xf
	v_mul_f32_dpp v242, v115, v242 quad_perm:[2,2,2,2] row_mask:0xf bank_mask:0xf
	v_mul_f32_dpp v243, v115, v243 quad_perm:[3,3,3,3] row_mask:0xf bank_mask:0xf
	v_mul_f32_dpp v244, v115, v244 quad_perm:[0,0,0,0] row_mask:0xf bank_mask:0xf
	v_mul_f32_dpp v245, v115, v245 quad_perm:[1,1,1,1] row_mask:0xf bank_mask:0xf
	v_mul_f32_dpp v246, v115, v246 quad_perm:[2,2,2,2] row_mask:0xf bank_mask:0xf
	v_mul_f32_dpp v247, v115, v247 quad_perm:[3,3,3,3] row_mask:0xf bank_mask:0xf
	s_and_saveexec_b64 s[8:9], s[4:5]
	ds_write_b32 v187, v115
	s_or_b64 exec, exec, s[8:9]
	s_waitcnt lgkmcnt(0)
	v_add_u32_e32 v115, s90, v184
	ds_read_b128 v[116:119], v115 offset:96
	ds_read_b128 v[120:123], v115 offset:64
	ds_read_b128 v[124:127], v115 offset:32
	ds_read_b128 v[136:139], v115
	s_waitcnt lgkmcnt(3)
	v_pk_mul_f32 v[30:31], v[30:31], v[116:117]
	s_waitcnt lgkmcnt(2)
	v_pk_mul_f32 v[26:27], v[26:27], v[120:121]
	s_waitcnt lgkmcnt(1)
	v_pk_mul_f32 v[22:23], v[22:23], v[124:125]
	v_pk_mul_f32 v[32:33], v[32:33], v[118:119]
	v_pk_mul_f32 v[28:29], v[28:29], v[122:123]
	v_pk_mul_f32 v[24:25], v[24:25], v[126:127]
	s_waitcnt lgkmcnt(0)
	v_pk_mul_f32 v[20:21], v[20:21], v[138:139]
	v_pk_mul_f32 v[18:19], v[18:19], v[136:137]
	v_pk_mul_f32 v[46:47], v[46:47], v[116:117]
	v_pk_mul_f32 v[42:43], v[42:43], v[120:121]
	v_pk_mul_f32 v[38:39], v[38:39], v[124:125]
	v_pk_mul_f32 v[48:49], v[48:49], v[118:119]
	v_pk_mul_f32 v[44:45], v[44:45], v[122:123]
	v_pk_mul_f32 v[40:41], v[40:41], v[126:127]
	v_pk_mul_f32 v[36:37], v[36:37], v[138:139]
	v_pk_mul_f32 v[34:35], v[34:35], v[136:137]
	v_pk_mul_f32 v[62:63], v[62:63], v[116:117]
	v_pk_mul_f32 v[58:59], v[58:59], v[120:121]
	v_pk_mul_f32 v[54:55], v[54:55], v[124:125]
	v_pk_mul_f32 v[64:65], v[64:65], v[118:119]
	v_pk_mul_f32 v[60:61], v[60:61], v[122:123]
	v_pk_mul_f32 v[56:57], v[56:57], v[126:127]
	v_pk_mul_f32 v[52:53], v[52:53], v[138:139]
	v_pk_mul_f32 v[50:51], v[50:51], v[136:137]
	v_pk_mul_f32 v[78:79], v[78:79], v[116:117]
	v_pk_mul_f32 v[74:75], v[74:75], v[120:121]
	v_pk_mul_f32 v[70:71], v[70:71], v[124:125]
	v_pk_mul_f32 v[80:81], v[80:81], v[118:119]
	v_pk_mul_f32 v[76:77], v[76:77], v[122:123]
	v_pk_mul_f32 v[72:73], v[72:73], v[126:127]
	v_pk_mul_f32 v[68:69], v[68:69], v[138:139]
	v_pk_mul_f32 v[66:67], v[66:67], v[136:137]

; __device__ __forceinline__ float softmax_shift(f32x16& p0, f32x16& p1, f32x16& negm, float pmax, bool first) {
;   asm volatile("s_nop 4" ::: "memory");
;   { auto rr = __builtin_amdgcn_permlane32_swap(__float_as_uint(pmax), __float_as_uint(pmax), false, false);
;     pmax = fmaxf(__uint_as_float(rr[0]), __uint_as_float(rr[1])); }
;   const float delta = first ? pmax : fmaxf(pmax, 0.f);
; #pragma unroll
;   for (int r = 0; r < 16; ++r) { p0[r] -= delta; p1[r] -= delta; negm[r] -= delta; }
;   return first ? 1.f : __builtin_amdgcn_exp2f(-delta);
; }
.LBB0_319:
	v_mov_b32_e32 v171, v170
	s_nop 1
	v_permlane32_swap_b32_e32 v170, v171
	v_max3_f32 v170, v170, v171, 0
	v_exp_f32_e64 v171, -v170
	s_nop 4
	s_nop 0
	v_cmp_gt_f32_e32 vcc, 1.0, v171
	s_cbranch_vccz .LBB0_323
	v_mul_f32_dpp v240, v171, v240 quad_perm:[0,0,0,0] row_mask:0xf bank_mask:0xf
	v_mul_f32_dpp v241, v171, v241 quad_perm:[1,1,1,1] row_mask:0xf bank_mask:0xf
	v_mul_f32_dpp v242, v171, v242 quad_perm:[2,2,2,2] row_mask:0xf bank_mask:0xf
	v_mul_f32_dpp v243, v171, v243 quad_perm:[3,3,3,3] row_mask:0xf bank_mask:0xf
	v_mul_f32_dpp v244, v171, v244 quad_perm:[0,0,0,0] row_mask:0xf bank_mask:0xf
	v_mul_f32_dpp v245, v171, v245 quad_perm:[1,1,1,1] row_mask:0xf bank_mask:0xf
	v_mul_f32_dpp v246, v171, v246 quad_perm:[2,2,2,2] row_mask:0xf bank_mask:0xf
	v_mul_f32_dpp v247, v171, v247 quad_perm:[3,3,3,3] row_mask:0xf bank_mask:0xf
	s_and_saveexec_b64 s[14:15], s[4:5]
	ds_write_b32 v165, v171
	s_or_b64 exec, exec, s[14:15]
	s_waitcnt lgkmcnt(0)
	v_add_u32_e32 v171, s6, v184
	ds_read_b128 v[172:175], v171 offset:96
	ds_read_b128 v[176:179], v171 offset:64
	ds_read_b128 v[180:183], v171 offset:32
	ds_read_b128 v[186:189], v171
	s_waitcnt lgkmcnt(3)
	v_pk_mul_f32 v[30:31], v[30:31], v[172:173]
	s_waitcnt lgkmcnt(2)
	v_pk_mul_f32 v[26:27], v[26:27], v[176:177]
	s_waitcnt lgkmcnt(1)
	v_pk_mul_f32 v[22:23], v[22:23], v[180:181]
	v_pk_mul_f32 v[32:33], v[32:33], v[174:175]
	v_pk_mul_f32 v[28:29], v[28:29], v[178:179]
	v_pk_mul_f32 v[24:25], v[24:25], v[182:183]
	s_waitcnt lgkmcnt(0)
	v_pk_mul_f32 v[20:21], v[20:21], v[188:189]
	v_pk_mul_f32 v[18:19], v[18:19], v[186:187]
	v_pk_mul_f32 v[46:47], v[46:47], v[172:173]
	v_pk_mul_f32 v[42:43], v[42:43], v[176:177]
	v_pk_mul_f32 v[38:39], v[38:39], v[180:181]
	v_pk_mul_f32 v[48:49], v[48:49], v[174:175]
	v_pk_mul_f32 v[44:45], v[44:45], v[178:179]
	v_pk_mul_f32 v[40:41], v[40:41], v[182:183]
	v_pk_mul_f32 v[36:37], v[36:37], v[188:189]
	v_pk_mul_f32 v[34:35], v[34:35], v[186:187]
	v_pk_mul_f32 v[62:63], v[62:63], v[172:173]
	v_pk_mul_f32 v[58:59], v[58:59], v[176:177]
	v_pk_mul_f32 v[54:55], v[54:55], v[180:181]
	v_pk_mul_f32 v[64:65], v[64:65], v[174:175]
	v_pk_mul_f32 v[60:61], v[60:61], v[178:179]
	v_pk_mul_f32 v[56:57], v[56:57], v[182:183]
	v_pk_mul_f32 v[52:53], v[52:53], v[188:189]
	v_pk_mul_f32 v[50:51], v[50:51], v[186:187]
	v_pk_mul_f32 v[78:79], v[78:79], v[172:173]
	v_pk_mul_f32 v[74:75], v[74:75], v[176:177]
	v_pk_mul_f32 v[70:71], v[70:71], v[180:181]
	v_pk_mul_f32 v[80:81], v[80:81], v[174:175]
	v_pk_mul_f32 v[76:77], v[76:77], v[178:179]
	v_pk_mul_f32 v[72:73], v[72:73], v[182:183]
	v_pk_mul_f32 v[68:69], v[68:69], v[188:189]
	v_pk_mul_f32 v[66:67], v[66:67], v[186:187]

; __device__ __forceinline__ float softmax_shift(f32x16& p0, f32x16& p1, f32x16& negm, float pmax, bool first) {
;   asm volatile("s_nop 4" ::: "memory");
;   { auto rr = __builtin_amdgcn_permlane32_swap(__float_as_uint(pmax), __float_as_uint(pmax), false, false);
;     pmax = fmaxf(__uint_as_float(rr[0]), __uint_as_float(rr[1])); }
;   const float delta = first ? pmax : fmaxf(pmax, 0.f);
; #pragma unroll
;   for (int r = 0; r < 16; ++r) { p0[r] -= delta; p1[r] -= delta; negm[r] -= delta; }
;   return first ? 1.f : __builtin_amdgcn_exp2f(-delta);
; }
.LBB0_324:
	v_mov_b32_e32 v115, v114
	s_nop 1
	v_permlane32_swap_b32_e32 v114, v115
	v_max3_f32 v114, v114, v115, 0
	v_exp_f32_e64 v115, -v114
	s_nop 4
	s_nop 0
	v_cmp_gt_f32_e32 vcc, 1.0, v115
	s_cbranch_vccz .LBB0_328
	v_mul_f32_dpp v240, v115, v240 quad_perm:[0,0,0,0] row_mask:0xf bank_mask:0xf
	v_mul_f32_dpp v241, v115, v241 quad_perm:[1,1,1,1] row_mask:0xf bank_mask:0xf
	v_mul_f32_dpp v242, v115, v242 quad_perm:[2,2,2,2] row_mask:0xf bank_mask:0xf
	v_mul_f32_dpp v243, v115, v243 quad_perm:[3,3,3,3] row_mask:0xf bank_mask:0xf
	v_mul_f32_dpp v244, v115, v244 quad_perm:[0,0,0,0] row_mask:0xf bank_mask:0xf
	v_mul_f32_dpp v245, v115, v245 quad_perm:[1,1,1,1] row_mask:0xf bank_mask:0xf
	v_mul_f32_dpp v246, v115, v246 quad_perm:[2,2,2,2] row_mask:0xf bank_mask:0xf
	v_mul_f32_dpp v247, v115, v247 quad_perm:[3,3,3,3] row_mask:0xf bank_mask:0xf
	s_and_saveexec_b64 s[14:15], s[4:5]
	ds_write_b32 v165, v115
	s_or_b64 exec, exec, s[14:15]
	s_waitcnt lgkmcnt(0)
	v_add_u32_e32 v115, s6, v184
	ds_read_b128 v[116:119], v115 offset:96
	ds_read_b128 v[120:123], v115 offset:64
	ds_read_b128 v[124:127], v115 offset:32
	ds_read_b128 v[136:139], v115
	s_waitcnt lgkmcnt(3)
	v_pk_mul_f32 v[30:31], v[30:31], v[116:117]
	s_waitcnt lgkmcnt(2)
	v_pk_mul_f32 v[26:27], v[26:27], v[120:121]
	s_waitcnt lgkmcnt(1)
	v_pk_mul_f32 v[22:23], v[22:23], v[124:125]
	v_pk_mul_f32 v[32:33], v[32:33], v[118:119]
	v_pk_mul_f32 v[28:29], v[28:29], v[122:123]
	v_pk_mul_f32 v[24:25], v[24:25], v[126:127]
	s_waitcnt lgkmcnt(0)
	v_pk_mul_f32 v[20:21], v[20:21], v[138:139]
	v_pk_mul_f32 v[18:19], v[18:19], v[136:137]
	v_pk_mul_f32 v[46:47], v[46:47], v[116:117]
	v_pk_mul_f32 v[42:43], v[42:43], v[120:121]
	v_pk_mul_f32 v[38:39], v[38:39], v[124:125]
	v_pk_mul_f32 v[48:49], v[48:49], v[118:119]
	v_pk_mul_f32 v[44:45], v[44:45], v[122:123]
	v_pk_mul_f32 v[40:41], v[40:41], v[126:127]
	v_pk_mul_f32 v[36:37], v[36:37], v[138:139]
	v_pk_mul_f32 v[34:35], v[34:35], v[136:137]
	v_pk_mul_f32 v[62:63], v[62:63], v[116:117]
	v_pk_mul_f32 v[58:59], v[58:59], v[120:121]
	v_pk_mul_f32 v[54:55], v[54:55], v[124:125]
	v_pk_mul_f32 v[64:65], v[64:65], v[118:119]
	v_pk_mul_f32 v[60:61], v[60:61], v[122:123]
	v_pk_mul_f32 v[56:57], v[56:57], v[126:127]
	v_pk_mul_f32 v[52:53], v[52:53], v[138:139]
	v_pk_mul_f32 v[50:51], v[50:51], v[136:137]
	v_pk_mul_f32 v[78:79], v[78:79], v[116:117]
	v_pk_mul_f32 v[74:75], v[74:75], v[120:121]
	v_pk_mul_f32 v[70:71], v[70:71], v[124:125]
	v_pk_mul_f32 v[80:81], v[80:81], v[118:119]
	v_pk_mul_f32 v[76:77], v[76:77], v[122:123]
	v_pk_mul_f32 v[72:73], v[72:73], v[126:127]
	v_pk_mul_f32 v[68:69], v[68:69], v[138:139]
	v_pk_mul_f32 v[66:67], v[66:67], v[136:137]

; __device__ __forceinline__ float softmax_shift(f32x16& p0, f32x16& p1, f32x16& negm, float pmax, bool first) {
;   asm volatile("s_nop 4" ::: "memory");
;   { auto rr = __builtin_amdgcn_permlane32_swap(__float_as_uint(pmax), __float_as_uint(pmax), false, false);
;     pmax = fmaxf(__uint_as_float(rr[0]), __uint_as_float(rr[1])); }
;   const float delta = first ? pmax : fmaxf(pmax, 0.f);
; #pragma unroll
;   for (int r = 0; r < 16; ++r) { p0[r] -= delta; p1[r] -= delta; negm[r] -= delta; }
;   return first ? 1.f : __builtin_amdgcn_exp2f(-delta);
; }
.LBB0_329:
	v_mov_b32_e32 v172, v171
	s_nop 1
	v_permlane32_swap_b32_e32 v171, v172
	v_max3_f32 v171, v171, v172, 0
	v_exp_f32_e64 v172, -v171
	s_nop 4
	s_nop 0
	v_cmp_gt_f32_e32 vcc, 1.0, v172
	s_cbranch_vccz .LBB0_333
	v_mul_f32_dpp v240, v172, v240 quad_perm:[0,0,0,0] row_mask:0xf bank_mask:0xf
	v_mul_f32_dpp v241, v172, v241 quad_perm:[1,1,1,1] row_mask:0xf bank_mask:0xf
	v_mul_f32_dpp v242, v172, v242 quad_perm:[2,2,2,2] row_mask:0xf bank_mask:0xf
	v_mul_f32_dpp v243, v172, v243 quad_perm:[3,3,3,3] row_mask:0xf bank_mask:0xf
	v_mul_f32_dpp v244, v172, v244 quad_perm:[0,0,0,0] row_mask:0xf bank_mask:0xf
	v_mul_f32_dpp v245, v172, v245 quad_perm:[1,1,1,1] row_mask:0xf bank_mask:0xf
	v_mul_f32_dpp v246, v172, v246 quad_perm:[2,2,2,2] row_mask:0xf bank_mask:0xf
	v_mul_f32_dpp v247, v172, v247 quad_perm:[3,3,3,3] row_mask:0xf bank_mask:0xf
	s_and_saveexec_b64 s[8:9], s[4:5]
	ds_write_b32 v166, v172
	s_or_b64 exec, exec, s[8:9]
	s_waitcnt lgkmcnt(0)
	v_add_u32_e32 v186, s6, v184
	ds_read_b128 v[172:175], v186 offset:96
	ds_read_b128 v[176:179], v186 offset:64
	ds_read_b128 v[180:183], v186 offset:32
	ds_read_b128 v[186:189], v186
	s_waitcnt lgkmcnt(3)
	v_pk_mul_f32 v[78:79], v[78:79], v[172:173]
	s_waitcnt lgkmcnt(2)
	v_pk_mul_f32 v[74:75], v[74:75], v[176:177]
	s_waitcnt lgkmcnt(1)
	v_pk_mul_f32 v[70:71], v[70:71], v[180:181]
	v_pk_mul_f32 v[80:81], v[80:81], v[174:175]
	v_pk_mul_f32 v[76:77], v[76:77], v[178:179]
	v_pk_mul_f32 v[72:73], v[72:73], v[182:183]
	s_waitcnt lgkmcnt(0)
	v_pk_mul_f32 v[68:69], v[68:69], v[188:189]
	v_pk_mul_f32 v[66:67], v[66:67], v[186:187]
	v_pk_mul_f32 v[62:63], v[62:63], v[172:173]
	v_pk_mul_f32 v[58:59], v[58:59], v[176:177]
	v_pk_mul_f32 v[54:55], v[54:55], v[180:181]
	v_pk_mul_f32 v[64:65], v[64:65], v[174:175]
	v_pk_mul_f32 v[60:61], v[60:61], v[178:179]
	v_pk_mul_f32 v[56:57], v[56:57], v[182:183]
	v_pk_mul_f32 v[52:53], v[52:53], v[188:189]
	v_pk_mul_f32 v[50:51], v[50:51], v[186:187]
	v_pk_mul_f32 v[46:47], v[46:47], v[172:173]
	v_pk_mul_f32 v[42:43], v[42:43], v[176:177]
	v_pk_mul_f32 v[38:39], v[38:39], v[180:181]
	v_pk_mul_f32 v[48:49], v[48:49], v[174:175]
	v_pk_mul_f32 v[44:45], v[44:45], v[178:179]
	v_pk_mul_f32 v[40:41], v[40:41], v[182:183]
	v_pk_mul_f32 v[36:37], v[36:37], v[188:189]
	v_pk_mul_f32 v[34:35], v[34:35], v[186:187]
	v_pk_mul_f32 v[14:15], v[14:15], v[172:173]
	v_pk_mul_f32 v[10:11], v[10:11], v[176:177]
	v_pk_mul_f32 v[6:7], v[6:7], v[180:181]
	v_pk_mul_f32 v[16:17], v[16:17], v[174:175]
	v_pk_mul_f32 v[12:13], v[12:13], v[178:179]
	v_pk_mul_f32 v[8:9], v[8:9], v[182:183]
	v_pk_mul_f32 v[4:5], v[4:5], v[188:189]
	v_pk_mul_f32 v[2:3], v[2:3], v[186:187]

; __device__ __forceinline__ float softmax_shift(f32x16& p0, f32x16& p1, f32x16& negm, float pmax, bool first) {
;   asm volatile("s_nop 4" ::: "memory");
;   { auto rr = __builtin_amdgcn_permlane32_swap(__float_as_uint(pmax), __float_as_uint(pmax), false, false);
;     pmax = fmaxf(__uint_as_float(rr[0]), __uint_as_float(rr[1])); }
;   const float delta = first ? pmax : fmaxf(pmax, 0.f);
; #pragma unroll
;   for (int r = 0; r < 16; ++r) { p0[r] -= delta; p1[r] -= delta; negm[r] -= delta; }
;   return first ? 1.f : __builtin_amdgcn_exp2f(-delta);
; }
.LBB0_334:
	v_mov_b32_e32 v115, v114
	s_nop 1
	v_permlane32_swap_b32_e32 v114, v115
	v_max3_f32 v114, v114, v115, 0
	v_exp_f32_e64 v115, -v114
	s_nop 4
	s_nop 0
	v_cmp_gt_f32_e32 vcc, 1.0, v115
	s_cbranch_vccz .LBB0_338
	v_mul_f32_dpp v240, v115, v240 quad_perm:[0,0,0,0] row_mask:0xf bank_mask:0xf
	v_mul_f32_dpp v241, v115, v241 quad_perm:[1,1,1,1] row_mask:0xf bank_mask:0xf
	v_mul_f32_dpp v242, v115, v242 quad_perm:[2,2,2,2] row_mask:0xf bank_mask:0xf
	v_mul_f32_dpp v243, v115, v243 quad_perm:[3,3,3,3] row_mask:0xf bank_mask:0xf
	v_mul_f32_dpp v244, v115, v244 quad_perm:[0,0,0,0] row_mask:0xf bank_mask:0xf
	v_mul_f32_dpp v245, v115, v245 quad_perm:[1,1,1,1] row_mask:0xf bank_mask:0xf
	v_mul_f32_dpp v246, v115, v246 quad_perm:[2,2,2,2] row_mask:0xf bank_mask:0xf
	v_mul_f32_dpp v247, v115, v247 quad_perm:[3,3,3,3] row_mask:0xf bank_mask:0xf
	s_and_saveexec_b64 s[8:9], s[4:5]
	ds_write_b32 v166, v115
	s_or_b64 exec, exec, s[8:9]
	s_waitcnt lgkmcnt(0)
	v_add_u32_e32 v115, s6, v184
	ds_read_b128 v[116:119], v115 offset:96
	ds_read_b128 v[120:123], v115 offset:64
	ds_read_b128 v[124:127], v115 offset:32
	ds_read_b128 v[136:139], v115
	s_waitcnt lgkmcnt(3)
	v_pk_mul_f32 v[78:79], v[78:79], v[116:117]
	s_waitcnt lgkmcnt(2)
	v_pk_mul_f32 v[74:75], v[74:75], v[120:121]
	s_waitcnt lgkmcnt(1)
	v_pk_mul_f32 v[70:71], v[70:71], v[124:125]
	v_pk_mul_f32 v[80:81], v[80:81], v[118:119]
	v_pk_mul_f32 v[76:77], v[76:77], v[122:123]
	v_pk_mul_f32 v[72:73], v[72:73], v[126:127]
	s_waitcnt lgkmcnt(0)
	v_pk_mul_f32 v[68:69], v[68:69], v[138:139]
	v_pk_mul_f32 v[66:67], v[66:67], v[136:137]
	v_pk_mul_f32 v[62:63], v[62:63], v[116:117]
	v_pk_mul_f32 v[58:59], v[58:59], v[120:121]
	v_pk_mul_f32 v[54:55], v[54:55], v[124:125]
	v_pk_mul_f32 v[64:65], v[64:65], v[118:119]
	v_pk_mul_f32 v[60:61], v[60:61], v[122:123]
	v_pk_mul_f32 v[56:57], v[56:57], v[126:127]
	v_pk_mul_f32 v[52:53], v[52:53], v[138:139]
	v_pk_mul_f32 v[50:51], v[50:51], v[136:137]
	v_pk_mul_f32 v[46:47], v[46:47], v[116:117]
	v_pk_mul_f32 v[42:43], v[42:43], v[120:121]
	v_pk_mul_f32 v[38:39], v[38:39], v[124:125]
	v_pk_mul_f32 v[48:49], v[48:49], v[118:119]
	v_pk_mul_f32 v[44:45], v[44:45], v[122:123]
	v_pk_mul_f32 v[40:41], v[40:41], v[126:127]
	v_pk_mul_f32 v[36:37], v[36:37], v[138:139]
	v_pk_mul_f32 v[34:35], v[34:35], v[136:137]
	v_pk_mul_f32 v[14:15], v[14:15], v[116:117]
	v_pk_mul_f32 v[10:11], v[10:11], v[120:121]
	v_pk_mul_f32 v[6:7], v[6:7], v[124:125]
	v_pk_mul_f32 v[16:17], v[16:17], v[118:119]
	v_pk_mul_f32 v[12:13], v[12:13], v[122:123]
	v_pk_mul_f32 v[8:9], v[8:9], v[126:127]
	v_pk_mul_f32 v[4:5], v[4:5], v[138:139]
	v_pk_mul_f32 v[2:3], v[2:3], v[136:137]

; __global__ void __launch_bounds__(NWAVES * 64, 2) fwd_kernel(Args args) {
;     extern __shared__ __attribute__((aligned(16))) unsigned char lds[];
;     Frame F;
;     F.lds = lds; F.tid = threadIdx.x; F.lane = F.tid & 63; F.wave = __builtin_amdgcn_readfirstlane(F.tid >> 6);
	.amdhsa_kernel _Z10fwd_kernel4Args
		.amdhsa_group_segment_fixed_size 0
		.amdhsa_private_segment_fixed_size 0
		.amdhsa_kernarg_size 464
		.amdhsa_user_sgpr_count 2
		.amdhsa_user_sgpr_dispatch_ptr 0
		.amdhsa_user_sgpr_queue_ptr 0
		.amdhsa_user_sgpr_kernarg_segment_ptr 1
		.amdhsa_user_sgpr_dispatch_id 0
		.amdhsa_user_sgpr_kernarg_preload_length 0
		.amdhsa_user_sgpr_kernarg_preload_offset 0
		.amdhsa_user_sgpr_private_segment_size 0
		.amdhsa_uses_dynamic_stack 0
		.amdhsa_enable_private_segment 0
		.amdhsa_system_sgpr_workgroup_id_x 1
		.amdhsa_system_sgpr_workgroup_id_y 0
		.amdhsa_system_sgpr_workgroup_id_z 0
		.amdhsa_system_sgpr_workgroup_info 0
		.amdhsa_system_vgpr_workitem_id 0
		.amdhsa_next_free_vgpr 251
		.amdhsa_next_free_sgpr 100
		.amdhsa_accum_offset 252
		.amdhsa_reserve_vcc 1
		.amdhsa_float_round_mode_32 0
		.amdhsa_float_round_mode_16_64 0
		.amdhsa_float_denorm_mode_32 3
		.amdhsa_float_denorm_mode_16_64 3
		.amdhsa_dx10_clamp 1
		.amdhsa_ieee_mode 1
		.amdhsa_fp16_overflow 0
		.amdhsa_tg_split 0
		.amdhsa_exception_fp_ieee_invalid_op 0
		.amdhsa_exception_fp_denorm_src 0
		.amdhsa_exception_fp_ieee_div_zero 0
		.amdhsa_exception_fp_ieee_overflow 0
		.amdhsa_exception_fp_ieee_underflow 0
		.amdhsa_exception_fp_ieee_inexact 0
		.amdhsa_exception_int_div_zero 0
	.end_amdhsa_kernel

; __global__ void __launch_bounds__(NWAVES * 64, 2) fwd_kernel(Args args) {
;     extern __shared__ __attribute__((aligned(16))) unsigned char lds[];
;     Frame F;
;     F.lds = lds; F.tid = threadIdx.x; F.lane = F.tid & 63; F.wave = __builtin_amdgcn_readfirstlane(F.tid >> 6);
amdhsa.kernels:
  - .agpr_count:     0
    .args:
      - .offset:         0
        .size:           208
        .value_kind:     by_value
      - .offset:         208
        .size:           4
        .value_kind:     hidden_block_count_x
      - .offset:         212
        .size:           4
        .value_kind:     hidden_block_count_y
      - .offset:         216
        .size:           4
        .value_kind:     hidden_block_count_z
      - .offset:         220
        .size:           2
        .value_kind:     hidden_group_size_x
      - .offset:         222
        .size:           2
        .value_kind:     hidden_group_size_y
      - .offset:         224
        .size:           2
        .value_kind:     hidden_group_size_z
      - .offset:         226
        .size:           2
        .value_kind:     hidden_remainder_x
      - .offset:         228
        .size:           2
        .value_kind:     hidden_remainder_y
      - .offset:         230
        .size:           2
        .value_kind:     hidden_remainder_z
      - .offset:         248
        .size:           8
        .value_kind:     hidden_global_offset_x
      - .offset:         256
        .size:           8
        .value_kind:     hidden_global_offset_y
      - .offset:         264
        .size:           8
        .value_kind:     hidden_global_offset_z
      - .offset:         272
        .size:           2
        .value_kind:     hidden_grid_dims
      - .offset:         328
        .size:           4
        .value_kind:     hidden_dynamic_lds_size
    .group_segment_fixed_size: 0
    .kernarg_segment_align: 8
    .kernarg_segment_size: 464
    .language:       OpenCL C
    .language_version:
      - 2
      - 0
    .max_flat_workgroup_size: 512
    .name:           _Z10fwd_kernel4Args
    .private_segment_fixed_size: 0
    .sgpr_count:     106
    .sgpr_spill_count: 4
    .symbol:         _Z10fwd_kernel4Args.kd
    .uniform_work_group_size: 1
    .uses_dynamic_stack: false
    .vgpr_count:     251
    .vgpr_spill_count: 0
    .wavefront_size: 64
